# baseline (speedup 1.0000x reference)
_Z12k1_colsum_q8PKfPjPfS2_:
	s_load_dwordx8 s[4:11], s[0:1], 0x0
	v_and_b32_e32 v1, 63, v0
	v_lshrrev_b32_e32 v41, 6, v0
	s_mul_i32 s12, s2, 0xc35
	s_lshr_b32 s12, s12, 4
	v_readfirstlane_b32 s14, v41
	s_add_i32 s13, s2, 1
	s_mul_i32 s13, s13, 0xc35
	s_lshr_b32 s13, s13, 4
	s_sub_u32 s13, s13, s12
	s_sub_u32 s15, s13, 0xc0
	s_cmp_lt_u32 s14, s15
	s_cselect_b32 s29, 1, 0
	v_lshlrev_b32_e32 v34, 4, v1
	v_min_u32_e32 v35, 57, v1
	v_lshlrev_b32_e32 v35, 4, v35
	v_cmp_gt_u32_e64 s[18:19], 58, v1
	s_lshl_b32 s35, s14, 13
	s_add_u32 s36, s35, 0x1000
	v_add_u32_e32 v38, s35, v34
	v_lshrrev_b32_e32 v41, 5, v1
	v_mov_b32_e32 v42, 0xc35000
	v_mul_lo_u32 v39, v41, v42
	v_and_b32_e32 v42, 31, v1
	v_lshl_add_u32 v39, v42, 2, v39
	v_mov_b32_e32 v2, 0
	v_mov_b32_e32 v3, 0
	v_mov_b32_e32 v4, 0
	v_mov_b32_e32 v5, 0
	v_mov_b32_e32 v6, 0
	v_mov_b32_e32 v7, 0
	v_mov_b32_e32 v8, 0
	v_mov_b32_e32 v9, 0
	v_mov_b32_e32 v10, 0
	v_mov_b32_e32 v11, 0
	v_mov_b32_e32 v12, 0
	v_mov_b32_e32 v13, 0
	v_mov_b32_e32 v14, 0
	v_mov_b32_e32 v15, 0
	v_mov_b32_e32 v16, 0
	v_mov_b32_e32 v17, 0
	v_mov_b32_e32 v40, 0
	v_mov_b32_e32 v47, 0x42fe0000
	s_mov_b32 s32, 0x42fe0000
	s_mov_b32 s33, 0xc0c0400
	s_mov_b32 s34, 0x4000c0c
	s_add_u32 s15, s12, s14
	s_mul_i32 s37, s15, 0xfa0
	s_lshl_b32 s15, s15, 7
	s_waitcnt lgkmcnt(0)
	s_add_u32 s16, s4, s37
	s_addc_u32 s17, s5, 0
	s_add_u32 s40, s6, s15
	s_addc_u32 s41, s7, 0
	s_add_u32 s20, s40, 0x4800
	s_addc_u32 s21, s41, 0
	s_add_u32 s22, s20, 0x186a000
	s_addc_u32 s23, s21, 0
	s_add_u32 s24, s22, 0x186a000
	s_addc_u32 s25, s23, 0
	s_add_u32 s26, s24, 0x186a000
	s_addc_u32 s27, s25, 0
	s_mov_b32 m0, s35
	s_nop 0
	global_load_lds_dwordx4 v34, s[16:17] nt
	global_load_lds_dwordx4 v34, s[16:17] offset:1024 nt
	global_load_lds_dwordx4 v34, s[16:17] offset:2048 nt
	global_load_lds_dwordx4 v35, s[16:17] offset:3072 nt
	s_add_u32 s16, s16, 0x7d00
	s_addc_u32 s17, s17, 0
	s_mov_b32 m0, s36
	s_nop 0
	global_load_lds_dwordx4 v34, s[16:17] nt
	global_load_lds_dwordx4 v34, s[16:17] offset:1024 nt
	global_load_lds_dwordx4 v34, s[16:17] offset:2048 nt
	global_load_lds_dwordx4 v35, s[16:17] offset:3072 nt
	s_add_u32 s16, s16, 0x7d00
	s_addc_u32 s17, s17, 0
	s_waitcnt vmcnt(4)
	ds_read_b128 v[18:21], v38 offset:0
	ds_read_b128 v[22:25], v38 offset:1024
	ds_read_b128 v[26:29], v38 offset:2048
	ds_read_b128 v[30:33], v38 offset:3072
	s_waitcnt lgkmcnt(0)
	s_mov_b32 m0, s35
	s_nop 0
	global_load_lds_dwordx4 v34, s[16:17] nt
	global_load_lds_dwordx4 v34, s[16:17] offset:1024 nt
	global_load_lds_dwordx4 v34, s[16:17] offset:2048 nt
	global_load_lds_dwordx4 v35, s[16:17] offset:3072 nt
	s_add_u32 s16, s16, 0x7d00
	s_addc_u32 s17, s17, 0
	v_cndmask_b32_e64 v30, 0, v30, s[18:19]
	v_cndmask_b32_e64 v31, 0, v31, s[18:19]
	v_cndmask_b32_e64 v32, 0, v32, s[18:19]
	v_cndmask_b32_e64 v33, 0, v33, s[18:19]
	v_max3_f32 v41, |v18|, |v19|, |v20|
	v_max3_f32 v42, |v21|, |v22|, |v23|
	v_max3_f32 v43, |v24|, |v25|, |v26|
	v_max3_f32 v44, |v27|, |v28|, |v29|
	v_max3_f32 v45, |v30|, |v31|, |v32|
	v_max3_f32 v41, v41, v42, |v33|
	v_max3_f32 v43, v43, v44, v45
	v_max_f32_e32 v41, v41, v43
	v_pk_add_f32 v[2:3], v[2:3], v[18:19]
	v_pk_add_f32 v[4:5], v[4:5], v[20:21]
	v_max_f32_dpp v41, v41, v41 quad_perm:[1,0,3,2] row_mask:0xf bank_mask:0xf
	v_pk_add_f32 v[6:7], v[6:7], v[22:23]
	v_pk_add_f32 v[8:9], v[8:9], v[24:25]
	v_max_f32_dpp v41, v41, v41 quad_perm:[2,3,0,1] row_mask:0xf bank_mask:0xf
	v_pk_add_f32 v[10:11], v[10:11], v[26:27]
	v_pk_add_f32 v[12:13], v[12:13], v[28:29]
	v_max_f32_dpp v41, v41, v41 row_half_mirror row_mask:0xf bank_mask:0xf
	v_pk_add_f32 v[14:15], v[14:15], v[30:31]
	v_pk_add_f32 v[16:17], v[16:17], v[32:33]
	v_max_f32_dpp v41, v41, v41 row_mirror row_mask:0xf bank_mask:0xf
	s_nop 1
	v_max_f32_dpp v41, v41, v41 row_bcast:15 row_mask:0xa bank_mask:0xf
	s_nop 1
	v_max_f32_dpp v41, v41, v41 row_bcast:31 row_mask:0xc bank_mask:0xf
	s_nop 1
	v_readlane_b32 s28, v41, 63
	s_nop 1
	v_div_scale_f32 v48, s[30:31], s28, s28, v47
	v_rcp_f32_e32 v49, v48
	s_nop 0
	v_fma_f32 v50, -v48, v49, 1.0
	v_fmac_f32_e32 v49, v50, v49
	v_mov_b32_e32 v50, s28
	v_div_scale_f32 v50, vcc, s32, v50, s32
	v_mul_f32_e32 v51, v50, v49
	v_fma_f32 v52, -v48, v51, v50
	v_fmac_f32_e32 v51, v52, v49
	v_fma_f32 v48, -v48, v51, v50
	v_div_fmas_f32 v48, v48, v49, v51
	v_div_fixup_f32 v48, v48, s28, v47
	v_cmp_gt_f32_e64 vcc, s28, 0
	v_writelane_b32 v40, s28, 0
	s_nop 0
	v_cndmask_b32_e32 v48, 0, v48, vcc
	v_fmaak_f32 v49, v18, v48, 0x4b400000
	v_fmaak_f32 v50, v19, v48, 0x4b400000
	v_fmaak_f32 v51, v20, v48, 0x4b400000
	v_fmaak_f32 v52, v21, v48, 0x4b400000
	v_perm_b32 v49, v50, v49, s33
	v_perm_b32 v51, v52, v51, s34
	v_or_b32_e32 v56, v49, v51
	v_fmaak_f32 v53, v22, v48, 0x4b400000
	v_fmaak_f32 v54, v23, v48, 0x4b400000
	v_fmaak_f32 v55, v24, v48, 0x4b400000
	v_fmaak_f32 v46, v25, v48, 0x4b400000
	v_perm_b32 v53, v54, v53, s33
	v_perm_b32 v55, v46, v55, s34
	v_or_b32_e32 v57, v53, v55
	v_fmaak_f32 v49, v26, v48, 0x4b400000
	v_fmaak_f32 v50, v27, v48, 0x4b400000
	v_fmaak_f32 v51, v28, v48, 0x4b400000
	v_fmaak_f32 v52, v29, v48, 0x4b400000
	v_perm_b32 v49, v50, v49, s33
	v_perm_b32 v51, v52, v51, s34
	v_or_b32_e32 v58, v49, v51
	v_fmaak_f32 v53, v30, v48, 0x4b400000
	v_fmaak_f32 v54, v31, v48, 0x4b400000
	v_fmaak_f32 v55, v32, v48, 0x4b400000
	v_fmaak_f32 v46, v33, v48, 0x4b400000
	v_perm_b32 v53, v54, v53, s33
	v_perm_b32 v55, v46, v55, s34
	v_or_b32_e32 v59, v53, v55
	s_waitcnt vmcnt(4)
	ds_read_b128 v[18:21], v38 offset:4096
	ds_read_b128 v[22:25], v38 offset:5120
	ds_read_b128 v[26:29], v38 offset:6144
	ds_read_b128 v[30:33], v38 offset:7168
	s_waitcnt lgkmcnt(0)
	s_mov_b32 m0, s36
	s_nop 0
	global_load_lds_dwordx4 v34, s[16:17] nt
	global_load_lds_dwordx4 v34, s[16:17] offset:1024 nt
	global_load_lds_dwordx4 v34, s[16:17] offset:2048 nt
	global_load_lds_dwordx4 v35, s[16:17] offset:3072 nt
	s_add_u32 s16, s16, 0x7d00
	s_addc_u32 s17, s17, 0
	v_cndmask_b32_e64 v30, 0, v30, s[18:19]
	v_cndmask_b32_e64 v31, 0, v31, s[18:19]
	v_cndmask_b32_e64 v32, 0, v32, s[18:19]
	v_cndmask_b32_e64 v33, 0, v33, s[18:19]
	v_max3_f32 v41, |v18|, |v19|, |v20|
	v_max3_f32 v42, |v21|, |v22|, |v23|
	v_max3_f32 v43, |v24|, |v25|, |v26|
	v_max3_f32 v44, |v27|, |v28|, |v29|
	v_max3_f32 v45, |v30|, |v31|, |v32|
	v_max3_f32 v41, v41, v42, |v33|
	v_max3_f32 v43, v43, v44, v45
	v_max_f32_e32 v41, v41, v43
	v_pk_add_f32 v[2:3], v[2:3], v[18:19]
	v_pk_add_f32 v[4:5], v[4:5], v[20:21]
	v_max_f32_dpp v41, v41, v41 quad_perm:[1,0,3,2] row_mask:0xf bank_mask:0xf
	v_pk_add_f32 v[6:7], v[6:7], v[22:23]
	v_pk_add_f32 v[8:9], v[8:9], v[24:25]
	v_max_f32_dpp v41, v41, v41 quad_perm:[2,3,0,1] row_mask:0xf bank_mask:0xf
	v_pk_add_f32 v[10:11], v[10:11], v[26:27]
	v_pk_add_f32 v[12:13], v[12:13], v[28:29]
	v_max_f32_dpp v41, v41, v41 row_half_mirror row_mask:0xf bank_mask:0xf
	v_pk_add_f32 v[14:15], v[14:15], v[30:31]
	v_pk_add_f32 v[16:17], v[16:17], v[32:33]
	v_max_f32_dpp v41, v41, v41 row_mirror row_mask:0xf bank_mask:0xf
	s_nop 1
	v_max_f32_dpp v41, v41, v41 row_bcast:15 row_mask:0xa bank_mask:0xf
	s_nop 1
	v_max_f32_dpp v41, v41, v41 row_bcast:31 row_mask:0xc bank_mask:0xf
	s_nop 1
	v_readlane_b32 s28, v41, 63
	s_nop 1
	v_div_scale_f32 v48, s[30:31], s28, s28, v47
	v_rcp_f32_e32 v49, v48
	s_nop 0
	v_fma_f32 v50, -v48, v49, 1.0
	v_fmac_f32_e32 v49, v50, v49
	v_mov_b32_e32 v50, s28
	v_div_scale_f32 v50, vcc, s32, v50, s32
	v_mul_f32_e32 v51, v50, v49
	v_fma_f32 v52, -v48, v51, v50
	v_fmac_f32_e32 v51, v52, v49
	v_fma_f32 v48, -v48, v51, v50
	v_div_fmas_f32 v48, v48, v49, v51
	v_div_fixup_f32 v48, v48, s28, v47
	v_cmp_gt_f32_e64 vcc, s28, 0
	v_writelane_b32 v40, s28, 1
	s_nop 0
	v_cndmask_b32_e32 v48, 0, v48, vcc
	v_fmaak_f32 v49, v18, v48, 0x4b400000
	v_fmaak_f32 v50, v19, v48, 0x4b400000
	v_fmaak_f32 v51, v20, v48, 0x4b400000
	v_fmaak_f32 v52, v21, v48, 0x4b400000
	v_perm_b32 v49, v50, v49, s33
	v_perm_b32 v51, v52, v51, s34
	v_or_b32_e32 v60, v49, v51
	v_fmaak_f32 v53, v22, v48, 0x4b400000
	v_fmaak_f32 v54, v23, v48, 0x4b400000
	v_fmaak_f32 v55, v24, v48, 0x4b400000
	v_fmaak_f32 v46, v25, v48, 0x4b400000
	v_perm_b32 v53, v54, v53, s33
	v_perm_b32 v55, v46, v55, s34
	v_or_b32_e32 v61, v53, v55
	v_fmaak_f32 v49, v26, v48, 0x4b400000
	v_fmaak_f32 v50, v27, v48, 0x4b400000
	v_fmaak_f32 v51, v28, v48, 0x4b400000
	v_fmaak_f32 v52, v29, v48, 0x4b400000
	v_perm_b32 v49, v50, v49, s33
	v_perm_b32 v51, v52, v51, s34
	v_or_b32_e32 v62, v49, v51
	v_fmaak_f32 v53, v30, v48, 0x4b400000
	v_fmaak_f32 v54, v31, v48, 0x4b400000
	v_fmaak_f32 v55, v32, v48, 0x4b400000
	v_fmaak_f32 v46, v33, v48, 0x4b400000
	v_perm_b32 v53, v54, v53, s33
	v_perm_b32 v55, v46, v55, s34
	v_or_b32_e32 v63, v53, v55
	s_waitcnt vmcnt(4)
	ds_read_b128 v[18:21], v38 offset:0
	ds_read_b128 v[22:25], v38 offset:1024
	ds_read_b128 v[26:29], v38 offset:2048
	ds_read_b128 v[30:33], v38 offset:3072
	s_waitcnt lgkmcnt(0)
	s_mov_b32 m0, s35
	s_nop 0
	global_load_lds_dwordx4 v34, s[16:17] nt
	global_load_lds_dwordx4 v34, s[16:17] offset:1024 nt
	global_load_lds_dwordx4 v34, s[16:17] offset:2048 nt
	global_load_lds_dwordx4 v35, s[16:17] offset:3072 nt
	s_add_u32 s16, s16, 0x7d00
	s_addc_u32 s17, s17, 0
	v_cndmask_b32_e64 v30, 0, v30, s[18:19]
	v_cndmask_b32_e64 v31, 0, v31, s[18:19]
	v_cndmask_b32_e64 v32, 0, v32, s[18:19]
	v_cndmask_b32_e64 v33, 0, v33, s[18:19]
	v_max3_f32 v41, |v18|, |v19|, |v20|
	v_max3_f32 v42, |v21|, |v22|, |v23|
	v_max3_f32 v43, |v24|, |v25|, |v26|
	v_max3_f32 v44, |v27|, |v28|, |v29|
	v_max3_f32 v45, |v30|, |v31|, |v32|
	v_max3_f32 v41, v41, v42, |v33|
	v_max3_f32 v43, v43, v44, v45
	v_max_f32_e32 v41, v41, v43
	v_pk_add_f32 v[2:3], v[2:3], v[18:19]
	v_pk_add_f32 v[4:5], v[4:5], v[20:21]
	v_max_f32_dpp v41, v41, v41 quad_perm:[1,0,3,2] row_mask:0xf bank_mask:0xf
	v_pk_add_f32 v[6:7], v[6:7], v[22:23]
	v_pk_add_f32 v[8:9], v[8:9], v[24:25]
	v_max_f32_dpp v41, v41, v41 quad_perm:[2,3,0,1] row_mask:0xf bank_mask:0xf
	v_pk_add_f32 v[10:11], v[10:11], v[26:27]
	v_pk_add_f32 v[12:13], v[12:13], v[28:29]
	v_max_f32_dpp v41, v41, v41 row_half_mirror row_mask:0xf bank_mask:0xf
	v_pk_add_f32 v[14:15], v[14:15], v[30:31]
	v_pk_add_f32 v[16:17], v[16:17], v[32:33]
	v_max_f32_dpp v41, v41, v41 row_mirror row_mask:0xf bank_mask:0xf
	s_nop 1
	v_max_f32_dpp v41, v41, v41 row_bcast:15 row_mask:0xa bank_mask:0xf
	s_nop 1
	v_max_f32_dpp v41, v41, v41 row_bcast:31 row_mask:0xc bank_mask:0xf
	s_nop 1
	v_readlane_b32 s28, v41, 63
	s_nop 1
	v_div_scale_f32 v48, s[30:31], s28, s28, v47
	v_rcp_f32_e32 v49, v48
	s_nop 0
	v_fma_f32 v50, -v48, v49, 1.0
	v_fmac_f32_e32 v49, v50, v49
	v_mov_b32_e32 v50, s28
	v_div_scale_f32 v50, vcc, s32, v50, s32
	v_mul_f32_e32 v51, v50, v49
	v_fma_f32 v52, -v48, v51, v50
	v_fmac_f32_e32 v51, v52, v49
	v_fma_f32 v48, -v48, v51, v50
	v_div_fmas_f32 v48, v48, v49, v51
	v_div_fixup_f32 v48, v48, s28, v47
	v_cmp_gt_f32_e64 vcc, s28, 0
	v_writelane_b32 v40, s28, 2
	s_nop 0
	v_cndmask_b32_e32 v48, 0, v48, vcc
	v_fmaak_f32 v49, v18, v48, 0x4b400000
	v_fmaak_f32 v50, v19, v48, 0x4b400000
	v_fmaak_f32 v51, v20, v48, 0x4b400000
	v_fmaak_f32 v52, v21, v48, 0x4b400000
	v_perm_b32 v49, v50, v49, s33
	v_perm_b32 v51, v52, v51, s34
	v_or_b32_e32 v64, v49, v51
	v_fmaak_f32 v53, v22, v48, 0x4b400000
	v_fmaak_f32 v54, v23, v48, 0x4b400000
	v_fmaak_f32 v55, v24, v48, 0x4b400000
	v_fmaak_f32 v46, v25, v48, 0x4b400000
	v_perm_b32 v53, v54, v53, s33
	v_perm_b32 v55, v46, v55, s34
	v_or_b32_e32 v65, v53, v55
	v_fmaak_f32 v49, v26, v48, 0x4b400000
	v_fmaak_f32 v50, v27, v48, 0x4b400000
	v_fmaak_f32 v51, v28, v48, 0x4b400000
	v_fmaak_f32 v52, v29, v48, 0x4b400000
	v_perm_b32 v49, v50, v49, s33
	v_perm_b32 v51, v52, v51, s34
	v_or_b32_e32 v66, v49, v51
	v_fmaak_f32 v53, v30, v48, 0x4b400000
	v_fmaak_f32 v54, v31, v48, 0x4b400000
	v_fmaak_f32 v55, v32, v48, 0x4b400000
	v_fmaak_f32 v46, v33, v48, 0x4b400000
	v_perm_b32 v53, v54, v53, s33
	v_perm_b32 v55, v46, v55, s34
	v_or_b32_e32 v67, v53, v55
	s_waitcnt vmcnt(4)
	ds_read_b128 v[18:21], v38 offset:4096
	ds_read_b128 v[22:25], v38 offset:5120
	ds_read_b128 v[26:29], v38 offset:6144
	ds_read_b128 v[30:33], v38 offset:7168
	s_waitcnt lgkmcnt(0)
	s_mov_b32 m0, s36
	s_nop 0
	global_load_lds_dwordx4 v34, s[16:17] nt
	global_load_lds_dwordx4 v34, s[16:17] offset:1024 nt
	global_load_lds_dwordx4 v34, s[16:17] offset:2048 nt
	global_load_lds_dwordx4 v35, s[16:17] offset:3072 nt
	s_add_u32 s16, s16, 0x7d00
	s_addc_u32 s17, s17, 0
	v_cndmask_b32_e64 v30, 0, v30, s[18:19]
	v_cndmask_b32_e64 v31, 0, v31, s[18:19]
	v_cndmask_b32_e64 v32, 0, v32, s[18:19]
	v_cndmask_b32_e64 v33, 0, v33, s[18:19]
	v_max3_f32 v41, |v18|, |v19|, |v20|
	v_max3_f32 v42, |v21|, |v22|, |v23|
	v_max3_f32 v43, |v24|, |v25|, |v26|
	v_max3_f32 v44, |v27|, |v28|, |v29|
	v_max3_f32 v45, |v30|, |v31|, |v32|
	v_max3_f32 v41, v41, v42, |v33|
	v_max3_f32 v43, v43, v44, v45
	v_max_f32_e32 v41, v41, v43
	v_pk_add_f32 v[2:3], v[2:3], v[18:19]
	v_pk_add_f32 v[4:5], v[4:5], v[20:21]
	v_max_f32_dpp v41, v41, v41 quad_perm:[1,0,3,2] row_mask:0xf bank_mask:0xf
	v_pk_add_f32 v[6:7], v[6:7], v[22:23]
	v_pk_add_f32 v[8:9], v[8:9], v[24:25]
	v_max_f32_dpp v41, v41, v41 quad_perm:[2,3,0,1] row_mask:0xf bank_mask:0xf
	v_pk_add_f32 v[10:11], v[10:11], v[26:27]
	v_pk_add_f32 v[12:13], v[12:13], v[28:29]
	v_max_f32_dpp v41, v41, v41 row_half_mirror row_mask:0xf bank_mask:0xf
	v_pk_add_f32 v[14:15], v[14:15], v[30:31]
	v_pk_add_f32 v[16:17], v[16:17], v[32:33]
	v_max_f32_dpp v41, v41, v41 row_mirror row_mask:0xf bank_mask:0xf
	s_nop 1
	v_max_f32_dpp v41, v41, v41 row_bcast:15 row_mask:0xa bank_mask:0xf
	s_nop 1
	v_max_f32_dpp v41, v41, v41 row_bcast:31 row_mask:0xc bank_mask:0xf
	s_nop 1
	v_readlane_b32 s28, v41, 63
	s_nop 1
	v_div_scale_f32 v48, s[30:31], s28, s28, v47
	v_rcp_f32_e32 v49, v48
	s_nop 0
	v_fma_f32 v50, -v48, v49, 1.0
	v_fmac_f32_e32 v49, v50, v49
	v_mov_b32_e32 v50, s28
	v_div_scale_f32 v50, vcc, s32, v50, s32
	v_mul_f32_e32 v51, v50, v49
	v_fma_f32 v52, -v48, v51, v50
	v_fmac_f32_e32 v51, v52, v49
	v_fma_f32 v48, -v48, v51, v50
	v_div_fmas_f32 v48, v48, v49, v51
	v_div_fixup_f32 v48, v48, s28, v47
	v_cmp_gt_f32_e64 vcc, s28, 0
	v_writelane_b32 v40, s28, 3
	s_nop 0
	v_cndmask_b32_e32 v48, 0, v48, vcc
	v_fmaak_f32 v49, v18, v48, 0x4b400000
	v_fmaak_f32 v50, v19, v48, 0x4b400000
	v_fmaak_f32 v51, v20, v48, 0x4b400000
	v_fmaak_f32 v52, v21, v48, 0x4b400000
	v_perm_b32 v49, v50, v49, s33
	v_perm_b32 v51, v52, v51, s34
	v_or_b32_e32 v68, v49, v51
	v_fmaak_f32 v53, v22, v48, 0x4b400000
	v_fmaak_f32 v54, v23, v48, 0x4b400000
	v_fmaak_f32 v55, v24, v48, 0x4b400000
	v_fmaak_f32 v46, v25, v48, 0x4b400000
	v_perm_b32 v53, v54, v53, s33
	v_perm_b32 v55, v46, v55, s34
	v_or_b32_e32 v69, v53, v55
	v_fmaak_f32 v49, v26, v48, 0x4b400000
	v_fmaak_f32 v50, v27, v48, 0x4b400000
	v_fmaak_f32 v51, v28, v48, 0x4b400000
	v_fmaak_f32 v52, v29, v48, 0x4b400000
	v_perm_b32 v49, v50, v49, s33
	v_perm_b32 v51, v52, v51, s34
	v_or_b32_e32 v70, v49, v51
	v_fmaak_f32 v53, v30, v48, 0x4b400000
	v_fmaak_f32 v54, v31, v48, 0x4b400000
	v_fmaak_f32 v55, v32, v48, 0x4b400000
	v_fmaak_f32 v46, v33, v48, 0x4b400000
	v_perm_b32 v53, v54, v53, s33
	v_perm_b32 v55, v46, v55, s34
	v_or_b32_e32 v71, v53, v55
	s_waitcnt vmcnt(4)
	ds_read_b128 v[18:21], v38 offset:0
	ds_read_b128 v[22:25], v38 offset:1024
	ds_read_b128 v[26:29], v38 offset:2048
	ds_read_b128 v[30:33], v38 offset:3072
	s_waitcnt lgkmcnt(0)
	s_mov_b32 m0, s35
	s_nop 0
	global_load_lds_dwordx4 v34, s[16:17] nt
	global_load_lds_dwordx4 v34, s[16:17] offset:1024 nt
	global_load_lds_dwordx4 v34, s[16:17] offset:2048 nt
	global_load_lds_dwordx4 v35, s[16:17] offset:3072 nt
	s_add_u32 s16, s16, 0x7d00
	s_addc_u32 s17, s17, 0
	v_cndmask_b32_e64 v30, 0, v30, s[18:19]
	v_cndmask_b32_e64 v31, 0, v31, s[18:19]
	v_cndmask_b32_e64 v32, 0, v32, s[18:19]
	v_cndmask_b32_e64 v33, 0, v33, s[18:19]
	v_max3_f32 v41, |v18|, |v19|, |v20|
	v_max3_f32 v42, |v21|, |v22|, |v23|
	v_max3_f32 v43, |v24|, |v25|, |v26|
	v_max3_f32 v44, |v27|, |v28|, |v29|
	v_max3_f32 v45, |v30|, |v31|, |v32|
	v_max3_f32 v41, v41, v42, |v33|
	v_max3_f32 v43, v43, v44, v45
	v_max_f32_e32 v41, v41, v43
	v_pk_add_f32 v[2:3], v[2:3], v[18:19]
	v_pk_add_f32 v[4:5], v[4:5], v[20:21]
	v_max_f32_dpp v41, v41, v41 quad_perm:[1,0,3,2] row_mask:0xf bank_mask:0xf
	v_pk_add_f32 v[6:7], v[6:7], v[22:23]
	v_pk_add_f32 v[8:9], v[8:9], v[24:25]
	v_max_f32_dpp v41, v41, v41 quad_perm:[2,3,0,1] row_mask:0xf bank_mask:0xf
	v_pk_add_f32 v[10:11], v[10:11], v[26:27]
	v_pk_add_f32 v[12:13], v[12:13], v[28:29]
	v_max_f32_dpp v41, v41, v41 row_half_mirror row_mask:0xf bank_mask:0xf
	v_pk_add_f32 v[14:15], v[14:15], v[30:31]
	v_pk_add_f32 v[16:17], v[16:17], v[32:33]
	v_max_f32_dpp v41, v41, v41 row_mirror row_mask:0xf bank_mask:0xf
	s_nop 1
	v_max_f32_dpp v41, v41, v41 row_bcast:15 row_mask:0xa bank_mask:0xf
	s_nop 1
	v_max_f32_dpp v41, v41, v41 row_bcast:31 row_mask:0xc bank_mask:0xf
	s_nop 1
	v_readlane_b32 s28, v41, 63
	s_nop 1
	v_div_scale_f32 v48, s[30:31], s28, s28, v47
	v_rcp_f32_e32 v49, v48
	s_nop 0
	v_fma_f32 v50, -v48, v49, 1.0
	v_fmac_f32_e32 v49, v50, v49
	v_mov_b32_e32 v50, s28
	v_div_scale_f32 v50, vcc, s32, v50, s32
	v_mul_f32_e32 v51, v50, v49
	v_fma_f32 v52, -v48, v51, v50
	v_fmac_f32_e32 v51, v52, v49
	v_fma_f32 v48, -v48, v51, v50
	v_div_fmas_f32 v48, v48, v49, v51
	v_div_fixup_f32 v48, v48, s28, v47
	v_cmp_gt_f32_e64 vcc, s28, 0
	v_writelane_b32 v40, s28, 4
	s_nop 0
	v_cndmask_b32_e32 v48, 0, v48, vcc
	v_fmaak_f32 v49, v18, v48, 0x4b400000
	v_fmaak_f32 v50, v19, v48, 0x4b400000
	v_fmaak_f32 v51, v20, v48, 0x4b400000
	v_fmaak_f32 v52, v21, v48, 0x4b400000
	v_perm_b32 v49, v50, v49, s33
	v_perm_b32 v51, v52, v51, s34
	v_or_b32_e32 v72, v49, v51
	v_fmaak_f32 v53, v22, v48, 0x4b400000
	v_fmaak_f32 v54, v23, v48, 0x4b400000
	v_fmaak_f32 v55, v24, v48, 0x4b400000
	v_fmaak_f32 v46, v25, v48, 0x4b400000
	v_perm_b32 v53, v54, v53, s33
	v_perm_b32 v55, v46, v55, s34
	v_or_b32_e32 v73, v53, v55
	v_fmaak_f32 v49, v26, v48, 0x4b400000
	v_fmaak_f32 v50, v27, v48, 0x4b400000
	v_fmaak_f32 v51, v28, v48, 0x4b400000
	v_fmaak_f32 v52, v29, v48, 0x4b400000
	v_perm_b32 v49, v50, v49, s33
	v_perm_b32 v51, v52, v51, s34
	v_or_b32_e32 v74, v49, v51
	v_fmaak_f32 v53, v30, v48, 0x4b400000
	v_fmaak_f32 v54, v31, v48, 0x4b400000
	v_fmaak_f32 v55, v32, v48, 0x4b400000
	v_fmaak_f32 v46, v33, v48, 0x4b400000
	v_perm_b32 v53, v54, v53, s33
	v_perm_b32 v55, v46, v55, s34
	v_or_b32_e32 v75, v53, v55
	s_waitcnt vmcnt(4)
	ds_read_b128 v[18:21], v38 offset:4096
	ds_read_b128 v[22:25], v38 offset:5120
	ds_read_b128 v[26:29], v38 offset:6144
	ds_read_b128 v[30:33], v38 offset:7168
	s_waitcnt lgkmcnt(0)
	s_mov_b32 m0, s36
	s_nop 0
	global_load_lds_dwordx4 v34, s[16:17] nt
	global_load_lds_dwordx4 v34, s[16:17] offset:1024 nt
	global_load_lds_dwordx4 v34, s[16:17] offset:2048 nt
	global_load_lds_dwordx4 v35, s[16:17] offset:3072 nt
	s_add_u32 s16, s16, 0x7d00
	s_addc_u32 s17, s17, 0
	v_cndmask_b32_e64 v30, 0, v30, s[18:19]
	v_cndmask_b32_e64 v31, 0, v31, s[18:19]
	v_cndmask_b32_e64 v32, 0, v32, s[18:19]
	v_cndmask_b32_e64 v33, 0, v33, s[18:19]
	v_max3_f32 v41, |v18|, |v19|, |v20|
	v_max3_f32 v42, |v21|, |v22|, |v23|
	v_max3_f32 v43, |v24|, |v25|, |v26|
	v_max3_f32 v44, |v27|, |v28|, |v29|
	v_max3_f32 v45, |v30|, |v31|, |v32|
	v_max3_f32 v41, v41, v42, |v33|
	v_max3_f32 v43, v43, v44, v45
	v_max_f32_e32 v41, v41, v43
	v_pk_add_f32 v[2:3], v[2:3], v[18:19]
	v_pk_add_f32 v[4:5], v[4:5], v[20:21]
	v_max_f32_dpp v41, v41, v41 quad_perm:[1,0,3,2] row_mask:0xf bank_mask:0xf
	v_pk_add_f32 v[6:7], v[6:7], v[22:23]
	v_pk_add_f32 v[8:9], v[8:9], v[24:25]
	v_max_f32_dpp v41, v41, v41 quad_perm:[2,3,0,1] row_mask:0xf bank_mask:0xf
	v_pk_add_f32 v[10:11], v[10:11], v[26:27]
	v_pk_add_f32 v[12:13], v[12:13], v[28:29]
	v_max_f32_dpp v41, v41, v41 row_half_mirror row_mask:0xf bank_mask:0xf
	v_pk_add_f32 v[14:15], v[14:15], v[30:31]
	v_pk_add_f32 v[16:17], v[16:17], v[32:33]
	v_max_f32_dpp v41, v41, v41 row_mirror row_mask:0xf bank_mask:0xf
	s_nop 1
	v_max_f32_dpp v41, v41, v41 row_bcast:15 row_mask:0xa bank_mask:0xf
	s_nop 1
	v_max_f32_dpp v41, v41, v41 row_bcast:31 row_mask:0xc bank_mask:0xf
	s_nop 1
	v_readlane_b32 s28, v41, 63
	s_nop 1
	v_div_scale_f32 v48, s[30:31], s28, s28, v47
	v_rcp_f32_e32 v49, v48
	s_nop 0
	v_fma_f32 v50, -v48, v49, 1.0
	v_fmac_f32_e32 v49, v50, v49
	v_mov_b32_e32 v50, s28
	v_div_scale_f32 v50, vcc, s32, v50, s32
	v_mul_f32_e32 v51, v50, v49
	v_fma_f32 v52, -v48, v51, v50
	v_fmac_f32_e32 v51, v52, v49
	v_fma_f32 v48, -v48, v51, v50
	v_div_fmas_f32 v48, v48, v49, v51
	v_div_fixup_f32 v48, v48, s28, v47
	v_cmp_gt_f32_e64 vcc, s28, 0
	v_writelane_b32 v40, s28, 5
	s_nop 0
	v_cndmask_b32_e32 v48, 0, v48, vcc
	v_fmaak_f32 v49, v18, v48, 0x4b400000
	v_fmaak_f32 v50, v19, v48, 0x4b400000
	v_fmaak_f32 v51, v20, v48, 0x4b400000
	v_fmaak_f32 v52, v21, v48, 0x4b400000
	v_perm_b32 v49, v50, v49, s33
	v_perm_b32 v51, v52, v51, s34
	v_or_b32_e32 v76, v49, v51
	v_fmaak_f32 v53, v22, v48, 0x4b400000
	v_fmaak_f32 v54, v23, v48, 0x4b400000
	v_fmaak_f32 v55, v24, v48, 0x4b400000
	v_fmaak_f32 v46, v25, v48, 0x4b400000
	v_perm_b32 v53, v54, v53, s33
	v_perm_b32 v55, v46, v55, s34
	v_or_b32_e32 v77, v53, v55
	v_fmaak_f32 v49, v26, v48, 0x4b400000
	v_fmaak_f32 v50, v27, v48, 0x4b400000
	v_fmaak_f32 v51, v28, v48, 0x4b400000
	v_fmaak_f32 v52, v29, v48, 0x4b400000
	v_perm_b32 v49, v50, v49, s33
	v_perm_b32 v51, v52, v51, s34
	v_or_b32_e32 v78, v49, v51
	v_fmaak_f32 v53, v30, v48, 0x4b400000
	v_fmaak_f32 v54, v31, v48, 0x4b400000
	v_fmaak_f32 v55, v32, v48, 0x4b400000
	v_fmaak_f32 v46, v33, v48, 0x4b400000
	v_perm_b32 v53, v54, v53, s33
	v_perm_b32 v55, v46, v55, s34
	v_or_b32_e32 v79, v53, v55
	s_waitcnt vmcnt(4)
	ds_read_b128 v[18:21], v38 offset:0
	ds_read_b128 v[22:25], v38 offset:1024
	ds_read_b128 v[26:29], v38 offset:2048
	ds_read_b128 v[30:33], v38 offset:3072
	s_waitcnt lgkmcnt(0)
	s_mov_b32 m0, s35
	s_nop 0
	global_load_lds_dwordx4 v34, s[16:17] nt
	global_load_lds_dwordx4 v34, s[16:17] offset:1024 nt
	global_load_lds_dwordx4 v34, s[16:17] offset:2048 nt
	global_load_lds_dwordx4 v35, s[16:17] offset:3072 nt
	s_add_u32 s16, s16, 0x7d00
	s_addc_u32 s17, s17, 0
	v_cndmask_b32_e64 v30, 0, v30, s[18:19]
	v_cndmask_b32_e64 v31, 0, v31, s[18:19]
	v_cndmask_b32_e64 v32, 0, v32, s[18:19]
	v_cndmask_b32_e64 v33, 0, v33, s[18:19]
	v_max3_f32 v41, |v18|, |v19|, |v20|
	v_max3_f32 v42, |v21|, |v22|, |v23|
	v_max3_f32 v43, |v24|, |v25|, |v26|
	v_max3_f32 v44, |v27|, |v28|, |v29|
	v_max3_f32 v45, |v30|, |v31|, |v32|
	v_max3_f32 v41, v41, v42, |v33|
	v_max3_f32 v43, v43, v44, v45
	v_max_f32_e32 v41, v41, v43
	v_pk_add_f32 v[2:3], v[2:3], v[18:19]
	v_pk_add_f32 v[4:5], v[4:5], v[20:21]
	v_max_f32_dpp v41, v41, v41 quad_perm:[1,0,3,2] row_mask:0xf bank_mask:0xf
	v_pk_add_f32 v[6:7], v[6:7], v[22:23]
	v_pk_add_f32 v[8:9], v[8:9], v[24:25]
	v_max_f32_dpp v41, v41, v41 quad_perm:[2,3,0,1] row_mask:0xf bank_mask:0xf
	v_pk_add_f32 v[10:11], v[10:11], v[26:27]
	v_pk_add_f32 v[12:13], v[12:13], v[28:29]
	v_max_f32_dpp v41, v41, v41 row_half_mirror row_mask:0xf bank_mask:0xf
	v_pk_add_f32 v[14:15], v[14:15], v[30:31]
	v_pk_add_f32 v[16:17], v[16:17], v[32:33]
	v_max_f32_dpp v41, v41, v41 row_mirror row_mask:0xf bank_mask:0xf
	s_nop 1
	v_max_f32_dpp v41, v41, v41 row_bcast:15 row_mask:0xa bank_mask:0xf
	s_nop 1
	v_max_f32_dpp v41, v41, v41 row_bcast:31 row_mask:0xc bank_mask:0xf
	s_nop 1
	v_readlane_b32 s28, v41, 63
	s_nop 1
	v_div_scale_f32 v48, s[30:31], s28, s28, v47
	v_rcp_f32_e32 v49, v48
	s_nop 0
	v_fma_f32 v50, -v48, v49, 1.0
	v_fmac_f32_e32 v49, v50, v49
	v_mov_b32_e32 v50, s28
	v_div_scale_f32 v50, vcc, s32, v50, s32
	v_mul_f32_e32 v51, v50, v49
	v_fma_f32 v52, -v48, v51, v50
	v_fmac_f32_e32 v51, v52, v49
	v_fma_f32 v48, -v48, v51, v50
	v_div_fmas_f32 v48, v48, v49, v51
	v_div_fixup_f32 v48, v48, s28, v47
	v_cmp_gt_f32_e64 vcc, s28, 0
	v_writelane_b32 v40, s28, 6
	s_nop 0
	v_cndmask_b32_e32 v48, 0, v48, vcc
	v_fmaak_f32 v49, v18, v48, 0x4b400000
	v_fmaak_f32 v50, v19, v48, 0x4b400000
	v_fmaak_f32 v51, v20, v48, 0x4b400000
	v_fmaak_f32 v52, v21, v48, 0x4b400000
	v_perm_b32 v49, v50, v49, s33
	v_perm_b32 v51, v52, v51, s34
	v_or_b32_e32 v80, v49, v51
	v_fmaak_f32 v53, v22, v48, 0x4b400000
	v_fmaak_f32 v54, v23, v48, 0x4b400000
	v_fmaak_f32 v55, v24, v48, 0x4b400000
	v_fmaak_f32 v46, v25, v48, 0x4b400000
	v_perm_b32 v53, v54, v53, s33
	v_perm_b32 v55, v46, v55, s34
	v_or_b32_e32 v81, v53, v55
	v_fmaak_f32 v49, v26, v48, 0x4b400000
	v_fmaak_f32 v50, v27, v48, 0x4b400000
	v_fmaak_f32 v51, v28, v48, 0x4b400000
	v_fmaak_f32 v52, v29, v48, 0x4b400000
	v_perm_b32 v49, v50, v49, s33
	v_perm_b32 v51, v52, v51, s34
	v_or_b32_e32 v82, v49, v51
	v_fmaak_f32 v53, v30, v48, 0x4b400000
	v_fmaak_f32 v54, v31, v48, 0x4b400000
	v_fmaak_f32 v55, v32, v48, 0x4b400000
	v_fmaak_f32 v46, v33, v48, 0x4b400000
	v_perm_b32 v53, v54, v53, s33
	v_perm_b32 v55, v46, v55, s34
	v_or_b32_e32 v83, v53, v55
	s_waitcnt vmcnt(4)
	ds_read_b128 v[18:21], v38 offset:4096
	ds_read_b128 v[22:25], v38 offset:5120
	ds_read_b128 v[26:29], v38 offset:6144
	ds_read_b128 v[30:33], v38 offset:7168
	s_waitcnt lgkmcnt(0)
	s_mov_b32 m0, s36
	s_nop 0
	global_load_lds_dwordx4 v34, s[16:17] nt
	global_load_lds_dwordx4 v34, s[16:17] offset:1024 nt
	global_load_lds_dwordx4 v34, s[16:17] offset:2048 nt
	global_load_lds_dwordx4 v35, s[16:17] offset:3072 nt
	s_add_u32 s16, s16, 0x7d00
	s_addc_u32 s17, s17, 0
	v_cndmask_b32_e64 v30, 0, v30, s[18:19]
	v_cndmask_b32_e64 v31, 0, v31, s[18:19]
	v_cndmask_b32_e64 v32, 0, v32, s[18:19]
	v_cndmask_b32_e64 v33, 0, v33, s[18:19]
	v_max3_f32 v41, |v18|, |v19|, |v20|
	v_max3_f32 v42, |v21|, |v22|, |v23|
	v_max3_f32 v43, |v24|, |v25|, |v26|
	v_max3_f32 v44, |v27|, |v28|, |v29|
	v_max3_f32 v45, |v30|, |v31|, |v32|
	v_max3_f32 v41, v41, v42, |v33|
	v_max3_f32 v43, v43, v44, v45
	v_max_f32_e32 v41, v41, v43
	v_pk_add_f32 v[2:3], v[2:3], v[18:19]
	v_pk_add_f32 v[4:5], v[4:5], v[20:21]
	v_max_f32_dpp v41, v41, v41 quad_perm:[1,0,3,2] row_mask:0xf bank_mask:0xf
	v_pk_add_f32 v[6:7], v[6:7], v[22:23]
	v_pk_add_f32 v[8:9], v[8:9], v[24:25]
	v_max_f32_dpp v41, v41, v41 quad_perm:[2,3,0,1] row_mask:0xf bank_mask:0xf
	v_pk_add_f32 v[10:11], v[10:11], v[26:27]
	v_pk_add_f32 v[12:13], v[12:13], v[28:29]
	v_max_f32_dpp v41, v41, v41 row_half_mirror row_mask:0xf bank_mask:0xf
	v_pk_add_f32 v[14:15], v[14:15], v[30:31]
	v_pk_add_f32 v[16:17], v[16:17], v[32:33]
	v_max_f32_dpp v41, v41, v41 row_mirror row_mask:0xf bank_mask:0xf
	s_nop 1
	v_max_f32_dpp v41, v41, v41 row_bcast:15 row_mask:0xa bank_mask:0xf
	s_nop 1
	v_max_f32_dpp v41, v41, v41 row_bcast:31 row_mask:0xc bank_mask:0xf
	s_nop 1
	v_readlane_b32 s28, v41, 63
	s_nop 1
	v_div_scale_f32 v48, s[30:31], s28, s28, v47
	v_rcp_f32_e32 v49, v48
	s_nop 0
	v_fma_f32 v50, -v48, v49, 1.0
	v_fmac_f32_e32 v49, v50, v49
	v_mov_b32_e32 v50, s28
	v_div_scale_f32 v50, vcc, s32, v50, s32
	v_mul_f32_e32 v51, v50, v49
	v_fma_f32 v52, -v48, v51, v50
	v_fmac_f32_e32 v51, v52, v49
	v_fma_f32 v48, -v48, v51, v50
	v_div_fmas_f32 v48, v48, v49, v51
	v_div_fixup_f32 v48, v48, s28, v47
	v_cmp_gt_f32_e64 vcc, s28, 0
	v_writelane_b32 v40, s28, 7
	s_nop 0
	v_cndmask_b32_e32 v48, 0, v48, vcc
	v_fmaak_f32 v49, v18, v48, 0x4b400000
	v_fmaak_f32 v50, v19, v48, 0x4b400000
	v_fmaak_f32 v51, v20, v48, 0x4b400000
	v_fmaak_f32 v52, v21, v48, 0x4b400000
	v_perm_b32 v49, v50, v49, s33
	v_perm_b32 v51, v52, v51, s34
	v_or_b32_e32 v84, v49, v51
	v_fmaak_f32 v53, v22, v48, 0x4b400000
	v_fmaak_f32 v54, v23, v48, 0x4b400000
	v_fmaak_f32 v55, v24, v48, 0x4b400000
	v_fmaak_f32 v46, v25, v48, 0x4b400000
	v_perm_b32 v53, v54, v53, s33
	v_perm_b32 v55, v46, v55, s34
	v_or_b32_e32 v85, v53, v55
	v_fmaak_f32 v49, v26, v48, 0x4b400000
	v_fmaak_f32 v50, v27, v48, 0x4b400000
	v_fmaak_f32 v51, v28, v48, 0x4b400000
	v_fmaak_f32 v52, v29, v48, 0x4b400000
	v_perm_b32 v49, v50, v49, s33
	v_perm_b32 v51, v52, v51, s34
	v_or_b32_e32 v86, v49, v51
	v_fmaak_f32 v53, v30, v48, 0x4b400000
	v_fmaak_f32 v54, v31, v48, 0x4b400000
	v_fmaak_f32 v55, v32, v48, 0x4b400000
	v_fmaak_f32 v46, v33, v48, 0x4b400000
	v_perm_b32 v53, v54, v53, s33
	v_perm_b32 v55, v46, v55, s34
	v_or_b32_e32 v87, v53, v55
	s_waitcnt vmcnt(4)
	ds_read_b128 v[18:21], v38 offset:0
	ds_read_b128 v[22:25], v38 offset:1024
	ds_read_b128 v[26:29], v38 offset:2048
	ds_read_b128 v[30:33], v38 offset:3072
	s_waitcnt lgkmcnt(0)
	s_mov_b32 m0, s35
	s_nop 0
	global_load_lds_dwordx4 v34, s[16:17] nt
	global_load_lds_dwordx4 v34, s[16:17] offset:1024 nt
	global_load_lds_dwordx4 v34, s[16:17] offset:2048 nt
	global_load_lds_dwordx4 v35, s[16:17] offset:3072 nt
	s_add_u32 s16, s16, 0x7d00
	s_addc_u32 s17, s17, 0
	v_cndmask_b32_e64 v30, 0, v30, s[18:19]
	v_cndmask_b32_e64 v31, 0, v31, s[18:19]
	v_cndmask_b32_e64 v32, 0, v32, s[18:19]
	v_cndmask_b32_e64 v33, 0, v33, s[18:19]
	v_max3_f32 v41, |v18|, |v19|, |v20|
	v_max3_f32 v42, |v21|, |v22|, |v23|
	v_max3_f32 v43, |v24|, |v25|, |v26|
	v_max3_f32 v44, |v27|, |v28|, |v29|
	v_max3_f32 v45, |v30|, |v31|, |v32|
	v_max3_f32 v41, v41, v42, |v33|
	v_max3_f32 v43, v43, v44, v45
	v_max_f32_e32 v41, v41, v43
	v_pk_add_f32 v[2:3], v[2:3], v[18:19]
	v_pk_add_f32 v[4:5], v[4:5], v[20:21]
	v_max_f32_dpp v41, v41, v41 quad_perm:[1,0,3,2] row_mask:0xf bank_mask:0xf
	v_pk_add_f32 v[6:7], v[6:7], v[22:23]
	v_pk_add_f32 v[8:9], v[8:9], v[24:25]
	v_max_f32_dpp v41, v41, v41 quad_perm:[2,3,0,1] row_mask:0xf bank_mask:0xf
	v_pk_add_f32 v[10:11], v[10:11], v[26:27]
	v_pk_add_f32 v[12:13], v[12:13], v[28:29]
	v_max_f32_dpp v41, v41, v41 row_half_mirror row_mask:0xf bank_mask:0xf
	v_pk_add_f32 v[14:15], v[14:15], v[30:31]
	v_pk_add_f32 v[16:17], v[16:17], v[32:33]
	v_max_f32_dpp v41, v41, v41 row_mirror row_mask:0xf bank_mask:0xf
	s_nop 1
	v_max_f32_dpp v41, v41, v41 row_bcast:15 row_mask:0xa bank_mask:0xf
	s_nop 1
	v_max_f32_dpp v41, v41, v41 row_bcast:31 row_mask:0xc bank_mask:0xf
	s_nop 1
	v_readlane_b32 s28, v41, 63
	s_nop 1
	v_div_scale_f32 v48, s[30:31], s28, s28, v47
	v_rcp_f32_e32 v49, v48
	s_nop 0
	v_fma_f32 v50, -v48, v49, 1.0
	v_fmac_f32_e32 v49, v50, v49
	v_mov_b32_e32 v50, s28
	v_div_scale_f32 v50, vcc, s32, v50, s32
	v_mul_f32_e32 v51, v50, v49
	v_fma_f32 v52, -v48, v51, v50
	v_fmac_f32_e32 v51, v52, v49
	v_fma_f32 v48, -v48, v51, v50
	v_div_fmas_f32 v48, v48, v49, v51
	v_div_fixup_f32 v48, v48, s28, v47
	v_cmp_gt_f32_e64 vcc, s28, 0
	v_writelane_b32 v40, s28, 8
	s_nop 0
	v_cndmask_b32_e32 v48, 0, v48, vcc
	v_fmaak_f32 v49, v18, v48, 0x4b400000
	v_fmaak_f32 v50, v19, v48, 0x4b400000
	v_fmaak_f32 v51, v20, v48, 0x4b400000
	v_fmaak_f32 v52, v21, v48, 0x4b400000
	v_perm_b32 v49, v50, v49, s33
	v_perm_b32 v51, v52, v51, s34
	v_or_b32_e32 v88, v49, v51
	v_fmaak_f32 v53, v22, v48, 0x4b400000
	v_fmaak_f32 v54, v23, v48, 0x4b400000
	v_fmaak_f32 v55, v24, v48, 0x4b400000
	v_fmaak_f32 v46, v25, v48, 0x4b400000
	v_perm_b32 v53, v54, v53, s33
	v_perm_b32 v55, v46, v55, s34
	v_or_b32_e32 v89, v53, v55
	v_fmaak_f32 v49, v26, v48, 0x4b400000
	v_fmaak_f32 v50, v27, v48, 0x4b400000
	v_fmaak_f32 v51, v28, v48, 0x4b400000
	v_fmaak_f32 v52, v29, v48, 0x4b400000
	v_perm_b32 v49, v50, v49, s33
	v_perm_b32 v51, v52, v51, s34
	v_or_b32_e32 v90, v49, v51
	v_fmaak_f32 v53, v30, v48, 0x4b400000
	v_fmaak_f32 v54, v31, v48, 0x4b400000
	v_fmaak_f32 v55, v32, v48, 0x4b400000
	v_fmaak_f32 v46, v33, v48, 0x4b400000
	v_perm_b32 v53, v54, v53, s33
	v_perm_b32 v55, v46, v55, s34
	v_or_b32_e32 v91, v53, v55
	s_waitcnt vmcnt(4)
	ds_read_b128 v[18:21], v38 offset:4096
	ds_read_b128 v[22:25], v38 offset:5120
	ds_read_b128 v[26:29], v38 offset:6144
	ds_read_b128 v[30:33], v38 offset:7168
	s_waitcnt lgkmcnt(0)
	s_mov_b32 m0, s36
	s_nop 0
	global_load_lds_dwordx4 v34, s[16:17] nt
	global_load_lds_dwordx4 v34, s[16:17] offset:1024 nt
	global_load_lds_dwordx4 v34, s[16:17] offset:2048 nt
	global_load_lds_dwordx4 v35, s[16:17] offset:3072 nt
	s_add_u32 s16, s16, 0x7d00
	s_addc_u32 s17, s17, 0
	v_cndmask_b32_e64 v30, 0, v30, s[18:19]
	v_cndmask_b32_e64 v31, 0, v31, s[18:19]
	v_cndmask_b32_e64 v32, 0, v32, s[18:19]
	v_cndmask_b32_e64 v33, 0, v33, s[18:19]
	v_max3_f32 v41, |v18|, |v19|, |v20|
	v_max3_f32 v42, |v21|, |v22|, |v23|
	v_max3_f32 v43, |v24|, |v25|, |v26|
	v_max3_f32 v44, |v27|, |v28|, |v29|
	v_max3_f32 v45, |v30|, |v31|, |v32|
	v_max3_f32 v41, v41, v42, |v33|
	v_max3_f32 v43, v43, v44, v45
	v_max_f32_e32 v41, v41, v43
	v_pk_add_f32 v[2:3], v[2:3], v[18:19]
	v_pk_add_f32 v[4:5], v[4:5], v[20:21]
	v_max_f32_dpp v41, v41, v41 quad_perm:[1,0,3,2] row_mask:0xf bank_mask:0xf
	v_pk_add_f32 v[6:7], v[6:7], v[22:23]
	v_pk_add_f32 v[8:9], v[8:9], v[24:25]
	v_max_f32_dpp v41, v41, v41 quad_perm:[2,3,0,1] row_mask:0xf bank_mask:0xf
	v_pk_add_f32 v[10:11], v[10:11], v[26:27]
	v_pk_add_f32 v[12:13], v[12:13], v[28:29]
	v_max_f32_dpp v41, v41, v41 row_half_mirror row_mask:0xf bank_mask:0xf
	v_pk_add_f32 v[14:15], v[14:15], v[30:31]
	v_pk_add_f32 v[16:17], v[16:17], v[32:33]
	v_max_f32_dpp v41, v41, v41 row_mirror row_mask:0xf bank_mask:0xf
	s_nop 1
	v_max_f32_dpp v41, v41, v41 row_bcast:15 row_mask:0xa bank_mask:0xf
	s_nop 1
	v_max_f32_dpp v41, v41, v41 row_bcast:31 row_mask:0xc bank_mask:0xf
	s_nop 1
	v_readlane_b32 s28, v41, 63
	s_nop 1
	v_div_scale_f32 v48, s[30:31], s28, s28, v47
	v_rcp_f32_e32 v49, v48
	s_nop 0
	v_fma_f32 v50, -v48, v49, 1.0
	v_fmac_f32_e32 v49, v50, v49
	v_mov_b32_e32 v50, s28
	v_div_scale_f32 v50, vcc, s32, v50, s32
	v_mul_f32_e32 v51, v50, v49
	v_fma_f32 v52, -v48, v51, v50
	v_fmac_f32_e32 v51, v52, v49
	v_fma_f32 v48, -v48, v51, v50
	v_div_fmas_f32 v48, v48, v49, v51
	v_div_fixup_f32 v48, v48, s28, v47
	v_cmp_gt_f32_e64 vcc, s28, 0
	v_writelane_b32 v40, s28, 9
	s_nop 0
	v_cndmask_b32_e32 v48, 0, v48, vcc
	v_fmaak_f32 v49, v18, v48, 0x4b400000
	v_fmaak_f32 v50, v19, v48, 0x4b400000
	v_fmaak_f32 v51, v20, v48, 0x4b400000
	v_fmaak_f32 v52, v21, v48, 0x4b400000
	v_perm_b32 v49, v50, v49, s33
	v_perm_b32 v51, v52, v51, s34
	v_or_b32_e32 v92, v49, v51
	v_fmaak_f32 v53, v22, v48, 0x4b400000
	v_fmaak_f32 v54, v23, v48, 0x4b400000
	v_fmaak_f32 v55, v24, v48, 0x4b400000
	v_fmaak_f32 v46, v25, v48, 0x4b400000
	v_perm_b32 v53, v54, v53, s33
	v_perm_b32 v55, v46, v55, s34
	v_or_b32_e32 v93, v53, v55
	v_fmaak_f32 v49, v26, v48, 0x4b400000
	v_fmaak_f32 v50, v27, v48, 0x4b400000
	v_fmaak_f32 v51, v28, v48, 0x4b400000
	v_fmaak_f32 v52, v29, v48, 0x4b400000
	v_perm_b32 v49, v50, v49, s33
	v_perm_b32 v51, v52, v51, s34
	v_or_b32_e32 v94, v49, v51
	v_fmaak_f32 v53, v30, v48, 0x4b400000
	v_fmaak_f32 v54, v31, v48, 0x4b400000
	v_fmaak_f32 v55, v32, v48, 0x4b400000
	v_fmaak_f32 v46, v33, v48, 0x4b400000
	v_perm_b32 v53, v54, v53, s33
	v_perm_b32 v55, v46, v55, s34
	v_or_b32_e32 v95, v53, v55
	s_waitcnt vmcnt(4)
	ds_read_b128 v[18:21], v38 offset:0
	ds_read_b128 v[22:25], v38 offset:1024
	ds_read_b128 v[26:29], v38 offset:2048
	ds_read_b128 v[30:33], v38 offset:3072
	s_waitcnt lgkmcnt(0)
	s_mov_b32 m0, s35
	s_nop 0
	global_load_lds_dwordx4 v34, s[16:17] nt
	global_load_lds_dwordx4 v34, s[16:17] offset:1024 nt
	global_load_lds_dwordx4 v34, s[16:17] offset:2048 nt
	global_load_lds_dwordx4 v35, s[16:17] offset:3072 nt
	s_add_u32 s16, s16, 0x7d00
	s_addc_u32 s17, s17, 0
	v_cndmask_b32_e64 v30, 0, v30, s[18:19]
	v_cndmask_b32_e64 v31, 0, v31, s[18:19]
	v_cndmask_b32_e64 v32, 0, v32, s[18:19]
	v_cndmask_b32_e64 v33, 0, v33, s[18:19]
	v_max3_f32 v41, |v18|, |v19|, |v20|
	v_max3_f32 v42, |v21|, |v22|, |v23|
	v_max3_f32 v43, |v24|, |v25|, |v26|
	v_max3_f32 v44, |v27|, |v28|, |v29|
	v_max3_f32 v45, |v30|, |v31|, |v32|
	v_max3_f32 v41, v41, v42, |v33|
	v_max3_f32 v43, v43, v44, v45
	v_max_f32_e32 v41, v41, v43
	v_pk_add_f32 v[2:3], v[2:3], v[18:19]
	v_pk_add_f32 v[4:5], v[4:5], v[20:21]
	v_max_f32_dpp v41, v41, v41 quad_perm:[1,0,3,2] row_mask:0xf bank_mask:0xf
	v_pk_add_f32 v[6:7], v[6:7], v[22:23]
	v_pk_add_f32 v[8:9], v[8:9], v[24:25]
	v_max_f32_dpp v41, v41, v41 quad_perm:[2,3,0,1] row_mask:0xf bank_mask:0xf
	v_pk_add_f32 v[10:11], v[10:11], v[26:27]
	v_pk_add_f32 v[12:13], v[12:13], v[28:29]
	v_max_f32_dpp v41, v41, v41 row_half_mirror row_mask:0xf bank_mask:0xf
	v_pk_add_f32 v[14:15], v[14:15], v[30:31]
	v_pk_add_f32 v[16:17], v[16:17], v[32:33]
	v_max_f32_dpp v41, v41, v41 row_mirror row_mask:0xf bank_mask:0xf
	s_nop 1
	v_max_f32_dpp v41, v41, v41 row_bcast:15 row_mask:0xa bank_mask:0xf
	s_nop 1
	v_max_f32_dpp v41, v41, v41 row_bcast:31 row_mask:0xc bank_mask:0xf
	s_nop 1
	v_readlane_b32 s28, v41, 63
	s_nop 1
	v_div_scale_f32 v48, s[30:31], s28, s28, v47
	v_rcp_f32_e32 v49, v48
	s_nop 0
	v_fma_f32 v50, -v48, v49, 1.0
	v_fmac_f32_e32 v49, v50, v49
	v_mov_b32_e32 v50, s28
	v_div_scale_f32 v50, vcc, s32, v50, s32
	v_mul_f32_e32 v51, v50, v49
	v_fma_f32 v52, -v48, v51, v50
	v_fmac_f32_e32 v51, v52, v49
	v_fma_f32 v48, -v48, v51, v50
	v_div_fmas_f32 v48, v48, v49, v51
	v_div_fixup_f32 v48, v48, s28, v47
	v_cmp_gt_f32_e64 vcc, s28, 0
	v_writelane_b32 v40, s28, 10
	s_nop 0
	v_cndmask_b32_e32 v48, 0, v48, vcc
	v_fmaak_f32 v49, v18, v48, 0x4b400000
	v_fmaak_f32 v50, v19, v48, 0x4b400000
	v_fmaak_f32 v51, v20, v48, 0x4b400000
	v_fmaak_f32 v52, v21, v48, 0x4b400000
	v_perm_b32 v49, v50, v49, s33
	v_perm_b32 v51, v52, v51, s34
	v_or_b32_e32 v96, v49, v51
	v_fmaak_f32 v53, v22, v48, 0x4b400000
	v_fmaak_f32 v54, v23, v48, 0x4b400000
	v_fmaak_f32 v55, v24, v48, 0x4b400000
	v_fmaak_f32 v46, v25, v48, 0x4b400000
	v_perm_b32 v53, v54, v53, s33
	v_perm_b32 v55, v46, v55, s34
	v_or_b32_e32 v97, v53, v55
	v_fmaak_f32 v49, v26, v48, 0x4b400000
	v_fmaak_f32 v50, v27, v48, 0x4b400000
	v_fmaak_f32 v51, v28, v48, 0x4b400000
	v_fmaak_f32 v52, v29, v48, 0x4b400000
	v_perm_b32 v49, v50, v49, s33
	v_perm_b32 v51, v52, v51, s34
	v_or_b32_e32 v98, v49, v51
	v_fmaak_f32 v53, v30, v48, 0x4b400000
	v_fmaak_f32 v54, v31, v48, 0x4b400000
	v_fmaak_f32 v55, v32, v48, 0x4b400000
	v_fmaak_f32 v46, v33, v48, 0x4b400000
	v_perm_b32 v53, v54, v53, s33
	v_perm_b32 v55, v46, v55, s34
	v_or_b32_e32 v99, v53, v55
	s_waitcnt vmcnt(4)
	ds_read_b128 v[18:21], v38 offset:4096
	ds_read_b128 v[22:25], v38 offset:5120
	ds_read_b128 v[26:29], v38 offset:6144
	ds_read_b128 v[30:33], v38 offset:7168
	s_waitcnt lgkmcnt(0)
	s_mov_b32 m0, s36
	s_nop 0
	global_load_lds_dwordx4 v34, s[16:17] nt
	global_load_lds_dwordx4 v34, s[16:17] offset:1024 nt
	global_load_lds_dwordx4 v34, s[16:17] offset:2048 nt
	global_load_lds_dwordx4 v35, s[16:17] offset:3072 nt
	s_add_u32 s16, s16, 0x7d00
	s_addc_u32 s17, s17, 0
	v_cndmask_b32_e64 v30, 0, v30, s[18:19]
	v_cndmask_b32_e64 v31, 0, v31, s[18:19]
	v_cndmask_b32_e64 v32, 0, v32, s[18:19]
	v_cndmask_b32_e64 v33, 0, v33, s[18:19]
	v_max3_f32 v41, |v18|, |v19|, |v20|
	v_max3_f32 v42, |v21|, |v22|, |v23|
	v_max3_f32 v43, |v24|, |v25|, |v26|
	v_max3_f32 v44, |v27|, |v28|, |v29|
	v_max3_f32 v45, |v30|, |v31|, |v32|
	v_max3_f32 v41, v41, v42, |v33|
	v_max3_f32 v43, v43, v44, v45
	v_max_f32_e32 v41, v41, v43
	v_pk_add_f32 v[2:3], v[2:3], v[18:19]
	v_pk_add_f32 v[4:5], v[4:5], v[20:21]
	v_max_f32_dpp v41, v41, v41 quad_perm:[1,0,3,2] row_mask:0xf bank_mask:0xf
	v_pk_add_f32 v[6:7], v[6:7], v[22:23]
	v_pk_add_f32 v[8:9], v[8:9], v[24:25]
	v_max_f32_dpp v41, v41, v41 quad_perm:[2,3,0,1] row_mask:0xf bank_mask:0xf
	v_pk_add_f32 v[10:11], v[10:11], v[26:27]
	v_pk_add_f32 v[12:13], v[12:13], v[28:29]
	v_max_f32_dpp v41, v41, v41 row_half_mirror row_mask:0xf bank_mask:0xf
	v_pk_add_f32 v[14:15], v[14:15], v[30:31]
	v_pk_add_f32 v[16:17], v[16:17], v[32:33]
	v_max_f32_dpp v41, v41, v41 row_mirror row_mask:0xf bank_mask:0xf
	s_nop 1
	v_max_f32_dpp v41, v41, v41 row_bcast:15 row_mask:0xa bank_mask:0xf
	s_nop 1
	v_max_f32_dpp v41, v41, v41 row_bcast:31 row_mask:0xc bank_mask:0xf
	s_nop 1
	v_readlane_b32 s28, v41, 63
	s_nop 1
	v_div_scale_f32 v48, s[30:31], s28, s28, v47
	v_rcp_f32_e32 v49, v48
	s_nop 0
	v_fma_f32 v50, -v48, v49, 1.0
	v_fmac_f32_e32 v49, v50, v49
	v_mov_b32_e32 v50, s28
	v_div_scale_f32 v50, vcc, s32, v50, s32
	v_mul_f32_e32 v51, v50, v49
	v_fma_f32 v52, -v48, v51, v50
	v_fmac_f32_e32 v51, v52, v49
	v_fma_f32 v48, -v48, v51, v50
	v_div_fmas_f32 v48, v48, v49, v51
	v_div_fixup_f32 v48, v48, s28, v47
	v_cmp_gt_f32_e64 vcc, s28, 0
	v_writelane_b32 v40, s28, 11
	s_nop 0
	v_cndmask_b32_e32 v48, 0, v48, vcc
	v_fmaak_f32 v49, v18, v48, 0x4b400000
	v_fmaak_f32 v50, v19, v48, 0x4b400000
	v_fmaak_f32 v51, v20, v48, 0x4b400000
	v_fmaak_f32 v52, v21, v48, 0x4b400000
	v_perm_b32 v49, v50, v49, s33
	v_perm_b32 v51, v52, v51, s34
	v_or_b32_e32 v100, v49, v51
	v_fmaak_f32 v53, v22, v48, 0x4b400000
	v_fmaak_f32 v54, v23, v48, 0x4b400000
	v_fmaak_f32 v55, v24, v48, 0x4b400000
	v_fmaak_f32 v46, v25, v48, 0x4b400000
	v_perm_b32 v53, v54, v53, s33
	v_perm_b32 v55, v46, v55, s34
	v_or_b32_e32 v101, v53, v55
	v_fmaak_f32 v49, v26, v48, 0x4b400000
	v_fmaak_f32 v50, v27, v48, 0x4b400000
	v_fmaak_f32 v51, v28, v48, 0x4b400000
	v_fmaak_f32 v52, v29, v48, 0x4b400000
	v_perm_b32 v49, v50, v49, s33
	v_perm_b32 v51, v52, v51, s34
	v_or_b32_e32 v102, v49, v51
	v_fmaak_f32 v53, v30, v48, 0x4b400000
	v_fmaak_f32 v54, v31, v48, 0x4b400000
	v_fmaak_f32 v55, v32, v48, 0x4b400000
	v_fmaak_f32 v46, v33, v48, 0x4b400000
	v_perm_b32 v53, v54, v53, s33
	v_perm_b32 v55, v46, v55, s34
	v_or_b32_e32 v103, v53, v55
	s_waitcnt vmcnt(4)
	ds_read_b128 v[18:21], v38 offset:0
	ds_read_b128 v[22:25], v38 offset:1024
	ds_read_b128 v[26:29], v38 offset:2048
	ds_read_b128 v[30:33], v38 offset:3072
	s_waitcnt lgkmcnt(0)
	s_mov_b32 m0, s35
	s_nop 0
	global_load_lds_dwordx4 v34, s[16:17] nt
	global_load_lds_dwordx4 v34, s[16:17] offset:1024 nt
	global_load_lds_dwordx4 v34, s[16:17] offset:2048 nt
	global_load_lds_dwordx4 v35, s[16:17] offset:3072 nt
	s_add_u32 s16, s16, 0x7d00
	s_addc_u32 s17, s17, 0
	v_cndmask_b32_e64 v30, 0, v30, s[18:19]
	v_cndmask_b32_e64 v31, 0, v31, s[18:19]
	v_cndmask_b32_e64 v32, 0, v32, s[18:19]
	v_cndmask_b32_e64 v33, 0, v33, s[18:19]
	v_max3_f32 v41, |v18|, |v19|, |v20|
	v_max3_f32 v42, |v21|, |v22|, |v23|
	v_max3_f32 v43, |v24|, |v25|, |v26|
	v_max3_f32 v44, |v27|, |v28|, |v29|
	v_max3_f32 v45, |v30|, |v31|, |v32|
	v_max3_f32 v41, v41, v42, |v33|
	v_max3_f32 v43, v43, v44, v45
	v_max_f32_e32 v41, v41, v43
	v_pk_add_f32 v[2:3], v[2:3], v[18:19]
	v_pk_add_f32 v[4:5], v[4:5], v[20:21]
	v_max_f32_dpp v41, v41, v41 quad_perm:[1,0,3,2] row_mask:0xf bank_mask:0xf
	v_pk_add_f32 v[6:7], v[6:7], v[22:23]
	v_pk_add_f32 v[8:9], v[8:9], v[24:25]
	v_max_f32_dpp v41, v41, v41 quad_perm:[2,3,0,1] row_mask:0xf bank_mask:0xf
	v_pk_add_f32 v[10:11], v[10:11], v[26:27]
	v_pk_add_f32 v[12:13], v[12:13], v[28:29]
	v_max_f32_dpp v41, v41, v41 row_half_mirror row_mask:0xf bank_mask:0xf
	v_pk_add_f32 v[14:15], v[14:15], v[30:31]
	v_pk_add_f32 v[16:17], v[16:17], v[32:33]
	v_max_f32_dpp v41, v41, v41 row_mirror row_mask:0xf bank_mask:0xf
	s_nop 1
	v_max_f32_dpp v41, v41, v41 row_bcast:15 row_mask:0xa bank_mask:0xf
	s_nop 1
	v_max_f32_dpp v41, v41, v41 row_bcast:31 row_mask:0xc bank_mask:0xf
	s_nop 1
	v_readlane_b32 s28, v41, 63
	s_nop 1
	v_div_scale_f32 v48, s[30:31], s28, s28, v47
	v_rcp_f32_e32 v49, v48
	s_nop 0
	v_fma_f32 v50, -v48, v49, 1.0
	v_fmac_f32_e32 v49, v50, v49
	v_mov_b32_e32 v50, s28
	v_div_scale_f32 v50, vcc, s32, v50, s32
	v_mul_f32_e32 v51, v50, v49
	v_fma_f32 v52, -v48, v51, v50
	v_fmac_f32_e32 v51, v52, v49
	v_fma_f32 v48, -v48, v51, v50
	v_div_fmas_f32 v48, v48, v49, v51
	v_div_fixup_f32 v48, v48, s28, v47
	v_cmp_gt_f32_e64 vcc, s28, 0
	v_writelane_b32 v40, s28, 12
	s_nop 0
	v_cndmask_b32_e32 v48, 0, v48, vcc
	v_fmaak_f32 v49, v18, v48, 0x4b400000
	v_fmaak_f32 v50, v19, v48, 0x4b400000
	v_fmaak_f32 v51, v20, v48, 0x4b400000
	v_fmaak_f32 v52, v21, v48, 0x4b400000
	v_perm_b32 v49, v50, v49, s33
	v_perm_b32 v51, v52, v51, s34
	v_or_b32_e32 v104, v49, v51
	v_fmaak_f32 v53, v22, v48, 0x4b400000
	v_fmaak_f32 v54, v23, v48, 0x4b400000
	v_fmaak_f32 v55, v24, v48, 0x4b400000
	v_fmaak_f32 v46, v25, v48, 0x4b400000
	v_perm_b32 v53, v54, v53, s33
	v_perm_b32 v55, v46, v55, s34
	v_or_b32_e32 v105, v53, v55
	v_fmaak_f32 v49, v26, v48, 0x4b400000
	v_fmaak_f32 v50, v27, v48, 0x4b400000
	v_fmaak_f32 v51, v28, v48, 0x4b400000
	v_fmaak_f32 v52, v29, v48, 0x4b400000
	v_perm_b32 v49, v50, v49, s33
	v_perm_b32 v51, v52, v51, s34
	v_or_b32_e32 v106, v49, v51
	v_fmaak_f32 v53, v30, v48, 0x4b400000
	v_fmaak_f32 v54, v31, v48, 0x4b400000
	v_fmaak_f32 v55, v32, v48, 0x4b400000
	v_fmaak_f32 v46, v33, v48, 0x4b400000
	v_perm_b32 v53, v54, v53, s33
	v_perm_b32 v55, v46, v55, s34
	v_or_b32_e32 v107, v53, v55
	s_waitcnt vmcnt(4)
	ds_read_b128 v[18:21], v38 offset:4096
	ds_read_b128 v[22:25], v38 offset:5120
	ds_read_b128 v[26:29], v38 offset:6144
	ds_read_b128 v[30:33], v38 offset:7168
	s_waitcnt lgkmcnt(0)
	s_mov_b32 m0, s36
	s_nop 0
	global_load_lds_dwordx4 v34, s[16:17] nt
	global_load_lds_dwordx4 v34, s[16:17] offset:1024 nt
	global_load_lds_dwordx4 v34, s[16:17] offset:2048 nt
	global_load_lds_dwordx4 v35, s[16:17] offset:3072 nt
	s_add_u32 s16, s16, 0x7d00
	s_addc_u32 s17, s17, 0
	v_cndmask_b32_e64 v30, 0, v30, s[18:19]
	v_cndmask_b32_e64 v31, 0, v31, s[18:19]
	v_cndmask_b32_e64 v32, 0, v32, s[18:19]
	v_cndmask_b32_e64 v33, 0, v33, s[18:19]
	v_max3_f32 v41, |v18|, |v19|, |v20|
	v_max3_f32 v42, |v21|, |v22|, |v23|
	v_max3_f32 v43, |v24|, |v25|, |v26|
	v_max3_f32 v44, |v27|, |v28|, |v29|
	v_max3_f32 v45, |v30|, |v31|, |v32|
	v_max3_f32 v41, v41, v42, |v33|
	v_max3_f32 v43, v43, v44, v45
	v_max_f32_e32 v41, v41, v43
	v_pk_add_f32 v[2:3], v[2:3], v[18:19]
	v_pk_add_f32 v[4:5], v[4:5], v[20:21]
	v_max_f32_dpp v41, v41, v41 quad_perm:[1,0,3,2] row_mask:0xf bank_mask:0xf
	v_pk_add_f32 v[6:7], v[6:7], v[22:23]
	v_pk_add_f32 v[8:9], v[8:9], v[24:25]
	v_max_f32_dpp v41, v41, v41 quad_perm:[2,3,0,1] row_mask:0xf bank_mask:0xf
	v_pk_add_f32 v[10:11], v[10:11], v[26:27]
	v_pk_add_f32 v[12:13], v[12:13], v[28:29]
	v_max_f32_dpp v41, v41, v41 row_half_mirror row_mask:0xf bank_mask:0xf
	v_pk_add_f32 v[14:15], v[14:15], v[30:31]
	v_pk_add_f32 v[16:17], v[16:17], v[32:33]
	v_max_f32_dpp v41, v41, v41 row_mirror row_mask:0xf bank_mask:0xf
	s_nop 1
	v_max_f32_dpp v41, v41, v41 row_bcast:15 row_mask:0xa bank_mask:0xf
	s_nop 1
	v_max_f32_dpp v41, v41, v41 row_bcast:31 row_mask:0xc bank_mask:0xf
	s_nop 1
	v_readlane_b32 s28, v41, 63
	s_nop 1
	v_div_scale_f32 v48, s[30:31], s28, s28, v47
	v_rcp_f32_e32 v49, v48
	s_nop 0
	v_fma_f32 v50, -v48, v49, 1.0
	v_fmac_f32_e32 v49, v50, v49
	v_mov_b32_e32 v50, s28
	v_div_scale_f32 v50, vcc, s32, v50, s32
	v_mul_f32_e32 v51, v50, v49
	v_fma_f32 v52, -v48, v51, v50
	v_fmac_f32_e32 v51, v52, v49
	v_fma_f32 v48, -v48, v51, v50
	v_div_fmas_f32 v48, v48, v49, v51
	v_div_fixup_f32 v48, v48, s28, v47
	v_cmp_gt_f32_e64 vcc, s28, 0
	v_writelane_b32 v40, s28, 13
	s_nop 0
	v_cndmask_b32_e32 v48, 0, v48, vcc
	v_fmaak_f32 v49, v18, v48, 0x4b400000
	v_fmaak_f32 v50, v19, v48, 0x4b400000
	v_fmaak_f32 v51, v20, v48, 0x4b400000
	v_fmaak_f32 v52, v21, v48, 0x4b400000
	v_perm_b32 v49, v50, v49, s33
	v_perm_b32 v51, v52, v51, s34
	v_or_b32_e32 v108, v49, v51
	v_fmaak_f32 v53, v22, v48, 0x4b400000
	v_fmaak_f32 v54, v23, v48, 0x4b400000
	v_fmaak_f32 v55, v24, v48, 0x4b400000
	v_fmaak_f32 v46, v25, v48, 0x4b400000
	v_perm_b32 v53, v54, v53, s33
	v_perm_b32 v55, v46, v55, s34
	v_or_b32_e32 v109, v53, v55
	v_fmaak_f32 v49, v26, v48, 0x4b400000
	v_fmaak_f32 v50, v27, v48, 0x4b400000
	v_fmaak_f32 v51, v28, v48, 0x4b400000
	v_fmaak_f32 v52, v29, v48, 0x4b400000
	v_perm_b32 v49, v50, v49, s33
	v_perm_b32 v51, v52, v51, s34
	v_or_b32_e32 v110, v49, v51
	v_fmaak_f32 v53, v30, v48, 0x4b400000
	v_fmaak_f32 v54, v31, v48, 0x4b400000
	v_fmaak_f32 v55, v32, v48, 0x4b400000
	v_fmaak_f32 v46, v33, v48, 0x4b400000
	v_perm_b32 v53, v54, v53, s33
	v_perm_b32 v55, v46, v55, s34
	v_or_b32_e32 v111, v53, v55
	s_waitcnt vmcnt(4)
	ds_read_b128 v[18:21], v38 offset:0
	ds_read_b128 v[22:25], v38 offset:1024
	ds_read_b128 v[26:29], v38 offset:2048
	ds_read_b128 v[30:33], v38 offset:3072
	s_waitcnt lgkmcnt(0)
	s_mov_b32 m0, s35
	s_nop 0
	global_load_lds_dwordx4 v34, s[16:17] nt
	global_load_lds_dwordx4 v34, s[16:17] offset:1024 nt
	global_load_lds_dwordx4 v34, s[16:17] offset:2048 nt
	global_load_lds_dwordx4 v35, s[16:17] offset:3072 nt
	s_add_u32 s16, s16, 0x7d00
	s_addc_u32 s17, s17, 0
	v_cndmask_b32_e64 v30, 0, v30, s[18:19]
	v_cndmask_b32_e64 v31, 0, v31, s[18:19]
	v_cndmask_b32_e64 v32, 0, v32, s[18:19]
	v_cndmask_b32_e64 v33, 0, v33, s[18:19]
	v_max3_f32 v41, |v18|, |v19|, |v20|
	v_max3_f32 v42, |v21|, |v22|, |v23|
	v_max3_f32 v43, |v24|, |v25|, |v26|
	v_max3_f32 v44, |v27|, |v28|, |v29|
	v_max3_f32 v45, |v30|, |v31|, |v32|
	v_max3_f32 v41, v41, v42, |v33|
	v_max3_f32 v43, v43, v44, v45
	v_max_f32_e32 v41, v41, v43
	v_pk_add_f32 v[2:3], v[2:3], v[18:19]
	v_pk_add_f32 v[4:5], v[4:5], v[20:21]
	v_max_f32_dpp v41, v41, v41 quad_perm:[1,0,3,2] row_mask:0xf bank_mask:0xf
	v_pk_add_f32 v[6:7], v[6:7], v[22:23]
	v_pk_add_f32 v[8:9], v[8:9], v[24:25]
	v_max_f32_dpp v41, v41, v41 quad_perm:[2,3,0,1] row_mask:0xf bank_mask:0xf
	v_pk_add_f32 v[10:11], v[10:11], v[26:27]
	v_pk_add_f32 v[12:13], v[12:13], v[28:29]
	v_max_f32_dpp v41, v41, v41 row_half_mirror row_mask:0xf bank_mask:0xf
	v_pk_add_f32 v[14:15], v[14:15], v[30:31]
	v_pk_add_f32 v[16:17], v[16:17], v[32:33]
	v_max_f32_dpp v41, v41, v41 row_mirror row_mask:0xf bank_mask:0xf
	s_nop 1
	v_max_f32_dpp v41, v41, v41 row_bcast:15 row_mask:0xa bank_mask:0xf
	s_nop 1
	v_max_f32_dpp v41, v41, v41 row_bcast:31 row_mask:0xc bank_mask:0xf
	s_nop 1
	v_readlane_b32 s28, v41, 63
	s_nop 1
	v_div_scale_f32 v48, s[30:31], s28, s28, v47
	v_rcp_f32_e32 v49, v48
	s_nop 0
	v_fma_f32 v50, -v48, v49, 1.0
	v_fmac_f32_e32 v49, v50, v49
	v_mov_b32_e32 v50, s28
	v_div_scale_f32 v50, vcc, s32, v50, s32
	v_mul_f32_e32 v51, v50, v49
	v_fma_f32 v52, -v48, v51, v50
	v_fmac_f32_e32 v51, v52, v49
	v_fma_f32 v48, -v48, v51, v50
	v_div_fmas_f32 v48, v48, v49, v51
	v_div_fixup_f32 v48, v48, s28, v47
	v_cmp_gt_f32_e64 vcc, s28, 0
	v_writelane_b32 v40, s28, 14
	s_nop 0
	v_cndmask_b32_e32 v48, 0, v48, vcc
	v_fmaak_f32 v49, v18, v48, 0x4b400000
	v_fmaak_f32 v50, v19, v48, 0x4b400000
	v_fmaak_f32 v51, v20, v48, 0x4b400000
	v_fmaak_f32 v52, v21, v48, 0x4b400000
	v_perm_b32 v49, v50, v49, s33
	v_perm_b32 v51, v52, v51, s34
	v_or_b32_e32 v112, v49, v51
	v_fmaak_f32 v53, v22, v48, 0x4b400000
	v_fmaak_f32 v54, v23, v48, 0x4b400000
	v_fmaak_f32 v55, v24, v48, 0x4b400000
	v_fmaak_f32 v46, v25, v48, 0x4b400000
	v_perm_b32 v53, v54, v53, s33
	v_perm_b32 v55, v46, v55, s34
	v_or_b32_e32 v113, v53, v55
	v_fmaak_f32 v49, v26, v48, 0x4b400000
	v_fmaak_f32 v50, v27, v48, 0x4b400000
	v_fmaak_f32 v51, v28, v48, 0x4b400000
	v_fmaak_f32 v52, v29, v48, 0x4b400000
	v_perm_b32 v49, v50, v49, s33
	v_perm_b32 v51, v52, v51, s34
	v_or_b32_e32 v114, v49, v51
	v_fmaak_f32 v53, v30, v48, 0x4b400000
	v_fmaak_f32 v54, v31, v48, 0x4b400000
	v_fmaak_f32 v55, v32, v48, 0x4b400000
	v_fmaak_f32 v46, v33, v48, 0x4b400000
	v_perm_b32 v53, v54, v53, s33
	v_perm_b32 v55, v46, v55, s34
	v_or_b32_e32 v115, v53, v55
	s_waitcnt vmcnt(4)
	ds_read_b128 v[18:21], v38 offset:4096
	ds_read_b128 v[22:25], v38 offset:5120
	ds_read_b128 v[26:29], v38 offset:6144
	ds_read_b128 v[30:33], v38 offset:7168
	s_waitcnt lgkmcnt(0)
	s_mov_b32 m0, s36
	s_nop 0
	global_load_lds_dwordx4 v34, s[16:17] nt
	global_load_lds_dwordx4 v34, s[16:17] offset:1024 nt
	global_load_lds_dwordx4 v34, s[16:17] offset:2048 nt
	global_load_lds_dwordx4 v35, s[16:17] offset:3072 nt
	s_add_u32 s16, s16, 0x7d00
	s_addc_u32 s17, s17, 0
	v_cndmask_b32_e64 v30, 0, v30, s[18:19]
	v_cndmask_b32_e64 v31, 0, v31, s[18:19]
	v_cndmask_b32_e64 v32, 0, v32, s[18:19]
	v_cndmask_b32_e64 v33, 0, v33, s[18:19]
	v_max3_f32 v41, |v18|, |v19|, |v20|
	v_max3_f32 v42, |v21|, |v22|, |v23|
	v_max3_f32 v43, |v24|, |v25|, |v26|
	v_max3_f32 v44, |v27|, |v28|, |v29|
	v_max3_f32 v45, |v30|, |v31|, |v32|
	v_max3_f32 v41, v41, v42, |v33|
	v_max3_f32 v43, v43, v44, v45
	v_max_f32_e32 v41, v41, v43
	v_pk_add_f32 v[2:3], v[2:3], v[18:19]
	v_pk_add_f32 v[4:5], v[4:5], v[20:21]
	v_max_f32_dpp v41, v41, v41 quad_perm:[1,0,3,2] row_mask:0xf bank_mask:0xf
	v_pk_add_f32 v[6:7], v[6:7], v[22:23]
	v_pk_add_f32 v[8:9], v[8:9], v[24:25]
	v_max_f32_dpp v41, v41, v41 quad_perm:[2,3,0,1] row_mask:0xf bank_mask:0xf
	v_pk_add_f32 v[10:11], v[10:11], v[26:27]
	v_pk_add_f32 v[12:13], v[12:13], v[28:29]
	v_max_f32_dpp v41, v41, v41 row_half_mirror row_mask:0xf bank_mask:0xf
	v_pk_add_f32 v[14:15], v[14:15], v[30:31]
	v_pk_add_f32 v[16:17], v[16:17], v[32:33]
	v_max_f32_dpp v41, v41, v41 row_mirror row_mask:0xf bank_mask:0xf
	s_nop 1
	v_max_f32_dpp v41, v41, v41 row_bcast:15 row_mask:0xa bank_mask:0xf
	s_nop 1
	v_max_f32_dpp v41, v41, v41 row_bcast:31 row_mask:0xc bank_mask:0xf
	s_nop 1
	v_readlane_b32 s28, v41, 63
	s_nop 1
	v_div_scale_f32 v48, s[30:31], s28, s28, v47
	v_rcp_f32_e32 v49, v48
	s_nop 0
	v_fma_f32 v50, -v48, v49, 1.0
	v_fmac_f32_e32 v49, v50, v49
	v_mov_b32_e32 v50, s28
	v_div_scale_f32 v50, vcc, s32, v50, s32
	v_mul_f32_e32 v51, v50, v49
	v_fma_f32 v52, -v48, v51, v50
	v_fmac_f32_e32 v51, v52, v49
	v_fma_f32 v48, -v48, v51, v50
	v_div_fmas_f32 v48, v48, v49, v51
	v_div_fixup_f32 v48, v48, s28, v47
	v_cmp_gt_f32_e64 vcc, s28, 0
	v_writelane_b32 v40, s28, 15
	s_nop 0
	v_cndmask_b32_e32 v48, 0, v48, vcc
	v_fmaak_f32 v49, v18, v48, 0x4b400000
	v_fmaak_f32 v50, v19, v48, 0x4b400000
	v_fmaak_f32 v51, v20, v48, 0x4b400000
	v_fmaak_f32 v52, v21, v48, 0x4b400000
	v_perm_b32 v49, v50, v49, s33
	v_perm_b32 v51, v52, v51, s34
	v_or_b32_e32 v116, v49, v51
	v_fmaak_f32 v53, v22, v48, 0x4b400000
	v_fmaak_f32 v54, v23, v48, 0x4b400000
	v_fmaak_f32 v55, v24, v48, 0x4b400000
	v_fmaak_f32 v46, v25, v48, 0x4b400000
	v_perm_b32 v53, v54, v53, s33
	v_perm_b32 v55, v46, v55, s34
	v_or_b32_e32 v117, v53, v55
	v_fmaak_f32 v49, v26, v48, 0x4b400000
	v_fmaak_f32 v50, v27, v48, 0x4b400000
	v_fmaak_f32 v51, v28, v48, 0x4b400000
	v_fmaak_f32 v52, v29, v48, 0x4b400000
	v_perm_b32 v49, v50, v49, s33
	v_perm_b32 v51, v52, v51, s34
	v_or_b32_e32 v118, v49, v51
	v_fmaak_f32 v53, v30, v48, 0x4b400000
	v_fmaak_f32 v54, v31, v48, 0x4b400000
	v_fmaak_f32 v55, v32, v48, 0x4b400000
	v_fmaak_f32 v46, v33, v48, 0x4b400000
	v_perm_b32 v53, v54, v53, s33
	v_perm_b32 v55, v46, v55, s34
	v_or_b32_e32 v119, v53, v55
	s_waitcnt vmcnt(4)
	ds_read_b128 v[18:21], v38 offset:0
	ds_read_b128 v[22:25], v38 offset:1024
	ds_read_b128 v[26:29], v38 offset:2048
	ds_read_b128 v[30:33], v38 offset:3072
	s_waitcnt lgkmcnt(0)
	s_mov_b32 m0, s35
	s_nop 0
	global_load_lds_dwordx4 v34, s[16:17] nt
	global_load_lds_dwordx4 v34, s[16:17] offset:1024 nt
	global_load_lds_dwordx4 v34, s[16:17] offset:2048 nt
	global_load_lds_dwordx4 v35, s[16:17] offset:3072 nt
	s_add_u32 s16, s16, 0x7d00
	s_addc_u32 s17, s17, 0
	v_cndmask_b32_e64 v30, 0, v30, s[18:19]
	v_cndmask_b32_e64 v31, 0, v31, s[18:19]
	v_cndmask_b32_e64 v32, 0, v32, s[18:19]
	v_cndmask_b32_e64 v33, 0, v33, s[18:19]
	v_max3_f32 v41, |v18|, |v19|, |v20|
	v_max3_f32 v42, |v21|, |v22|, |v23|
	v_max3_f32 v43, |v24|, |v25|, |v26|
	v_max3_f32 v44, |v27|, |v28|, |v29|
	v_max3_f32 v45, |v30|, |v31|, |v32|
	v_max3_f32 v41, v41, v42, |v33|
	v_max3_f32 v43, v43, v44, v45
	v_max_f32_e32 v41, v41, v43
	v_pk_add_f32 v[2:3], v[2:3], v[18:19]
	v_pk_add_f32 v[4:5], v[4:5], v[20:21]
	v_max_f32_dpp v41, v41, v41 quad_perm:[1,0,3,2] row_mask:0xf bank_mask:0xf
	v_pk_add_f32 v[6:7], v[6:7], v[22:23]
	v_pk_add_f32 v[8:9], v[8:9], v[24:25]
	v_max_f32_dpp v41, v41, v41 quad_perm:[2,3,0,1] row_mask:0xf bank_mask:0xf
	v_pk_add_f32 v[10:11], v[10:11], v[26:27]
	v_pk_add_f32 v[12:13], v[12:13], v[28:29]
	v_max_f32_dpp v41, v41, v41 row_half_mirror row_mask:0xf bank_mask:0xf
	v_pk_add_f32 v[14:15], v[14:15], v[30:31]
	v_pk_add_f32 v[16:17], v[16:17], v[32:33]
	v_max_f32_dpp v41, v41, v41 row_mirror row_mask:0xf bank_mask:0xf
	s_nop 1
	v_max_f32_dpp v41, v41, v41 row_bcast:15 row_mask:0xa bank_mask:0xf
	s_nop 1
	v_max_f32_dpp v41, v41, v41 row_bcast:31 row_mask:0xc bank_mask:0xf
	s_nop 1
	v_readlane_b32 s28, v41, 63
	s_nop 1
	v_div_scale_f32 v48, s[30:31], s28, s28, v47
	v_rcp_f32_e32 v49, v48
	s_nop 0
	v_fma_f32 v50, -v48, v49, 1.0
	v_fmac_f32_e32 v49, v50, v49
	v_mov_b32_e32 v50, s28
	v_div_scale_f32 v50, vcc, s32, v50, s32
	v_mul_f32_e32 v51, v50, v49
	v_fma_f32 v52, -v48, v51, v50
	v_fmac_f32_e32 v51, v52, v49
	v_fma_f32 v48, -v48, v51, v50
	v_div_fmas_f32 v48, v48, v49, v51
	v_div_fixup_f32 v48, v48, s28, v47
	v_cmp_gt_f32_e64 vcc, s28, 0
	v_writelane_b32 v40, s28, 16
	s_nop 0
	v_cndmask_b32_e32 v48, 0, v48, vcc
	v_fmaak_f32 v49, v18, v48, 0x4b400000
	v_fmaak_f32 v50, v19, v48, 0x4b400000
	v_fmaak_f32 v51, v20, v48, 0x4b400000
	v_fmaak_f32 v52, v21, v48, 0x4b400000
	v_perm_b32 v49, v50, v49, s33
	v_perm_b32 v51, v52, v51, s34
	v_or_b32_e32 v120, v49, v51
	v_fmaak_f32 v53, v22, v48, 0x4b400000
	v_fmaak_f32 v54, v23, v48, 0x4b400000
	v_fmaak_f32 v55, v24, v48, 0x4b400000
	v_fmaak_f32 v46, v25, v48, 0x4b400000
	v_perm_b32 v53, v54, v53, s33
	v_perm_b32 v55, v46, v55, s34
	v_or_b32_e32 v121, v53, v55
	v_fmaak_f32 v49, v26, v48, 0x4b400000
	v_fmaak_f32 v50, v27, v48, 0x4b400000
	v_fmaak_f32 v51, v28, v48, 0x4b400000
	v_fmaak_f32 v52, v29, v48, 0x4b400000
	v_perm_b32 v49, v50, v49, s33
	v_perm_b32 v51, v52, v51, s34
	v_or_b32_e32 v122, v49, v51
	v_fmaak_f32 v53, v30, v48, 0x4b400000
	v_fmaak_f32 v54, v31, v48, 0x4b400000
	v_fmaak_f32 v55, v32, v48, 0x4b400000
	v_fmaak_f32 v46, v33, v48, 0x4b400000
	v_perm_b32 v53, v54, v53, s33
	v_perm_b32 v55, v46, v55, s34
	v_or_b32_e32 v123, v53, v55
	s_waitcnt vmcnt(4)
	ds_read_b128 v[18:21], v38 offset:4096
	ds_read_b128 v[22:25], v38 offset:5120
	ds_read_b128 v[26:29], v38 offset:6144
	ds_read_b128 v[30:33], v38 offset:7168
	s_waitcnt lgkmcnt(0)
	s_mov_b32 m0, s36
	s_nop 0
	global_load_lds_dwordx4 v34, s[16:17] nt
	global_load_lds_dwordx4 v34, s[16:17] offset:1024 nt
	global_load_lds_dwordx4 v34, s[16:17] offset:2048 nt
	global_load_lds_dwordx4 v35, s[16:17] offset:3072 nt
	s_add_u32 s16, s16, 0x7d00
	s_addc_u32 s17, s17, 0
	v_cndmask_b32_e64 v30, 0, v30, s[18:19]
	v_cndmask_b32_e64 v31, 0, v31, s[18:19]
	v_cndmask_b32_e64 v32, 0, v32, s[18:19]
	v_cndmask_b32_e64 v33, 0, v33, s[18:19]
	v_max3_f32 v41, |v18|, |v19|, |v20|
	v_max3_f32 v42, |v21|, |v22|, |v23|
	v_max3_f32 v43, |v24|, |v25|, |v26|
	v_max3_f32 v44, |v27|, |v28|, |v29|
	v_max3_f32 v45, |v30|, |v31|, |v32|
	v_max3_f32 v41, v41, v42, |v33|
	v_max3_f32 v43, v43, v44, v45
	v_max_f32_e32 v41, v41, v43
	v_pk_add_f32 v[2:3], v[2:3], v[18:19]
	v_pk_add_f32 v[4:5], v[4:5], v[20:21]
	v_max_f32_dpp v41, v41, v41 quad_perm:[1,0,3,2] row_mask:0xf bank_mask:0xf
	v_pk_add_f32 v[6:7], v[6:7], v[22:23]
	v_pk_add_f32 v[8:9], v[8:9], v[24:25]
	v_max_f32_dpp v41, v41, v41 quad_perm:[2,3,0,1] row_mask:0xf bank_mask:0xf
	v_pk_add_f32 v[10:11], v[10:11], v[26:27]
	v_pk_add_f32 v[12:13], v[12:13], v[28:29]
	v_max_f32_dpp v41, v41, v41 row_half_mirror row_mask:0xf bank_mask:0xf
	v_pk_add_f32 v[14:15], v[14:15], v[30:31]
	v_pk_add_f32 v[16:17], v[16:17], v[32:33]
	v_max_f32_dpp v41, v41, v41 row_mirror row_mask:0xf bank_mask:0xf
	s_nop 1
	v_max_f32_dpp v41, v41, v41 row_bcast:15 row_mask:0xa bank_mask:0xf
	s_nop 1
	v_max_f32_dpp v41, v41, v41 row_bcast:31 row_mask:0xc bank_mask:0xf
	s_nop 1
	v_readlane_b32 s28, v41, 63
	s_nop 1
	v_div_scale_f32 v48, s[30:31], s28, s28, v47
	v_rcp_f32_e32 v49, v48
	s_nop 0
	v_fma_f32 v50, -v48, v49, 1.0
	v_fmac_f32_e32 v49, v50, v49
	v_mov_b32_e32 v50, s28
	v_div_scale_f32 v50, vcc, s32, v50, s32
	v_mul_f32_e32 v51, v50, v49
	v_fma_f32 v52, -v48, v51, v50
	v_fmac_f32_e32 v51, v52, v49
	v_fma_f32 v48, -v48, v51, v50
	v_div_fmas_f32 v48, v48, v49, v51
	v_div_fixup_f32 v48, v48, s28, v47
	v_cmp_gt_f32_e64 vcc, s28, 0
	v_writelane_b32 v40, s28, 17
	s_nop 0
	v_cndmask_b32_e32 v48, 0, v48, vcc
	v_fmaak_f32 v49, v18, v48, 0x4b400000
	v_fmaak_f32 v50, v19, v48, 0x4b400000
	v_fmaak_f32 v51, v20, v48, 0x4b400000
	v_fmaak_f32 v52, v21, v48, 0x4b400000
	v_perm_b32 v49, v50, v49, s33
	v_perm_b32 v51, v52, v51, s34
	v_or_b32_e32 v124, v49, v51
	v_fmaak_f32 v53, v22, v48, 0x4b400000
	v_fmaak_f32 v54, v23, v48, 0x4b400000
	v_fmaak_f32 v55, v24, v48, 0x4b400000
	v_fmaak_f32 v46, v25, v48, 0x4b400000
	v_perm_b32 v53, v54, v53, s33
	v_perm_b32 v55, v46, v55, s34
	v_or_b32_e32 v125, v53, v55
	v_fmaak_f32 v49, v26, v48, 0x4b400000
	v_fmaak_f32 v50, v27, v48, 0x4b400000
	v_fmaak_f32 v51, v28, v48, 0x4b400000
	v_fmaak_f32 v52, v29, v48, 0x4b400000
	v_perm_b32 v49, v50, v49, s33
	v_perm_b32 v51, v52, v51, s34
	v_or_b32_e32 v126, v49, v51
	v_fmaak_f32 v53, v30, v48, 0x4b400000
	v_fmaak_f32 v54, v31, v48, 0x4b400000
	v_fmaak_f32 v55, v32, v48, 0x4b400000
	v_fmaak_f32 v46, v33, v48, 0x4b400000
	v_perm_b32 v53, v54, v53, s33
	v_perm_b32 v55, v46, v55, s34
	v_or_b32_e32 v127, v53, v55
	s_waitcnt vmcnt(4)
	ds_read_b128 v[18:21], v38 offset:0
	ds_read_b128 v[22:25], v38 offset:1024
	ds_read_b128 v[26:29], v38 offset:2048
	ds_read_b128 v[30:33], v38 offset:3072
	s_waitcnt lgkmcnt(0)
	s_mov_b32 m0, s35
	s_nop 0
	global_load_lds_dwordx4 v34, s[16:17] nt
	global_load_lds_dwordx4 v34, s[16:17] offset:1024 nt
	global_load_lds_dwordx4 v34, s[16:17] offset:2048 nt
	global_load_lds_dwordx4 v35, s[16:17] offset:3072 nt
	s_add_u32 s16, s16, 0x7d00
	s_addc_u32 s17, s17, 0
	v_cndmask_b32_e64 v30, 0, v30, s[18:19]
	v_cndmask_b32_e64 v31, 0, v31, s[18:19]
	v_cndmask_b32_e64 v32, 0, v32, s[18:19]
	v_cndmask_b32_e64 v33, 0, v33, s[18:19]
	v_max3_f32 v41, |v18|, |v19|, |v20|
	v_max3_f32 v42, |v21|, |v22|, |v23|
	v_max3_f32 v43, |v24|, |v25|, |v26|
	v_max3_f32 v44, |v27|, |v28|, |v29|
	v_max3_f32 v45, |v30|, |v31|, |v32|
	v_max3_f32 v41, v41, v42, |v33|
	v_max3_f32 v43, v43, v44, v45
	v_max_f32_e32 v41, v41, v43
	v_pk_add_f32 v[2:3], v[2:3], v[18:19]
	v_pk_add_f32 v[4:5], v[4:5], v[20:21]
	v_max_f32_dpp v41, v41, v41 quad_perm:[1,0,3,2] row_mask:0xf bank_mask:0xf
	v_pk_add_f32 v[6:7], v[6:7], v[22:23]
	v_pk_add_f32 v[8:9], v[8:9], v[24:25]
	v_max_f32_dpp v41, v41, v41 quad_perm:[2,3,0,1] row_mask:0xf bank_mask:0xf
	v_pk_add_f32 v[10:11], v[10:11], v[26:27]
	v_pk_add_f32 v[12:13], v[12:13], v[28:29]
	v_max_f32_dpp v41, v41, v41 row_half_mirror row_mask:0xf bank_mask:0xf
	v_pk_add_f32 v[14:15], v[14:15], v[30:31]
	v_pk_add_f32 v[16:17], v[16:17], v[32:33]
	v_max_f32_dpp v41, v41, v41 row_mirror row_mask:0xf bank_mask:0xf
	s_nop 1
	v_max_f32_dpp v41, v41, v41 row_bcast:15 row_mask:0xa bank_mask:0xf
	s_nop 1
	v_max_f32_dpp v41, v41, v41 row_bcast:31 row_mask:0xc bank_mask:0xf
	s_nop 1
	v_readlane_b32 s28, v41, 63
	s_nop 1
	v_div_scale_f32 v48, s[30:31], s28, s28, v47
	v_rcp_f32_e32 v49, v48
	s_nop 0
	v_fma_f32 v50, -v48, v49, 1.0
	v_fmac_f32_e32 v49, v50, v49
	v_mov_b32_e32 v50, s28
	v_div_scale_f32 v50, vcc, s32, v50, s32
	v_mul_f32_e32 v51, v50, v49
	v_fma_f32 v52, -v48, v51, v50
	v_fmac_f32_e32 v51, v52, v49
	v_fma_f32 v48, -v48, v51, v50
	v_div_fmas_f32 v48, v48, v49, v51
	v_div_fixup_f32 v48, v48, s28, v47
	v_cmp_gt_f32_e64 vcc, s28, 0
	v_writelane_b32 v40, s28, 18
	s_nop 0
	v_cndmask_b32_e32 v48, 0, v48, vcc
	v_fmaak_f32 v49, v18, v48, 0x4b400000
	v_fmaak_f32 v50, v19, v48, 0x4b400000
	v_fmaak_f32 v51, v20, v48, 0x4b400000
	v_fmaak_f32 v52, v21, v48, 0x4b400000
	v_perm_b32 v49, v50, v49, s33
	v_perm_b32 v51, v52, v51, s34
	v_or_b32_e32 v49, v49, v51
	global_store_dword v39, v49, s[20:21]
	v_fmaak_f32 v53, v22, v48, 0x4b400000
	v_fmaak_f32 v54, v23, v48, 0x4b400000
	v_fmaak_f32 v55, v24, v48, 0x4b400000
	v_fmaak_f32 v46, v25, v48, 0x4b400000
	v_perm_b32 v53, v54, v53, s33
	v_perm_b32 v55, v46, v55, s34
	v_or_b32_e32 v53, v53, v55
	global_store_dword v39, v53, s[22:23]
	v_fmaak_f32 v49, v26, v48, 0x4b400000
	v_fmaak_f32 v50, v27, v48, 0x4b400000
	v_fmaak_f32 v51, v28, v48, 0x4b400000
	v_fmaak_f32 v52, v29, v48, 0x4b400000
	v_perm_b32 v49, v50, v49, s33
	v_perm_b32 v51, v52, v51, s34
	v_or_b32_e32 v49, v49, v51
	global_store_dword v39, v49, s[24:25]
	v_fmaak_f32 v53, v30, v48, 0x4b400000
	v_fmaak_f32 v54, v31, v48, 0x4b400000
	v_fmaak_f32 v55, v32, v48, 0x4b400000
	v_fmaak_f32 v46, v33, v48, 0x4b400000
	v_perm_b32 v53, v54, v53, s33
	v_perm_b32 v55, v46, v55, s34
	v_or_b32_e32 v53, v53, v55
	global_store_dword v39, v53, s[26:27]
	s_add_u32 s20, s20, 0x400
	s_addc_u32 s21, s21, 0
	s_add_u32 s22, s22, 0x400
	s_addc_u32 s23, s23, 0
	s_add_u32 s24, s24, 0x400
	s_addc_u32 s25, s25, 0
	s_add_u32 s26, s26, 0x400
	s_addc_u32 s27, s27, 0
	s_waitcnt vmcnt(8)
	ds_read_b128 v[18:21], v38 offset:4096
	ds_read_b128 v[22:25], v38 offset:5120
	ds_read_b128 v[26:29], v38 offset:6144
	ds_read_b128 v[30:33], v38 offset:7168
	s_waitcnt lgkmcnt(0)
	s_mov_b32 m0, s36
	s_nop 0
	global_load_lds_dwordx4 v34, s[16:17] nt
	global_load_lds_dwordx4 v34, s[16:17] offset:1024 nt
	global_load_lds_dwordx4 v34, s[16:17] offset:2048 nt
	global_load_lds_dwordx4 v35, s[16:17] offset:3072 nt
	s_add_u32 s16, s16, 0x7d00
	s_addc_u32 s17, s17, 0
	v_cndmask_b32_e64 v30, 0, v30, s[18:19]
	v_cndmask_b32_e64 v31, 0, v31, s[18:19]
	v_cndmask_b32_e64 v32, 0, v32, s[18:19]
	v_cndmask_b32_e64 v33, 0, v33, s[18:19]
	v_max3_f32 v41, |v18|, |v19|, |v20|
	v_max3_f32 v42, |v21|, |v22|, |v23|
	v_max3_f32 v43, |v24|, |v25|, |v26|
	v_max3_f32 v44, |v27|, |v28|, |v29|
	v_max3_f32 v45, |v30|, |v31|, |v32|
	v_max3_f32 v41, v41, v42, |v33|
	v_max3_f32 v43, v43, v44, v45
	v_max_f32_e32 v41, v41, v43
	v_pk_add_f32 v[2:3], v[2:3], v[18:19]
	v_pk_add_f32 v[4:5], v[4:5], v[20:21]
	v_max_f32_dpp v41, v41, v41 quad_perm:[1,0,3,2] row_mask:0xf bank_mask:0xf
	v_pk_add_f32 v[6:7], v[6:7], v[22:23]
	v_pk_add_f32 v[8:9], v[8:9], v[24:25]
	v_max_f32_dpp v41, v41, v41 quad_perm:[2,3,0,1] row_mask:0xf bank_mask:0xf
	v_pk_add_f32 v[10:11], v[10:11], v[26:27]
	v_pk_add_f32 v[12:13], v[12:13], v[28:29]
	v_max_f32_dpp v41, v41, v41 row_half_mirror row_mask:0xf bank_mask:0xf
	v_pk_add_f32 v[14:15], v[14:15], v[30:31]
	v_pk_add_f32 v[16:17], v[16:17], v[32:33]
	v_max_f32_dpp v41, v41, v41 row_mirror row_mask:0xf bank_mask:0xf
	s_nop 1
	v_max_f32_dpp v41, v41, v41 row_bcast:15 row_mask:0xa bank_mask:0xf
	s_nop 1
	v_max_f32_dpp v41, v41, v41 row_bcast:31 row_mask:0xc bank_mask:0xf
	s_nop 1
	v_readlane_b32 s28, v41, 63
	s_nop 1
	v_div_scale_f32 v48, s[30:31], s28, s28, v47
	v_rcp_f32_e32 v49, v48
	s_nop 0
	v_fma_f32 v50, -v48, v49, 1.0
	v_fmac_f32_e32 v49, v50, v49
	v_mov_b32_e32 v50, s28
	v_div_scale_f32 v50, vcc, s32, v50, s32
	v_mul_f32_e32 v51, v50, v49
	v_fma_f32 v52, -v48, v51, v50
	v_fmac_f32_e32 v51, v52, v49
	v_fma_f32 v48, -v48, v51, v50
	v_div_fmas_f32 v48, v48, v49, v51
	v_div_fixup_f32 v48, v48, s28, v47
	v_cmp_gt_f32_e64 vcc, s28, 0
	v_writelane_b32 v40, s28, 19
	s_nop 0
	v_cndmask_b32_e32 v48, 0, v48, vcc
	v_fmaak_f32 v49, v18, v48, 0x4b400000
	v_fmaak_f32 v50, v19, v48, 0x4b400000
	v_fmaak_f32 v51, v20, v48, 0x4b400000
	v_fmaak_f32 v52, v21, v48, 0x4b400000
	v_perm_b32 v49, v50, v49, s33
	v_perm_b32 v51, v52, v51, s34
	v_or_b32_e32 v49, v49, v51
	global_store_dword v39, v49, s[20:21]
	v_fmaak_f32 v53, v22, v48, 0x4b400000
	v_fmaak_f32 v54, v23, v48, 0x4b400000
	v_fmaak_f32 v55, v24, v48, 0x4b400000
	v_fmaak_f32 v46, v25, v48, 0x4b400000
	v_perm_b32 v53, v54, v53, s33
	v_perm_b32 v55, v46, v55, s34
	v_or_b32_e32 v53, v53, v55
	global_store_dword v39, v53, s[22:23]
	v_fmaak_f32 v49, v26, v48, 0x4b400000
	v_fmaak_f32 v50, v27, v48, 0x4b400000
	v_fmaak_f32 v51, v28, v48, 0x4b400000
	v_fmaak_f32 v52, v29, v48, 0x4b400000
	v_perm_b32 v49, v50, v49, s33
	v_perm_b32 v51, v52, v51, s34
	v_or_b32_e32 v49, v49, v51
	global_store_dword v39, v49, s[24:25]
	v_fmaak_f32 v53, v30, v48, 0x4b400000
	v_fmaak_f32 v54, v31, v48, 0x4b400000
	v_fmaak_f32 v55, v32, v48, 0x4b400000
	v_fmaak_f32 v46, v33, v48, 0x4b400000
	v_perm_b32 v53, v54, v53, s33
	v_perm_b32 v55, v46, v55, s34
	v_or_b32_e32 v53, v53, v55
	global_store_dword v39, v53, s[26:27]
	s_add_u32 s20, s20, 0x400
	s_addc_u32 s21, s21, 0
	s_add_u32 s22, s22, 0x400
	s_addc_u32 s23, s23, 0
	s_add_u32 s24, s24, 0x400
	s_addc_u32 s25, s25, 0
	s_add_u32 s26, s26, 0x400
	s_addc_u32 s27, s27, 0
	s_waitcnt vmcnt(12)
	ds_read_b128 v[18:21], v38 offset:0
	ds_read_b128 v[22:25], v38 offset:1024
	ds_read_b128 v[26:29], v38 offset:2048
	ds_read_b128 v[30:33], v38 offset:3072
	s_waitcnt lgkmcnt(0)
	s_mov_b32 m0, s35
	s_nop 0
	global_load_lds_dwordx4 v34, s[16:17] nt
	global_load_lds_dwordx4 v34, s[16:17] offset:1024 nt
	global_load_lds_dwordx4 v34, s[16:17] offset:2048 nt
	global_load_lds_dwordx4 v35, s[16:17] offset:3072 nt
	s_add_u32 s16, s16, 0x7d00
	s_addc_u32 s17, s17, 0
	v_cndmask_b32_e64 v30, 0, v30, s[18:19]
	v_cndmask_b32_e64 v31, 0, v31, s[18:19]
	v_cndmask_b32_e64 v32, 0, v32, s[18:19]
	v_cndmask_b32_e64 v33, 0, v33, s[18:19]
	v_max3_f32 v41, |v18|, |v19|, |v20|
	v_max3_f32 v42, |v21|, |v22|, |v23|
	v_max3_f32 v43, |v24|, |v25|, |v26|
	v_max3_f32 v44, |v27|, |v28|, |v29|
	v_max3_f32 v45, |v30|, |v31|, |v32|
	v_max3_f32 v41, v41, v42, |v33|
	v_max3_f32 v43, v43, v44, v45
	v_max_f32_e32 v41, v41, v43
	v_pk_add_f32 v[2:3], v[2:3], v[18:19]
	v_pk_add_f32 v[4:5], v[4:5], v[20:21]
	v_max_f32_dpp v41, v41, v41 quad_perm:[1,0,3,2] row_mask:0xf bank_mask:0xf
	v_pk_add_f32 v[6:7], v[6:7], v[22:23]
	v_pk_add_f32 v[8:9], v[8:9], v[24:25]
	v_max_f32_dpp v41, v41, v41 quad_perm:[2,3,0,1] row_mask:0xf bank_mask:0xf
	v_pk_add_f32 v[10:11], v[10:11], v[26:27]
	v_pk_add_f32 v[12:13], v[12:13], v[28:29]
	v_max_f32_dpp v41, v41, v41 row_half_mirror row_mask:0xf bank_mask:0xf
	v_pk_add_f32 v[14:15], v[14:15], v[30:31]
	v_pk_add_f32 v[16:17], v[16:17], v[32:33]
	v_max_f32_dpp v41, v41, v41 row_mirror row_mask:0xf bank_mask:0xf
	s_nop 1
	v_max_f32_dpp v41, v41, v41 row_bcast:15 row_mask:0xa bank_mask:0xf
	s_nop 1
	v_max_f32_dpp v41, v41, v41 row_bcast:31 row_mask:0xc bank_mask:0xf
	s_nop 1
	v_readlane_b32 s28, v41, 63
	s_nop 1
	v_div_scale_f32 v48, s[30:31], s28, s28, v47
	v_rcp_f32_e32 v49, v48
	s_nop 0
	v_fma_f32 v50, -v48, v49, 1.0
	v_fmac_f32_e32 v49, v50, v49
	v_mov_b32_e32 v50, s28
	v_div_scale_f32 v50, vcc, s32, v50, s32
	v_mul_f32_e32 v51, v50, v49
	v_fma_f32 v52, -v48, v51, v50
	v_fmac_f32_e32 v51, v52, v49
	v_fma_f32 v48, -v48, v51, v50
	v_div_fmas_f32 v48, v48, v49, v51
	v_div_fixup_f32 v48, v48, s28, v47
	v_cmp_gt_f32_e64 vcc, s28, 0
	v_writelane_b32 v40, s28, 20
	s_nop 0
	v_cndmask_b32_e32 v48, 0, v48, vcc
	v_fmaak_f32 v49, v18, v48, 0x4b400000
	v_fmaak_f32 v50, v19, v48, 0x4b400000
	v_fmaak_f32 v51, v20, v48, 0x4b400000
	v_fmaak_f32 v52, v21, v48, 0x4b400000
	v_perm_b32 v49, v50, v49, s33
	v_perm_b32 v51, v52, v51, s34
	v_or_b32_e32 v49, v49, v51
	global_store_dword v39, v49, s[20:21]
	v_fmaak_f32 v53, v22, v48, 0x4b400000
	v_fmaak_f32 v54, v23, v48, 0x4b400000
	v_fmaak_f32 v55, v24, v48, 0x4b400000
	v_fmaak_f32 v46, v25, v48, 0x4b400000
	v_perm_b32 v53, v54, v53, s33
	v_perm_b32 v55, v46, v55, s34
	v_or_b32_e32 v53, v53, v55
	global_store_dword v39, v53, s[22:23]
	v_fmaak_f32 v49, v26, v48, 0x4b400000
	v_fmaak_f32 v50, v27, v48, 0x4b400000
	v_fmaak_f32 v51, v28, v48, 0x4b400000
	v_fmaak_f32 v52, v29, v48, 0x4b400000
	v_perm_b32 v49, v50, v49, s33
	v_perm_b32 v51, v52, v51, s34
	v_or_b32_e32 v49, v49, v51
	global_store_dword v39, v49, s[24:25]
	v_fmaak_f32 v53, v30, v48, 0x4b400000
	v_fmaak_f32 v54, v31, v48, 0x4b400000
	v_fmaak_f32 v55, v32, v48, 0x4b400000
	v_fmaak_f32 v46, v33, v48, 0x4b400000
	v_perm_b32 v53, v54, v53, s33
	v_perm_b32 v55, v46, v55, s34
	v_or_b32_e32 v53, v53, v55
	global_store_dword v39, v53, s[26:27]
	s_add_u32 s20, s20, 0x400
	s_addc_u32 s21, s21, 0
	s_add_u32 s22, s22, 0x400
	s_addc_u32 s23, s23, 0
	s_add_u32 s24, s24, 0x400
	s_addc_u32 s25, s25, 0
	s_add_u32 s26, s26, 0x400
	s_addc_u32 s27, s27, 0
	s_waitcnt vmcnt(12)
	ds_read_b128 v[18:21], v38 offset:4096
	ds_read_b128 v[22:25], v38 offset:5120
	ds_read_b128 v[26:29], v38 offset:6144
	ds_read_b128 v[30:33], v38 offset:7168
	s_waitcnt lgkmcnt(0)
	s_mov_b32 m0, s36
	s_nop 0
	global_load_lds_dwordx4 v34, s[16:17] nt
	global_load_lds_dwordx4 v34, s[16:17] offset:1024 nt
	global_load_lds_dwordx4 v34, s[16:17] offset:2048 nt
	global_load_lds_dwordx4 v35, s[16:17] offset:3072 nt
	s_add_u32 s16, s16, 0x7d00
	s_addc_u32 s17, s17, 0
	v_cndmask_b32_e64 v30, 0, v30, s[18:19]
	v_cndmask_b32_e64 v31, 0, v31, s[18:19]
	v_cndmask_b32_e64 v32, 0, v32, s[18:19]
	v_cndmask_b32_e64 v33, 0, v33, s[18:19]
	v_max3_f32 v41, |v18|, |v19|, |v20|
	v_max3_f32 v42, |v21|, |v22|, |v23|
	v_max3_f32 v43, |v24|, |v25|, |v26|
	v_max3_f32 v44, |v27|, |v28|, |v29|
	v_max3_f32 v45, |v30|, |v31|, |v32|
	v_max3_f32 v41, v41, v42, |v33|
	v_max3_f32 v43, v43, v44, v45
	v_max_f32_e32 v41, v41, v43
	v_pk_add_f32 v[2:3], v[2:3], v[18:19]
	v_pk_add_f32 v[4:5], v[4:5], v[20:21]
	v_max_f32_dpp v41, v41, v41 quad_perm:[1,0,3,2] row_mask:0xf bank_mask:0xf
	v_pk_add_f32 v[6:7], v[6:7], v[22:23]
	v_pk_add_f32 v[8:9], v[8:9], v[24:25]
	v_max_f32_dpp v41, v41, v41 quad_perm:[2,3,0,1] row_mask:0xf bank_mask:0xf
	v_pk_add_f32 v[10:11], v[10:11], v[26:27]
	v_pk_add_f32 v[12:13], v[12:13], v[28:29]
	v_max_f32_dpp v41, v41, v41 row_half_mirror row_mask:0xf bank_mask:0xf
	v_pk_add_f32 v[14:15], v[14:15], v[30:31]
	v_pk_add_f32 v[16:17], v[16:17], v[32:33]
	v_max_f32_dpp v41, v41, v41 row_mirror row_mask:0xf bank_mask:0xf
	s_nop 1
	v_max_f32_dpp v41, v41, v41 row_bcast:15 row_mask:0xa bank_mask:0xf
	s_nop 1
	v_max_f32_dpp v41, v41, v41 row_bcast:31 row_mask:0xc bank_mask:0xf
	s_nop 1
	v_readlane_b32 s28, v41, 63
	s_nop 1
	v_div_scale_f32 v48, s[30:31], s28, s28, v47
	v_rcp_f32_e32 v49, v48
	s_nop 0
	v_fma_f32 v50, -v48, v49, 1.0
	v_fmac_f32_e32 v49, v50, v49
	v_mov_b32_e32 v50, s28
	v_div_scale_f32 v50, vcc, s32, v50, s32
	v_mul_f32_e32 v51, v50, v49
	v_fma_f32 v52, -v48, v51, v50
	v_fmac_f32_e32 v51, v52, v49
	v_fma_f32 v48, -v48, v51, v50
	v_div_fmas_f32 v48, v48, v49, v51
	v_div_fixup_f32 v48, v48, s28, v47
	v_cmp_gt_f32_e64 vcc, s28, 0
	v_writelane_b32 v40, s28, 21
	s_nop 0
	v_cndmask_b32_e32 v48, 0, v48, vcc
	v_fmaak_f32 v49, v18, v48, 0x4b400000
	v_fmaak_f32 v50, v19, v48, 0x4b400000
	v_fmaak_f32 v51, v20, v48, 0x4b400000
	v_fmaak_f32 v52, v21, v48, 0x4b400000
	v_perm_b32 v49, v50, v49, s33
	v_perm_b32 v51, v52, v51, s34
	v_or_b32_e32 v49, v49, v51
	global_store_dword v39, v49, s[20:21]
	v_fmaak_f32 v53, v22, v48, 0x4b400000
	v_fmaak_f32 v54, v23, v48, 0x4b400000
	v_fmaak_f32 v55, v24, v48, 0x4b400000
	v_fmaak_f32 v46, v25, v48, 0x4b400000
	v_perm_b32 v53, v54, v53, s33
	v_perm_b32 v55, v46, v55, s34
	v_or_b32_e32 v53, v53, v55
	global_store_dword v39, v53, s[22:23]
	v_fmaak_f32 v49, v26, v48, 0x4b400000
	v_fmaak_f32 v50, v27, v48, 0x4b400000
	v_fmaak_f32 v51, v28, v48, 0x4b400000
	v_fmaak_f32 v52, v29, v48, 0x4b400000
	v_perm_b32 v49, v50, v49, s33
	v_perm_b32 v51, v52, v51, s34
	v_or_b32_e32 v49, v49, v51
	global_store_dword v39, v49, s[24:25]
	v_fmaak_f32 v53, v30, v48, 0x4b400000
	v_fmaak_f32 v54, v31, v48, 0x4b400000
	v_fmaak_f32 v55, v32, v48, 0x4b400000
	v_fmaak_f32 v46, v33, v48, 0x4b400000
	v_perm_b32 v53, v54, v53, s33
	v_perm_b32 v55, v46, v55, s34
	v_or_b32_e32 v53, v53, v55
	global_store_dword v39, v53, s[26:27]
	s_add_u32 s20, s20, 0x400
	s_addc_u32 s21, s21, 0
	s_add_u32 s22, s22, 0x400
	s_addc_u32 s23, s23, 0
	s_add_u32 s24, s24, 0x400
	s_addc_u32 s25, s25, 0
	s_add_u32 s26, s26, 0x400
	s_addc_u32 s27, s27, 0
	s_waitcnt vmcnt(12)
	ds_read_b128 v[18:21], v38 offset:0
	ds_read_b128 v[22:25], v38 offset:1024
	ds_read_b128 v[26:29], v38 offset:2048
	ds_read_b128 v[30:33], v38 offset:3072
	s_waitcnt lgkmcnt(0)
	s_cmp_eq_u32 s29, 1
	s_cbranch_scc0 .Lk1_nodma24
	s_mov_b32 m0, s35
	s_nop 0
	global_load_lds_dwordx4 v34, s[16:17] nt
	global_load_lds_dwordx4 v34, s[16:17] offset:1024 nt
	global_load_lds_dwordx4 v34, s[16:17] offset:2048 nt
	global_load_lds_dwordx4 v35, s[16:17] offset:3072 nt
	s_add_u32 s16, s16, 0x7d00
	s_addc_u32 s17, s17, 0

.Lk1_flush:
	s_mov_b64 s[20:21], s[40:41]
	s_add_u32 s22, s20, 0x186a000
	s_addc_u32 s23, s21, 0
	s_add_u32 s24, s22, 0x186a000
	s_addc_u32 s25, s23, 0
	s_add_u32 s26, s24, 0x186a000
	s_addc_u32 s27, s25, 0
	global_store_dword v39, v56, s[20:21]
	global_store_dword v39, v57, s[22:23]
	global_store_dword v39, v58, s[24:25]
	global_store_dword v39, v59, s[26:27]
	global_store_dword v39, v60, s[20:21] offset:1024
	global_store_dword v39, v61, s[22:23] offset:1024
	global_store_dword v39, v62, s[24:25] offset:1024
	global_store_dword v39, v63, s[26:27] offset:1024
	global_store_dword v39, v64, s[20:21] offset:2048
	global_store_dword v39, v65, s[22:23] offset:2048
	global_store_dword v39, v66, s[24:25] offset:2048
	global_store_dword v39, v67, s[26:27] offset:2048
	global_store_dword v39, v68, s[20:21] offset:3072
	global_store_dword v39, v69, s[22:23] offset:3072
	global_store_dword v39, v70, s[24:25] offset:3072
	global_store_dword v39, v71, s[26:27] offset:3072
	s_add_u32 s20, s20, 0x1000
	s_addc_u32 s21, s21, 0
	s_add_u32 s22, s22, 0x1000
	s_addc_u32 s23, s23, 0
	s_add_u32 s24, s24, 0x1000
	s_addc_u32 s25, s25, 0
	s_add_u32 s26, s26, 0x1000
	s_addc_u32 s27, s27, 0
	global_store_dword v39, v72, s[20:21]
	global_store_dword v39, v73, s[22:23]
	global_store_dword v39, v74, s[24:25]
	global_store_dword v39, v75, s[26:27]
	global_store_dword v39, v76, s[20:21] offset:1024
	global_store_dword v39, v77, s[22:23] offset:1024
	global_store_dword v39, v78, s[24:25] offset:1024
	global_store_dword v39, v79, s[26:27] offset:1024
	global_store_dword v39, v80, s[20:21] offset:2048
	global_store_dword v39, v81, s[22:23] offset:2048
	global_store_dword v39, v82, s[24:25] offset:2048
	global_store_dword v39, v83, s[26:27] offset:2048
	global_store_dword v39, v84, s[20:21] offset:3072
	global_store_dword v39, v85, s[22:23] offset:3072
	global_store_dword v39, v86, s[24:25] offset:3072
	global_store_dword v39, v87, s[26:27] offset:3072
	s_add_u32 s20, s20, 0x1000
	s_addc_u32 s21, s21, 0
	s_add_u32 s22, s22, 0x1000
	s_addc_u32 s23, s23, 0
	s_add_u32 s24, s24, 0x1000
	s_addc_u32 s25, s25, 0
	s_add_u32 s26, s26, 0x1000
	s_addc_u32 s27, s27, 0
	global_store_dword v39, v88, s[20:21]
	global_store_dword v39, v89, s[22:23]
	global_store_dword v39, v90, s[24:25]
	global_store_dword v39, v91, s[26:27]
	global_store_dword v39, v92, s[20:21] offset:1024
	global_store_dword v39, v93, s[22:23] offset:1024
	global_store_dword v39, v94, s[24:25] offset:1024
	global_store_dword v39, v95, s[26:27] offset:1024
	global_store_dword v39, v96, s[20:21] offset:2048
	global_store_dword v39, v97, s[22:23] offset:2048
	global_store_dword v39, v98, s[24:25] offset:2048
	global_store_dword v39, v99, s[26:27] offset:2048
	global_store_dword v39, v100, s[20:21] offset:3072
	global_store_dword v39, v101, s[22:23] offset:3072
	global_store_dword v39, v102, s[24:25] offset:3072
	global_store_dword v39, v103, s[26:27] offset:3072
	s_add_u32 s20, s20, 0x1000
	s_addc_u32 s21, s21, 0
	s_add_u32 s22, s22, 0x1000
	s_addc_u32 s23, s23, 0
	s_add_u32 s24, s24, 0x1000
	s_addc_u32 s25, s25, 0
	s_add_u32 s26, s26, 0x1000
	s_addc_u32 s27, s27, 0
	global_store_dword v39, v104, s[20:21]
	global_store_dword v39, v105, s[22:23]
	global_store_dword v39, v106, s[24:25]
	global_store_dword v39, v107, s[26:27]
	global_store_dword v39, v108, s[20:21] offset:1024
	global_store_dword v39, v109, s[22:23] offset:1024
	global_store_dword v39, v110, s[24:25] offset:1024
	global_store_dword v39, v111, s[26:27] offset:1024
	global_store_dword v39, v112, s[20:21] offset:2048
	global_store_dword v39, v113, s[22:23] offset:2048
	global_store_dword v39, v114, s[24:25] offset:2048
	global_store_dword v39, v115, s[26:27] offset:2048
	global_store_dword v39, v116, s[20:21] offset:3072
	global_store_dword v39, v117, s[22:23] offset:3072
	global_store_dword v39, v118, s[24:25] offset:3072
	global_store_dword v39, v119, s[26:27] offset:3072
	s_add_u32 s20, s20, 0x1000
	s_addc_u32 s21, s21, 0
	s_add_u32 s22, s22, 0x1000
	s_addc_u32 s23, s23, 0
	s_add_u32 s24, s24, 0x1000
	s_addc_u32 s25, s25, 0
	s_add_u32 s26, s26, 0x1000
	s_addc_u32 s27, s27, 0
	global_store_dword v39, v120, s[20:21]
	global_store_dword v39, v121, s[22:23]
	global_store_dword v39, v122, s[24:25]
	global_store_dword v39, v123, s[26:27]
	global_store_dword v39, v124, s[20:21] offset:1024
	global_store_dword v39, v125, s[22:23] offset:1024
	global_store_dword v39, v126, s[24:25] offset:1024
	global_store_dword v39, v127, s[26:27] offset:1024
	v_mul_f32_e32 v40, 0x3c010204, v40
	v_lshlrev_b32_e32 v41, 5, v1
	s_add_u32 s15, s12, s14
	s_lshl_b32 s15, s15, 2
	s_add_u32 s8, s8, s15
	s_addc_u32 s9, s9, 0
	s_add_u32 s15, s29, 24
	v_cmp_gt_u32_e32 vcc, s15, v1
	s_and_saveexec_b64 s[38:39], vcc
	global_store_dword v41, v40, s[8:9]
	s_mov_b64 exec, s[38:39]
	s_lshl_b32 s15, s14, 12
	v_add_u32_e32 v41, s15, v34
	s_barrier
	ds_write_b128 v41, v[2:5]
	ds_write_b128 v41, v[6:9] offset:1024
	ds_write_b128 v41, v[10:13] offset:2048
	ds_write_b128 v41, v[14:17] offset:3072
	s_waitcnt lgkmcnt(0)
	s_barrier
	s_movk_i32 s15, 0x100
	v_cmp_gt_u32_e32 vcc, s15, v0
	s_and_saveexec_b64 s[38:39], vcc
	s_cbranch_execz .Lk1_end
	v_lshlrev_b32_e32 v16, 4, v0
	ds_read_b128 v[2:5], v16
	ds_read_b128 v[18:21], v16 offset:4096
	ds_read_b128 v[22:25], v16 offset:8192
	ds_read_b128 v[26:29], v16 offset:12288
	ds_read_b128 v[30:33], v16 offset:16384
	ds_read_b128 v[34:37], v16 offset:20480
	ds_read_b128 v[38:41], v16 offset:24576
	ds_read_b128 v[42:45], v16 offset:28672
	s_waitcnt lgkmcnt(6)
	v_pk_add_f32 v[2:3], v[2:3], v[18:19]
	v_pk_add_f32 v[4:5], v[4:5], v[20:21]
	s_waitcnt lgkmcnt(5)
	v_pk_add_f32 v[2:3], v[2:3], v[22:23]
	v_pk_add_f32 v[4:5], v[4:5], v[24:25]
	s_waitcnt lgkmcnt(4)
	v_pk_add_f32 v[2:3], v[2:3], v[26:27]
	v_pk_add_f32 v[4:5], v[4:5], v[28:29]
	s_waitcnt lgkmcnt(3)
	v_pk_add_f32 v[2:3], v[2:3], v[30:31]
	v_pk_add_f32 v[4:5], v[4:5], v[32:33]
	s_waitcnt lgkmcnt(2)
	v_pk_add_f32 v[2:3], v[2:3], v[34:35]
	v_pk_add_f32 v[4:5], v[4:5], v[36:37]
	s_waitcnt lgkmcnt(1)
	v_pk_add_f32 v[2:3], v[2:3], v[38:39]
	v_pk_add_f32 v[4:5], v[4:5], v[40:41]
	s_waitcnt lgkmcnt(0)
	v_pk_add_f32 v[2:3], v[2:3], v[42:43]
	v_pk_add_f32 v[4:5], v[4:5], v[44:45]
	s_lshl_b32 s15, s2, 12
	s_add_u32 s10, s10, s15
	s_addc_u32 s11, s11, 0
	global_store_dwordx4 v16, v[2:5], s[10:11]

_Z15k3_pairs_slicedPKDv4_jPKfPKiS5_PiPf:
	s_load_dwordx8 s[4:11], s[0:1], 0x0
	s_lshl_b32 s3, s2, 7
	v_lshlrev_b32_e32 v2, 2, v0
	s_and_b32 s3, s3, 0x7ffffc00
	v_and_b32_e32 v2, 0x300, v2
	v_and_b32_e32 v1, 63, v0
	v_or_b32_e32 v54, s3, v2
	v_or_b32_e32 v40, v54, v1
	v_mov_b32_e32 v41, 0
	v_lshlrev_b64 v[4:5], 2, v[40:41]
	s_waitcnt lgkmcnt(0)
	v_lshl_add_u64 v[2:3], s[8:9], 0, v[4:5]
	global_load_dword v52, v[2:3], off nt
	v_lshl_add_u64 v[4:5], s[10:11], 0, v[4:5]
	global_load_dword v53, v[4:5], off nt
	v_bfe_u32 v55, v0, 3, 3
	v_lshlrev_b32_e32 v44, 2, v55
	s_and_b32 s8, s2, 7
	v_and_b32_e32 v51, 7, v0
	s_lshl_b32 s2, s8, 9
	global_load_dword v50, v[2:3], off offset:256 nt
	global_load_dword v48, v[2:3], off offset:512 nt
	global_load_dword v45, v[2:3], off offset:768 nt
	global_load_dword v49, v[4:5], off offset:256 nt
	global_load_dword v47, v[4:5], off offset:512 nt
	global_load_dword v46, v[4:5], off offset:768 nt
	s_add_u32 s2, s6, s2
	s_mul_i32 s8, s8, 0xc35000
	s_addc_u32 s3, s7, 0
	s_add_u32 s4, s4, s8
	v_lshlrev_b32_e32 v40, 4, v51
	s_addc_u32 s5, s5, 0
	v_lshl_add_u64 v[42:43], s[4:5], 0, v[40:41]
	v_lshlrev_b32_e32 v40, 6, v51
	v_lshlrev_b32_e32 v56, 3, v51
	v_mov_b32_e32 v63, v41
	v_mov_b32_e32 v72, v41
	v_mov_b32_e32 v73, v41
	v_cmp_eq_u32_e32 vcc, 0, v51
	s_load_dwordx4 s[16:19], s[0:1], 0x20
	v_cmp_eq_u32_e64 s[0:1], 1, v51
	v_cmp_eq_u32_e64 s[4:5], 3, v51
	v_cmp_eq_u32_e64 s[6:7], 4, v51
	v_cmp_eq_u32_e64 s[8:9], 5, v51
	v_cmp_eq_u32_e64 s[10:11], 6, v51
	v_cmp_eq_u32_e64 s[12:13], 7, v51
	s_waitcnt vmcnt(7)
	ds_bpermute_b32 v0, v44, v52
	ds_bpermute_b32 v58, v44, v52 offset:128
	s_waitcnt vmcnt(6)
	ds_bpermute_b32 v2, v44, v53
	ds_bpermute_b32 v60, v44, v53 offset:128
	ds_bpermute_b32 v62, v44, v52 offset:160
	s_waitcnt lgkmcnt(0)
	v_ashrrev_i32_e32 v1, 31, v0
	v_lshlrev_b64 v[0:1], 7, v[0:1]
	v_ashrrev_i32_e32 v3, 31, v2
	v_lshlrev_b64 v[2:3], 7, v[2:3]
	v_lshl_add_u64 v[0:1], v[42:43], 0, v[0:1]
	v_lshl_add_u64 v[2:3], v[42:43], 0, v[2:3]
	global_load_dwordx4 v[28:31], v[0:1], off
	global_load_dwordx4 v[32:35], v[2:3], off
	ds_bpermute_b32 v0, v44, v52 offset:32
	ds_bpermute_b32 v2, v44, v53 offset:32
	v_ashrrev_i32_e32 v59, 31, v58
	v_ashrrev_i32_e32 v61, 31, v60
	v_lshlrev_b64 v[58:59], 7, v[58:59]
	s_waitcnt lgkmcnt(1)
	v_ashrrev_i32_e32 v1, 31, v0
	s_waitcnt lgkmcnt(0)
	v_ashrrev_i32_e32 v3, 31, v2
	v_lshlrev_b64 v[0:1], 7, v[0:1]
	v_lshlrev_b64 v[2:3], 7, v[2:3]
	v_lshl_add_u64 v[0:1], v[42:43], 0, v[0:1]
	v_lshl_add_u64 v[2:3], v[42:43], 0, v[2:3]
	global_load_dwordx4 v[20:23], v[0:1], off
	global_load_dwordx4 v[36:39], v[2:3], off
	ds_bpermute_b32 v0, v44, v52 offset:64
	ds_bpermute_b32 v2, v44, v53 offset:64
	v_lshlrev_b64 v[60:61], 7, v[60:61]
	v_lshl_add_u64 v[68:69], v[42:43], 0, v[58:59]
	v_lshl_add_u64 v[70:71], v[42:43], 0, v[60:61]
	s_waitcnt lgkmcnt(1)
	v_ashrrev_i32_e32 v1, 31, v0
	s_waitcnt lgkmcnt(0)
	v_ashrrev_i32_e32 v3, 31, v2
	v_lshlrev_b64 v[0:1], 7, v[0:1]
	v_lshlrev_b64 v[2:3], 7, v[2:3]
	v_lshl_add_u64 v[0:1], v[42:43], 0, v[0:1]
	v_lshl_add_u64 v[2:3], v[42:43], 0, v[2:3]
	global_load_dwordx4 v[16:19], v[0:1], off
	global_load_dwordx4 v[24:27], v[2:3], off
	global_load_dwordx4 v[8:11], v40, s[2:3] offset:16
	s_waitcnt vmcnt(6)
	v_cvt_f32_i32_sdwa v74, sext(v29) dst_sel:DWORD dst_unused:UNUSED_PAD src0_sel:BYTE_1
	global_load_dwordx4 v[0:3], v40, s[2:3]
	global_load_dwordx4 v[12:15], v40, s[2:3] offset:32
	global_load_dwordx4 v[4:7], v40, s[2:3] offset:48
	v_or3_b32 v40, v56, v54, v55
	ds_bpermute_b32 v54, v44, v52 offset:96
	ds_bpermute_b32 v56, v44, v53 offset:96
	s_waitcnt vmcnt(8)
	v_dot4c_i32_i8_e32 v63, v28, v32
	v_dot4c_i32_i8_e32 v63, v29, v33
	v_dot4c_i32_i8_e32 v63, v30, v34
	s_waitcnt lgkmcnt(1)
	v_ashrrev_i32_e32 v55, 31, v54
	s_waitcnt lgkmcnt(0)
	v_ashrrev_i32_e32 v57, 31, v56
	v_lshlrev_b64 v[54:55], 7, v[54:55]
	v_lshlrev_b64 v[56:57], 7, v[56:57]
	v_lshl_add_u64 v[64:65], v[42:43], 0, v[54:55]
	v_lshl_add_u64 v[66:67], v[42:43], 0, v[56:57]
	global_load_dwordx4 v[54:57], v[64:65], off
	global_load_dwordx4 v[58:61], v[66:67], off
	s_waitcnt vmcnt(8)
	v_dot4c_i32_i8_e32 v72, v20, v36
	v_dot4c_i32_i8_e32 v72, v21, v37
	v_dot4c_i32_i8_e32 v72, v22, v38
	v_cvt_f32_i32_sdwa v32, sext(v28) dst_sel:DWORD dst_unused:UNUSED_PAD src0_sel:BYTE_0
	v_cvt_f32_i32_sdwa v64, sext(v29) dst_sel:DWORD dst_unused:UNUSED_PAD src0_sel:BYTE_0
	v_cvt_f32_i32_sdwa v65, sext(v30) dst_sel:DWORD dst_unused:UNUSED_PAD src0_sel:BYTE_0
	v_cvt_f32_i32_sdwa v66, sext(v31) dst_sel:DWORD dst_unused:UNUSED_PAD src0_sel:BYTE_0
	v_cvt_f32_i32_sdwa v67, sext(v28) dst_sel:DWORD dst_unused:UNUSED_PAD src0_sel:BYTE_1
	v_cvt_f32_i32_sdwa v75, sext(v30) dst_sel:DWORD dst_unused:UNUSED_PAD src0_sel:BYTE_1
	v_cvt_f32_i32_sdwa v76, sext(v31) dst_sel:DWORD dst_unused:UNUSED_PAD src0_sel:BYTE_1
	v_cvt_f32_i32_sdwa v77, sext(v28) dst_sel:DWORD dst_unused:UNUSED_PAD src0_sel:BYTE_2
	v_cvt_f32_i32_sdwa v78, sext(v29) dst_sel:DWORD dst_unused:UNUSED_PAD src0_sel:BYTE_2
	v_cvt_f32_i32_sdwa v79, sext(v30) dst_sel:DWORD dst_unused:UNUSED_PAD src0_sel:BYTE_2
	v_cvt_f32_i32_sdwa v80, sext(v31) dst_sel:DWORD dst_unused:UNUSED_PAD src0_sel:BYTE_2
	v_cvt_f32_i32_sdwa v81, sext(v28) dst_sel:DWORD dst_unused:UNUSED_PAD src0_sel:BYTE_3
	v_cvt_f32_i32_sdwa v82, sext(v29) dst_sel:DWORD dst_unused:UNUSED_PAD src0_sel:BYTE_3
	v_cvt_f32_i32_sdwa v83, sext(v30) dst_sel:DWORD dst_unused:UNUSED_PAD src0_sel:BYTE_3
	v_cvt_f32_i32_sdwa v84, sext(v31) dst_sel:DWORD dst_unused:UNUSED_PAD src0_sel:BYTE_3
	v_cvt_f32_i32_sdwa v36, sext(v20) dst_sel:DWORD dst_unused:UNUSED_PAD src0_sel:BYTE_0
	v_cvt_f32_i32_sdwa v85, sext(v21) dst_sel:DWORD dst_unused:UNUSED_PAD src0_sel:BYTE_0
	v_cvt_f32_i32_sdwa v86, sext(v22) dst_sel:DWORD dst_unused:UNUSED_PAD src0_sel:BYTE_0
	v_cvt_f32_i32_sdwa v87, sext(v23) dst_sel:DWORD dst_unused:UNUSED_PAD src0_sel:BYTE_0
	v_cvt_f32_i32_sdwa v88, sext(v20) dst_sel:DWORD dst_unused:UNUSED_PAD src0_sel:BYTE_1
	v_dot4c_i32_i8_e32 v63, v31, v35
	v_cvt_f32_i32_sdwa v33, sext(v21) dst_sel:DWORD dst_unused:UNUSED_PAD src0_sel:BYTE_1
	v_cvt_f32_i32_sdwa v34, sext(v22) dst_sel:DWORD dst_unused:UNUSED_PAD src0_sel:BYTE_1
	v_cvt_f32_i32_sdwa v35, sext(v23) dst_sel:DWORD dst_unused:UNUSED_PAD src0_sel:BYTE_1
	v_cvt_f32_i32_sdwa v89, sext(v20) dst_sel:DWORD dst_unused:UNUSED_PAD src0_sel:BYTE_2
	v_cvt_f32_i32_sdwa v90, sext(v21) dst_sel:DWORD dst_unused:UNUSED_PAD src0_sel:BYTE_2
	v_cvt_f32_i32_sdwa v91, sext(v22) dst_sel:DWORD dst_unused:UNUSED_PAD src0_sel:BYTE_2
	v_cvt_f32_i32_sdwa v92, sext(v23) dst_sel:DWORD dst_unused:UNUSED_PAD src0_sel:BYTE_2
	v_cvt_f32_i32_sdwa v93, sext(v20) dst_sel:DWORD dst_unused:UNUSED_PAD src0_sel:BYTE_3
	v_dot4c_i32_i8_e32 v72, v23, v39
	v_cvt_f32_i32_sdwa v37, sext(v21) dst_sel:DWORD dst_unused:UNUSED_PAD src0_sel:BYTE_3
	v_cvt_f32_i32_sdwa v38, sext(v22) dst_sel:DWORD dst_unused:UNUSED_PAD src0_sel:BYTE_3
	v_cvt_f32_i32_sdwa v39, sext(v23) dst_sel:DWORD dst_unused:UNUSED_PAD src0_sel:BYTE_3
	global_load_dwordx4 v[20:23], v[68:69], off
	global_load_dwordx4 v[28:31], v[70:71], off
	s_waitcnt vmcnt(8)
	v_dot4c_i32_i8_e32 v73, v16, v24
	v_cvt_f32_i32_sdwa v24, sext(v16) dst_sel:DWORD dst_unused:UNUSED_PAD src0_sel:BYTE_0
	v_dot4c_i32_i8_e32 v73, v17, v25
	v_cvt_f32_i32_sdwa v25, sext(v17) dst_sel:DWORD dst_unused:UNUSED_PAD src0_sel:BYTE_0
	v_dot4c_i32_i8_e32 v73, v18, v26
	v_cvt_f32_i32_sdwa v26, sext(v18) dst_sel:DWORD dst_unused:UNUSED_PAD src0_sel:BYTE_0
	v_dot4c_i32_i8_e32 v73, v19, v27
	v_cvt_f32_i32_sdwa v27, sext(v19) dst_sel:DWORD dst_unused:UNUSED_PAD src0_sel:BYTE_0
	v_cvt_f32_i32_sdwa v68, sext(v16) dst_sel:DWORD dst_unused:UNUSED_PAD src0_sel:BYTE_1
	v_cmp_eq_u32_e64 s[2:3], 2, v51
	v_mov_b32_e32 v70, v41
	s_waitcnt vmcnt(6)
	v_fma_f32 v32, v32, v0, 0
	v_fma_f32 v36, v36, v0, 0
	v_fmac_f32_e32 v32, v64, v8
	v_fmac_f32_e32 v36, v85, v8
	s_waitcnt vmcnt(5)
	v_fmac_f32_e32 v32, v65, v12
	v_fmac_f32_e32 v36, v86, v12
	s_waitcnt vmcnt(4)
	v_fmac_f32_e32 v32, v66, v4
	v_fmac_f32_e32 v36, v87, v4
	v_fmac_f32_e32 v32, v67, v1
	v_fmac_f32_e32 v36, v88, v1
	v_fmac_f32_e32 v32, v74, v9
	v_fmac_f32_e32 v36, v33, v9
	v_fmac_f32_e32 v32, v75, v13
	v_fmac_f32_e32 v36, v34, v13
	v_fmac_f32_e32 v32, v76, v5
	v_fmac_f32_e32 v36, v35, v5
	v_fmac_f32_e32 v32, v77, v2
	v_fmac_f32_e32 v36, v89, v2
	v_fmac_f32_e32 v32, v78, v10
	v_fmac_f32_e32 v36, v90, v10
	v_fmac_f32_e32 v32, v79, v14
	v_fmac_f32_e32 v36, v91, v14
	v_fmac_f32_e32 v32, v80, v6
	v_fma_f32 v69, v24, v0, 0
	v_add_u32_dpp v24, v63, v63 quad_perm:[1,0,3,2] row_mask:0xf bank_mask:0xf bound_ctrl:1
	v_fmac_f32_e32 v36, v92, v6
	v_fmac_f32_e32 v32, v81, v3
	v_add_u32_dpp v63, v72, v72 quad_perm:[1,0,3,2] row_mask:0xf bank_mask:0xf bound_ctrl:1
	v_add_u32_dpp v24, v24, v24 quad_perm:[2,3,0,1] row_mask:0xf bank_mask:0xf bound_ctrl:1
	v_fmac_f32_e32 v36, v93, v3
	v_fmac_f32_e32 v32, v82, v11
	v_fmac_f32_e32 v69, v25, v8
	v_add_u32_dpp v25, v63, v63 quad_perm:[2,3,0,1] row_mask:0xf bank_mask:0xf bound_ctrl:1
	v_add_u32_dpp v24, v24, v24 row_half_mirror row_mask:0xf bank_mask:0xf bound_ctrl:1
	v_fmac_f32_e32 v36, v37, v11
	v_fmac_f32_e32 v32, v83, v15
	v_add_u32_dpp v25, v25, v25 row_half_mirror row_mask:0xf bank_mask:0xf bound_ctrl:1
	v_cndmask_b32_e32 v24, 0, v24, vcc
	v_fmac_f32_e32 v36, v38, v15
	v_fmac_f32_e32 v32, v84, v7
	v_cndmask_b32_e64 v64, v24, v25, s[0:1]
	v_fmac_f32_e32 v36, v39, v7
	v_add_f32_dpp v24, v32, v32 quad_perm:[1,0,3,2] row_mask:0xf bank_mask:0xf bound_ctrl:1
	v_fmac_f32_e32 v69, v26, v12
	v_add_f32_dpp v25, v36, v36 quad_perm:[1,0,3,2] row_mask:0xf bank_mask:0xf bound_ctrl:1
	v_add_f32_dpp v24, v24, v24 quad_perm:[2,3,0,1] row_mask:0xf bank_mask:0xf bound_ctrl:1
	v_fmac_f32_e32 v69, v27, v4
	v_add_f32_dpp v25, v25, v25 quad_perm:[2,3,0,1] row_mask:0xf bank_mask:0xf bound_ctrl:1
	v_add_f32_dpp v24, v24, v24 row_half_mirror row_mask:0xf bank_mask:0xf bound_ctrl:1
	v_cndmask_b32_e32 v24, 0, v24, vcc
	v_add_f32_dpp v25, v25, v25 row_half_mirror row_mask:0xf bank_mask:0xf bound_ctrl:1
	v_cndmask_b32_e64 v36, v24, v25, s[0:1]
	v_cvt_f32_i32_sdwa v24, sext(v17) dst_sel:DWORD dst_unused:UNUSED_PAD src0_sel:BYTE_1
	v_cvt_f32_i32_sdwa v25, sext(v18) dst_sel:DWORD dst_unused:UNUSED_PAD src0_sel:BYTE_1
	v_fmac_f32_e32 v69, v68, v1
	v_cvt_f32_i32_sdwa v26, sext(v19) dst_sel:DWORD dst_unused:UNUSED_PAD src0_sel:BYTE_1
	v_fmac_f32_e32 v69, v24, v9
	v_fmac_f32_e32 v69, v25, v13
	v_cvt_f32_i32_sdwa v25, sext(v16) dst_sel:DWORD dst_unused:UNUSED_PAD src0_sel:BYTE_2
	v_cvt_f32_i32_sdwa v32, sext(v17) dst_sel:DWORD dst_unused:UNUSED_PAD src0_sel:BYTE_2
	ds_bpermute_b32 v24, v44, v53 offset:160
	v_fmac_f32_e32 v69, v26, v5
	v_ashrrev_i32_e32 v63, 31, v62
	v_cvt_f32_i32_sdwa v34, sext(v18) dst_sel:DWORD dst_unused:UNUSED_PAD src0_sel:BYTE_2
	v_lshlrev_b64 v[26:27], 7, v[62:63]
	v_fmac_f32_e32 v69, v25, v2
	v_cvt_f32_i32_sdwa v35, sext(v19) dst_sel:DWORD dst_unused:UNUSED_PAD src0_sel:BYTE_2
	v_fmac_f32_e32 v69, v32, v10
	v_lshl_add_u64 v[32:33], v[42:43], 0, v[26:27]
	v_cvt_f32_i32_sdwa v26, sext(v16) dst_sel:DWORD dst_unused:UNUSED_PAD src0_sel:BYTE_3
	v_cvt_f32_i32_sdwa v27, sext(v17) dst_sel:DWORD dst_unused:UNUSED_PAD src0_sel:BYTE_3
	v_fmac_f32_e32 v69, v34, v14
	v_cvt_f32_i32_sdwa v37, sext(v18) dst_sel:DWORD dst_unused:UNUSED_PAD src0_sel:BYTE_3
	s_waitcnt lgkmcnt(0)
	v_ashrrev_i32_e32 v25, 31, v24
	v_fmac_f32_e32 v69, v35, v6
	v_cvt_f32_i32_sdwa v38, sext(v19) dst_sel:DWORD dst_unused:UNUSED_PAD src0_sel:BYTE_3
	v_lshlrev_b64 v[16:17], 7, v[24:25]
	v_fmac_f32_e32 v69, v26, v3
	v_lshl_add_u64 v[34:35], v[42:43], 0, v[16:17]
	v_fmac_f32_e32 v69, v27, v11
	global_load_dwordx4 v[16:19], v[32:33], off
	global_load_dwordx4 v[24:27], v[34:35], off
	v_add_u32_dpp v33, v73, v73 quad_perm:[1,0,3,2] row_mask:0xf bank_mask:0xf bound_ctrl:1
	v_fmac_f32_e32 v69, v37, v15
	v_fmac_f32_e32 v69, v38, v7
	v_add_u32_dpp v33, v33, v33 quad_perm:[2,3,0,1] row_mask:0xf bank_mask:0xf bound_ctrl:1
	s_waitcnt vmcnt(5)
	v_cvt_f32_i32_sdwa v35, sext(v57) dst_sel:DWORD dst_unused:UNUSED_PAD src0_sel:BYTE_0
	v_add_f32_dpp v34, v69, v69 quad_perm:[1,0,3,2] row_mask:0xf bank_mask:0xf bound_ctrl:1
	v_add_u32_dpp v33, v33, v33 row_half_mirror row_mask:0xf bank_mask:0xf bound_ctrl:1
	v_cndmask_b32_e64 v63, v64, v33, s[2:3]
	v_cvt_f32_i32_sdwa v33, sext(v54) dst_sel:DWORD dst_unused:UNUSED_PAD src0_sel:BYTE_0
	v_add_f32_dpp v34, v34, v34 quad_perm:[2,3,0,1] row_mask:0xf bank_mask:0xf bound_ctrl:1
	v_mov_b32_e32 v64, v41
	s_waitcnt vmcnt(4)
	v_dot4c_i32_i8_e32 v64, v54, v58
	v_add_f32_dpp v34, v34, v34 row_half_mirror row_mask:0xf bank_mask:0xf bound_ctrl:1
	v_cndmask_b32_e64 v62, v36, v34, s[2:3]
	v_dot4c_i32_i8_e32 v64, v55, v59
	v_cvt_f32_i32_sdwa v34, sext(v55) dst_sel:DWORD dst_unused:UNUSED_PAD src0_sel:BYTE_0
	v_dot4c_i32_i8_e32 v64, v56, v60
	v_fma_f32 v60, v33, v0, 0
	v_cvt_f32_i32_sdwa v33, sext(v56) dst_sel:DWORD dst_unused:UNUSED_PAD src0_sel:BYTE_0
	v_fmac_f32_e32 v60, v34, v8
	v_cvt_f32_i32_sdwa v34, sext(v54) dst_sel:DWORD dst_unused:UNUSED_PAD src0_sel:BYTE_1
	v_cvt_f32_i32_sdwa v36, sext(v57) dst_sel:DWORD dst_unused:UNUSED_PAD src0_sel:BYTE_1
	v_fmac_f32_e32 v60, v33, v12
	v_cvt_f32_i32_sdwa v33, sext(v55) dst_sel:DWORD dst_unused:UNUSED_PAD src0_sel:BYTE_1
	v_fmac_f32_e32 v60, v35, v4
	v_cvt_f32_i32_sdwa v35, sext(v56) dst_sel:DWORD dst_unused:UNUSED_PAD src0_sel:BYTE_1
	v_fmac_f32_e32 v60, v34, v1
	v_fmac_f32_e32 v60, v33, v9
	v_cvt_f32_i32_sdwa v37, sext(v57) dst_sel:DWORD dst_unused:UNUSED_PAD src0_sel:BYTE_2
	v_fmac_f32_e32 v60, v35, v13
	v_cvt_f32_i32_sdwa v35, sext(v54) dst_sel:DWORD dst_unused:UNUSED_PAD src0_sel:BYTE_2
	v_fmac_f32_e32 v60, v36, v5
	v_cvt_f32_i32_sdwa v36, sext(v55) dst_sel:DWORD dst_unused:UNUSED_PAD src0_sel:BYTE_2
	ds_bpermute_b32 v32, v44, v52 offset:192
	v_fmac_f32_e32 v60, v35, v2
	ds_bpermute_b32 v34, v44, v53 offset:192
	v_fmac_f32_e32 v60, v36, v10
	v_cvt_f32_i32_sdwa v36, sext(v56) dst_sel:DWORD dst_unused:UNUSED_PAD src0_sel:BYTE_2
	v_cvt_f32_i32_sdwa v56, sext(v56) dst_sel:DWORD dst_unused:UNUSED_PAD src0_sel:BYTE_3
	v_dot4c_i32_i8_e32 v64, v57, v61
	v_cvt_f32_i32_sdwa v57, sext(v57) dst_sel:DWORD dst_unused:UNUSED_PAD src0_sel:BYTE_3
	v_fmac_f32_e32 v60, v36, v14
	v_cvt_f32_i32_sdwa v36, sext(v54) dst_sel:DWORD dst_unused:UNUSED_PAD src0_sel:BYTE_3
	v_fmac_f32_e32 v60, v37, v6
	v_cvt_f32_i32_sdwa v37, sext(v55) dst_sel:DWORD dst_unused:UNUSED_PAD src0_sel:BYTE_3
	s_waitcnt lgkmcnt(1)
	v_ashrrev_i32_e32 v33, 31, v32
	v_fmac_f32_e32 v60, v36, v3
	v_lshlrev_b64 v[32:33], 7, v[32:33]
	s_waitcnt lgkmcnt(0)
	v_ashrrev_i32_e32 v35, 31, v34
	v_fmac_f32_e32 v60, v37, v11
	v_lshl_add_u64 v[58:59], v[42:43], 0, v[32:33]
	v_lshlrev_b64 v[32:33], 7, v[34:35]
	v_fmac_f32_e32 v60, v56, v15
	v_lshl_add_u64 v[54:55], v[42:43], 0, v[32:33]
	v_fmac_f32_e32 v60, v57, v7
	global_load_dwordx4 v[32:35], v[58:59], off
	global_load_dwordx4 v[36:39], v[54:55], off
	v_add_f32_dpp v55, v60, v60 quad_perm:[1,0,3,2] row_mask:0xf bank_mask:0xf bound_ctrl:1
	v_add_u32_dpp v54, v64, v64 quad_perm:[1,0,3,2] row_mask:0xf bank_mask:0xf bound_ctrl:1
	s_waitcnt vmcnt(5)
	v_cvt_f32_i32_sdwa v58, sext(v22) dst_sel:DWORD dst_unused:UNUSED_PAD src0_sel:BYTE_0
	v_add_f32_dpp v55, v55, v55 quad_perm:[2,3,0,1] row_mask:0xf bank_mask:0xf bound_ctrl:1
	v_add_u32_dpp v54, v54, v54 quad_perm:[2,3,0,1] row_mask:0xf bank_mask:0xf bound_ctrl:1
	ds_bpermute_b32 v52, v44, v52 offset:224
	v_add_f32_dpp v55, v55, v55 row_half_mirror row_mask:0xf bank_mask:0xf bound_ctrl:1
	v_cndmask_b32_e64 v56, v62, v55, s[4:5]
	v_cvt_f32_i32_sdwa v55, sext(v20) dst_sel:DWORD dst_unused:UNUSED_PAD src0_sel:BYTE_0
	v_add_u32_dpp v54, v54, v54 row_half_mirror row_mask:0xf bank_mask:0xf bound_ctrl:1
	v_cndmask_b32_e64 v57, v63, v54, s[4:5]
	v_cvt_f32_i32_sdwa v54, sext(v21) dst_sel:DWORD dst_unused:UNUSED_PAD src0_sel:BYTE_0
	v_fma_f32 v59, v55, v0, 0
	v_cvt_f32_i32_sdwa v55, sext(v23) dst_sel:DWORD dst_unused:UNUSED_PAD src0_sel:BYTE_0
	v_cvt_f32_i32_sdwa v60, sext(v20) dst_sel:DWORD dst_unused:UNUSED_PAD src0_sel:BYTE_3
	v_fmac_f32_e32 v59, v54, v8
	v_fmac_f32_e32 v59, v58, v12
	v_cvt_f32_i32_sdwa v54, sext(v20) dst_sel:DWORD dst_unused:UNUSED_PAD src0_sel:BYTE_1
	v_fmac_f32_e32 v59, v55, v4
	v_cvt_f32_i32_sdwa v55, sext(v21) dst_sel:DWORD dst_unused:UNUSED_PAD src0_sel:BYTE_1
	v_cvt_f32_i32_sdwa v58, sext(v22) dst_sel:DWORD dst_unused:UNUSED_PAD src0_sel:BYTE_1
	v_fmac_f32_e32 v59, v54, v1
	v_cvt_f32_i32_sdwa v54, sext(v23) dst_sel:DWORD dst_unused:UNUSED_PAD src0_sel:BYTE_1
	v_fmac_f32_e32 v59, v55, v9
	v_cvt_f32_i32_sdwa v55, sext(v20) dst_sel:DWORD dst_unused:UNUSED_PAD src0_sel:BYTE_2
	v_fmac_f32_e32 v59, v58, v13
	v_cvt_f32_i32_sdwa v58, sext(v21) dst_sel:DWORD dst_unused:UNUSED_PAD src0_sel:BYTE_2
	v_fmac_f32_e32 v59, v54, v5
	v_fmac_f32_e32 v59, v55, v2
	v_cvt_f32_i32_sdwa v55, sext(v22) dst_sel:DWORD dst_unused:UNUSED_PAD src0_sel:BYTE_2
	v_fmac_f32_e32 v59, v58, v10
	v_cvt_f32_i32_sdwa v58, sext(v23) dst_sel:DWORD dst_unused:UNUSED_PAD src0_sel:BYTE_2
	ds_bpermute_b32 v54, v44, v53 offset:224
	v_fmac_f32_e32 v59, v55, v14
	s_waitcnt lgkmcnt(1)
	v_ashrrev_i32_e32 v53, 31, v52
	v_fmac_f32_e32 v59, v58, v6
	v_mov_b32_e32 v58, v41
	s_waitcnt vmcnt(4)
	v_dot4c_i32_i8_e32 v58, v20, v28
	v_lshlrev_b64 v[52:53], 7, v[52:53]
	s_waitcnt lgkmcnt(0)
	v_ashrrev_i32_e32 v55, 31, v54
	v_dot4c_i32_i8_e32 v58, v21, v29
	v_lshl_add_u64 v[52:53], v[42:43], 0, v[52:53]
	v_lshlrev_b64 v[54:55], 7, v[54:55]
	v_dot4c_i32_i8_e32 v58, v22, v30
	v_lshl_add_u64 v[54:55], v[42:43], 0, v[54:55]
	v_dot4c_i32_i8_e32 v58, v23, v31
	v_cvt_f32_i32_sdwa v61, sext(v21) dst_sel:DWORD dst_unused:UNUSED_PAD src0_sel:BYTE_3
	v_cvt_f32_i32_sdwa v62, sext(v22) dst_sel:DWORD dst_unused:UNUSED_PAD src0_sel:BYTE_3
	v_cvt_f32_i32_sdwa v63, sext(v23) dst_sel:DWORD dst_unused:UNUSED_PAD src0_sel:BYTE_3
	global_load_dwordx4 v[20:23], v[52:53], off
	global_load_dwordx4 v[28:31], v[54:55], off
	v_mov_b32_e32 v54, v41
	s_waitcnt vmcnt(4)
	v_dot4c_i32_i8_e32 v54, v16, v24
	v_cvt_f32_i32_sdwa v24, sext(v16) dst_sel:DWORD dst_unused:UNUSED_PAD src0_sel:BYTE_0
	v_fmac_f32_e32 v59, v60, v3
	v_dot4c_i32_i8_e32 v54, v17, v25
	v_cvt_f32_i32_sdwa v25, sext(v17) dst_sel:DWORD dst_unused:UNUSED_PAD src0_sel:BYTE_0
	v_fmac_f32_e32 v59, v61, v11
	v_dot4c_i32_i8_e32 v54, v18, v26
	v_cvt_f32_i32_sdwa v26, sext(v18) dst_sel:DWORD dst_unused:UNUSED_PAD src0_sel:BYTE_0
	v_fmac_f32_e32 v59, v62, v15
	v_cvt_f32_i32_sdwa v55, sext(v19) dst_sel:DWORD dst_unused:UNUSED_PAD src0_sel:BYTE_0
	v_fmac_f32_e32 v59, v63, v7
	v_fma_f32 v24, v24, v0, 0
	v_fmac_f32_e32 v24, v25, v8
	v_add_f32_dpp v53, v59, v59 quad_perm:[1,0,3,2] row_mask:0xf bank_mask:0xf bound_ctrl:1
	v_cvt_f32_i32_sdwa v25, sext(v16) dst_sel:DWORD dst_unused:UNUSED_PAD src0_sel:BYTE_1
	v_fmac_f32_e32 v24, v26, v12
	v_add_f32_dpp v53, v53, v53 quad_perm:[2,3,0,1] row_mask:0xf bank_mask:0xf bound_ctrl:1
	v_cvt_f32_i32_sdwa v26, sext(v17) dst_sel:DWORD dst_unused:UNUSED_PAD src0_sel:BYTE_1
	v_fmac_f32_e32 v24, v55, v4
	v_add_f32_dpp v53, v53, v53 row_half_mirror row_mask:0xf bank_mask:0xf bound_ctrl:1
	v_cvt_f32_i32_sdwa v55, sext(v18) dst_sel:DWORD dst_unused:UNUSED_PAD src0_sel:BYTE_1
	v_cndmask_b32_e64 v53, v56, v53, s[6:7]
	v_cvt_f32_i32_sdwa v56, sext(v19) dst_sel:DWORD dst_unused:UNUSED_PAD src0_sel:BYTE_1
	v_fmac_f32_e32 v24, v25, v1
	v_cvt_f32_i32_sdwa v25, sext(v16) dst_sel:DWORD dst_unused:UNUSED_PAD src0_sel:BYTE_2
	v_fmac_f32_e32 v24, v26, v9
	v_cvt_f32_i32_sdwa v26, sext(v17) dst_sel:DWORD dst_unused:UNUSED_PAD src0_sel:BYTE_2
	v_fmac_f32_e32 v24, v55, v13
	v_cvt_f32_i32_sdwa v55, sext(v18) dst_sel:DWORD dst_unused:UNUSED_PAD src0_sel:BYTE_2
	v_fmac_f32_e32 v24, v56, v5
	v_cvt_f32_i32_sdwa v56, sext(v19) dst_sel:DWORD dst_unused:UNUSED_PAD src0_sel:BYTE_2
	v_fmac_f32_e32 v24, v25, v2
	v_cvt_f32_i32_sdwa v16, sext(v16) dst_sel:DWORD dst_unused:UNUSED_PAD src0_sel:BYTE_3
	v_fmac_f32_e32 v24, v26, v10
	v_cvt_f32_i32_sdwa v17, sext(v17) dst_sel:DWORD dst_unused:UNUSED_PAD src0_sel:BYTE_3
	v_fmac_f32_e32 v24, v55, v14
	v_cvt_f32_i32_sdwa v18, sext(v18) dst_sel:DWORD dst_unused:UNUSED_PAD src0_sel:BYTE_3
	v_fmac_f32_e32 v24, v56, v6
	v_cvt_f32_i32_sdwa v25, sext(v19) dst_sel:DWORD dst_unused:UNUSED_PAD src0_sel:BYTE_3
	v_fmac_f32_e32 v24, v16, v3
	v_fmac_f32_e32 v24, v17, v11
	v_fmac_f32_e32 v24, v18, v15
	v_fmac_f32_e32 v24, v25, v7
	v_dot4c_i32_i8_e32 v54, v19, v27
	s_waitcnt vmcnt(3)
	v_cvt_f32_i32_sdwa v19, sext(v32) dst_sel:DWORD dst_unused:UNUSED_PAD src0_sel:BYTE_0
	v_add_f32_dpp v17, v24, v24 quad_perm:[1,0,3,2] row_mask:0xf bank_mask:0xf bound_ctrl:1
	v_cvt_f32_i32_sdwa v24, sext(v33) dst_sel:DWORD dst_unused:UNUSED_PAD src0_sel:BYTE_0
	v_cvt_f32_i32_sdwa v25, sext(v34) dst_sel:DWORD dst_unused:UNUSED_PAD src0_sel:BYTE_0
	v_cvt_f32_i32_sdwa v26, sext(v35) dst_sel:DWORD dst_unused:UNUSED_PAD src0_sel:BYTE_0
	v_fma_f32 v19, v19, v0, 0
	v_fmac_f32_e32 v19, v24, v8
	v_cvt_f32_i32_sdwa v24, sext(v32) dst_sel:DWORD dst_unused:UNUSED_PAD src0_sel:BYTE_1
	v_fmac_f32_e32 v19, v25, v12
	v_cvt_f32_i32_sdwa v25, sext(v33) dst_sel:DWORD dst_unused:UNUSED_PAD src0_sel:BYTE_1
	v_fmac_f32_e32 v19, v26, v4
	v_cvt_f32_i32_sdwa v26, sext(v34) dst_sel:DWORD dst_unused:UNUSED_PAD src0_sel:BYTE_1
	v_cvt_f32_i32_sdwa v27, sext(v35) dst_sel:DWORD dst_unused:UNUSED_PAD src0_sel:BYTE_1
	v_fmac_f32_e32 v19, v24, v1
	v_cvt_f32_i32_sdwa v24, sext(v32) dst_sel:DWORD dst_unused:UNUSED_PAD src0_sel:BYTE_2
	v_fmac_f32_e32 v19, v25, v9
	v_cvt_f32_i32_sdwa v25, sext(v33) dst_sel:DWORD dst_unused:UNUSED_PAD src0_sel:BYTE_2
	v_fmac_f32_e32 v19, v26, v13
	v_cvt_f32_i32_sdwa v26, sext(v34) dst_sel:DWORD dst_unused:UNUSED_PAD src0_sel:BYTE_2
	v_fmac_f32_e32 v19, v27, v5
	v_cvt_f32_i32_sdwa v27, sext(v35) dst_sel:DWORD dst_unused:UNUSED_PAD src0_sel:BYTE_2
	v_fmac_f32_e32 v19, v24, v2
	v_cvt_f32_i32_sdwa v24, sext(v32) dst_sel:DWORD dst_unused:UNUSED_PAD src0_sel:BYTE_3
	v_fmac_f32_e32 v19, v25, v10
	v_cvt_f32_i32_sdwa v25, sext(v33) dst_sel:DWORD dst_unused:UNUSED_PAD src0_sel:BYTE_3
	v_fmac_f32_e32 v19, v26, v14
	v_cvt_f32_i32_sdwa v26, sext(v34) dst_sel:DWORD dst_unused:UNUSED_PAD src0_sel:BYTE_3
	v_fmac_f32_e32 v19, v27, v6
	v_cvt_f32_i32_sdwa v27, sext(v35) dst_sel:DWORD dst_unused:UNUSED_PAD src0_sel:BYTE_3
	v_fmac_f32_e32 v19, v24, v3
	v_fmac_f32_e32 v19, v25, v11
	v_fmac_f32_e32 v19, v26, v15
	v_fmac_f32_e32 v19, v27, v7
	v_add_f32_dpp v17, v17, v17 quad_perm:[2,3,0,1] row_mask:0xf bank_mask:0xf bound_ctrl:1
	s_waitcnt vmcnt(1)
	v_cvt_f32_i32_sdwa v24, sext(v21) dst_sel:DWORD dst_unused:UNUSED_PAD src0_sel:BYTE_0
	v_add_f32_dpp v19, v19, v19 quad_perm:[1,0,3,2] row_mask:0xf bank_mask:0xf bound_ctrl:1
	v_add_f32_dpp v17, v17, v17 row_half_mirror row_mask:0xf bank_mask:0xf bound_ctrl:1
	v_cndmask_b32_e64 v17, v53, v17, s[8:9]
	v_add_f32_dpp v19, v19, v19 quad_perm:[2,3,0,1] row_mask:0xf bank_mask:0xf bound_ctrl:1
	v_cvt_f32_i32_sdwa v25, sext(v22) dst_sel:DWORD dst_unused:UNUSED_PAD src0_sel:BYTE_0
	v_cvt_f32_i32_sdwa v26, sext(v23) dst_sel:DWORD dst_unused:UNUSED_PAD src0_sel:BYTE_0
	v_add_f32_dpp v19, v19, v19 row_half_mirror row_mask:0xf bank_mask:0xf bound_ctrl:1
	v_cndmask_b32_e64 v17, v17, v19, s[10:11]
	v_cvt_f32_i32_sdwa v19, sext(v20) dst_sel:DWORD dst_unused:UNUSED_PAD src0_sel:BYTE_0
	v_mov_b32_e32 v18, v41
	v_dot4c_i32_i8_e32 v18, v32, v36
	v_dot4c_i32_i8_e32 v18, v33, v37
	v_fma_f32 v19, v19, v0, 0
	v_fmac_f32_e32 v19, v24, v8
	v_cvt_f32_i32_sdwa v24, sext(v20) dst_sel:DWORD dst_unused:UNUSED_PAD src0_sel:BYTE_1
	v_fmac_f32_e32 v19, v25, v12
	v_cvt_f32_i32_sdwa v25, sext(v21) dst_sel:DWORD dst_unused:UNUSED_PAD src0_sel:BYTE_1
	v_add_u32_dpp v52, v58, v58 quad_perm:[1,0,3,2] row_mask:0xf bank_mask:0xf bound_ctrl:1
	v_dot4c_i32_i8_e32 v18, v34, v38
	v_fmac_f32_e32 v19, v26, v4
	v_cvt_f32_i32_sdwa v26, sext(v22) dst_sel:DWORD dst_unused:UNUSED_PAD src0_sel:BYTE_1
	v_add_u32_dpp v52, v52, v52 quad_perm:[2,3,0,1] row_mask:0xf bank_mask:0xf bound_ctrl:1
	v_add_u32_dpp v16, v54, v54 quad_perm:[1,0,3,2] row_mask:0xf bank_mask:0xf bound_ctrl:1
	v_dot4c_i32_i8_e32 v18, v35, v39
	v_cvt_f32_i32_sdwa v27, sext(v23) dst_sel:DWORD dst_unused:UNUSED_PAD src0_sel:BYTE_1
	v_add_u32_dpp v52, v52, v52 row_half_mirror row_mask:0xf bank_mask:0xf bound_ctrl:1
	v_add_u32_dpp v16, v16, v16 quad_perm:[2,3,0,1] row_mask:0xf bank_mask:0xf bound_ctrl:1
	v_add_u32_dpp v18, v18, v18 quad_perm:[1,0,3,2] row_mask:0xf bank_mask:0xf bound_ctrl:1
	v_fmac_f32_e32 v19, v24, v1
	v_cvt_f32_i32_sdwa v24, sext(v20) dst_sel:DWORD dst_unused:UNUSED_PAD src0_sel:BYTE_2
	v_cndmask_b32_e64 v52, v57, v52, s[6:7]
	v_add_u32_dpp v16, v16, v16 row_half_mirror row_mask:0xf bank_mask:0xf bound_ctrl:1
	v_add_u32_dpp v18, v18, v18 quad_perm:[2,3,0,1] row_mask:0xf bank_mask:0xf bound_ctrl:1
	v_fmac_f32_e32 v19, v25, v9
	v_cvt_f32_i32_sdwa v25, sext(v21) dst_sel:DWORD dst_unused:UNUSED_PAD src0_sel:BYTE_2
	v_cndmask_b32_e64 v16, v52, v16, s[8:9]
	v_add_u32_dpp v18, v18, v18 row_half_mirror row_mask:0xf bank_mask:0xf bound_ctrl:1
	v_fmac_f32_e32 v19, v26, v13
	v_cvt_f32_i32_sdwa v26, sext(v22) dst_sel:DWORD dst_unused:UNUSED_PAD src0_sel:BYTE_2
	v_cndmask_b32_e64 v16, v16, v18, s[10:11]
	v_mov_b32_e32 v18, v41
	v_fmac_f32_e32 v19, v27, v5
	v_cvt_f32_i32_sdwa v27, sext(v23) dst_sel:DWORD dst_unused:UNUSED_PAD src0_sel:BYTE_2
	s_waitcnt vmcnt(0)
	v_dot4c_i32_i8_e32 v18, v20, v28
	v_fmac_f32_e32 v19, v24, v2
	v_cvt_f32_i32_sdwa v20, sext(v20) dst_sel:DWORD dst_unused:UNUSED_PAD src0_sel:BYTE_3
	v_dot4c_i32_i8_e32 v18, v21, v29
	v_fmac_f32_e32 v19, v25, v10
	v_cvt_f32_i32_sdwa v21, sext(v21) dst_sel:DWORD dst_unused:UNUSED_PAD src0_sel:BYTE_3
	v_dot4c_i32_i8_e32 v18, v22, v30
	v_fmac_f32_e32 v19, v26, v14
	v_cvt_f32_i32_sdwa v22, sext(v22) dst_sel:DWORD dst_unused:UNUSED_PAD src0_sel:BYTE_3
	v_fmac_f32_e32 v19, v27, v6
	v_cvt_f32_i32_sdwa v24, sext(v23) dst_sel:DWORD dst_unused:UNUSED_PAD src0_sel:BYTE_3
	v_fmac_f32_e32 v19, v20, v3
	v_fmac_f32_e32 v19, v21, v11
	v_fmac_f32_e32 v19, v22, v15
	v_fmac_f32_e32 v19, v24, v7
	v_dot4c_i32_i8_e32 v18, v23, v31
	ds_bpermute_b32 v58, v44, v50 offset:96
	v_add_f32_dpp v19, v19, v19 quad_perm:[1,0,3,2] row_mask:0xf bank_mask:0xf bound_ctrl:1
	s_waitcnt lgkmcnt(0)
	v_ashrrev_i32_e32 v59, 31, v58
	v_add_u32_dpp v18, v18, v18 quad_perm:[1,0,3,2] row_mask:0xf bank_mask:0xf bound_ctrl:1
	v_add_f32_dpp v19, v19, v19 quad_perm:[2,3,0,1] row_mask:0xf bank_mask:0xf bound_ctrl:1
	v_lshlrev_b64 v[58:59], 7, v[58:59]
	v_add_u32_dpp v18, v18, v18 quad_perm:[2,3,0,1] row_mask:0xf bank_mask:0xf bound_ctrl:1
	v_add_f32_dpp v19, v19, v19 row_half_mirror row_mask:0xf bank_mask:0xf bound_ctrl:1
	v_cndmask_b32_e64 v19, v17, v19, s[12:13]
	v_add_u32_dpp v18, v18, v18 row_half_mirror row_mask:0xf bank_mask:0xf bound_ctrl:1
	v_cndmask_b32_e64 v20, v16, v18, s[12:13]
	v_lshlrev_b64 v[16:17], 2, v[40:41]
	ds_bpermute_b32 v18, v44, v50
	v_lshl_add_u64 v[28:29], s[16:17], 0, v[16:17]
	v_lshl_add_u64 v[30:31], s[18:19], 0, v[16:17]
	ds_bpermute_b32 v16, v44, v49
	global_atomic_add v[28:29], v20, off
	global_atomic_add_f32 v[30:31], v19, off
	s_waitcnt lgkmcnt(1)
	v_ashrrev_i32_e32 v19, 31, v18
	v_lshlrev_b64 v[18:19], 7, v[18:19]
	s_waitcnt lgkmcnt(0)
	v_ashrrev_i32_e32 v17, 31, v16
	v_lshl_add_u64 v[18:19], v[42:43], 0, v[18:19]
	v_lshlrev_b64 v[16:17], 7, v[16:17]
	v_lshl_add_u64 v[16:17], v[42:43], 0, v[16:17]
	global_load_dwordx4 v[32:35], v[18:19], off
	global_load_dwordx4 v[36:39], v[16:17], off
	ds_bpermute_b32 v16, v44, v50 offset:32
	ds_bpermute_b32 v18, v44, v49 offset:32
	v_mov_b32_e32 v40, v41
	v_lshl_add_u64 v[58:59], v[42:43], 0, v[58:59]
	s_waitcnt lgkmcnt(1)
	v_ashrrev_i32_e32 v17, 31, v16
	v_lshlrev_b64 v[16:17], 7, v[16:17]
	s_waitcnt lgkmcnt(0)
	v_ashrrev_i32_e32 v19, 31, v18
	v_lshl_add_u64 v[16:17], v[42:43], 0, v[16:17]
	v_lshlrev_b64 v[18:19], 7, v[18:19]
	v_lshl_add_u64 v[18:19], v[42:43], 0, v[18:19]
	global_load_dwordx4 v[24:27], v[16:17], off
	global_load_dwordx4 v[52:55], v[18:19], off
	ds_bpermute_b32 v16, v44, v50 offset:64
	ds_bpermute_b32 v18, v44, v49 offset:64
	s_waitcnt lgkmcnt(1)
	v_ashrrev_i32_e32 v17, 31, v16
	v_lshlrev_b64 v[16:17], 7, v[16:17]
	s_waitcnt lgkmcnt(0)
	v_ashrrev_i32_e32 v19, 31, v18
	v_lshl_add_u64 v[56:57], v[42:43], 0, v[16:17]
	v_lshlrev_b64 v[16:17], 7, v[18:19]
	v_lshl_add_u64 v[60:61], v[42:43], 0, v[16:17]
	global_load_dwordx4 v[16:19], v[56:57], off
	global_load_dwordx4 v[20:23], v[60:61], off
	v_mov_b32_e32 v61, v41
	ds_bpermute_b32 v56, v44, v49 offset:96
	s_waitcnt lgkmcnt(0)
	v_ashrrev_i32_e32 v57, 31, v56
	s_waitcnt vmcnt(5)
	v_cvt_f32_i32_sdwa v60, sext(v32) dst_sel:DWORD dst_unused:UNUSED_PAD src0_sel:BYTE_2
	s_waitcnt vmcnt(4)
	v_dot4c_i32_i8_e32 v40, v32, v36
	v_cvt_f32_i32_sdwa v36, sext(v32) dst_sel:DWORD dst_unused:UNUSED_PAD src0_sel:BYTE_0
	v_dot4c_i32_i8_e32 v40, v33, v37
	v_cvt_f32_i32_sdwa v37, sext(v33) dst_sel:DWORD dst_unused:UNUSED_PAD src0_sel:BYTE_0
	v_dot4c_i32_i8_e32 v40, v34, v38
	v_cvt_f32_i32_sdwa v38, sext(v34) dst_sel:DWORD dst_unused:UNUSED_PAD src0_sel:BYTE_0
	v_fma_f32 v51, v36, v0, 0
	v_cvt_f32_i32_sdwa v36, sext(v35) dst_sel:DWORD dst_unused:UNUSED_PAD src0_sel:BYTE_0
	v_fmac_f32_e32 v51, v37, v8
	v_cvt_f32_i32_sdwa v37, sext(v32) dst_sel:DWORD dst_unused:UNUSED_PAD src0_sel:BYTE_1
	v_fmac_f32_e32 v51, v38, v12
	v_cvt_f32_i32_sdwa v38, sext(v33) dst_sel:DWORD dst_unused:UNUSED_PAD src0_sel:BYTE_1
	v_fmac_f32_e32 v51, v36, v4
	v_fmac_f32_e32 v51, v37, v1
	v_dot4c_i32_i8_e32 v40, v35, v39
	v_fmac_f32_e32 v51, v38, v9
	v_cvt_f32_i32_sdwa v38, sext(v34) dst_sel:DWORD dst_unused:UNUSED_PAD src0_sel:BYTE_1
	v_cvt_f32_i32_sdwa v39, sext(v35) dst_sel:DWORD dst_unused:UNUSED_PAD src0_sel:BYTE_1
	v_cvt_f32_i32_sdwa v32, sext(v32) dst_sel:DWORD dst_unused:UNUSED_PAD src0_sel:BYTE_3
	s_waitcnt vmcnt(2)
	v_dot4c_i32_i8_e32 v61, v24, v52
	v_fmac_f32_e32 v51, v38, v13
	v_cvt_f32_i32_sdwa v38, sext(v33) dst_sel:DWORD dst_unused:UNUSED_PAD src0_sel:BYTE_2
	v_fmac_f32_e32 v51, v39, v5
	v_cvt_f32_i32_sdwa v39, sext(v34) dst_sel:DWORD dst_unused:UNUSED_PAD src0_sel:BYTE_2
	v_fmac_f32_e32 v51, v60, v2
	v_cvt_f32_i32_sdwa v60, sext(v35) dst_sel:DWORD dst_unused:UNUSED_PAD src0_sel:BYTE_2
	v_fmac_f32_e32 v51, v38, v10
	v_cvt_f32_i32_sdwa v33, sext(v33) dst_sel:DWORD dst_unused:UNUSED_PAD src0_sel:BYTE_3
	v_fmac_f32_e32 v51, v39, v14
	v_cvt_f32_i32_sdwa v34, sext(v34) dst_sel:DWORD dst_unused:UNUSED_PAD src0_sel:BYTE_3
	v_fmac_f32_e32 v51, v60, v6
	v_fmac_f32_e32 v51, v32, v3
	v_cvt_f32_i32_sdwa v32, sext(v24) dst_sel:DWORD dst_unused:UNUSED_PAD src0_sel:BYTE_0
	v_fmac_f32_e32 v51, v33, v11
	v_cvt_f32_i32_sdwa v33, sext(v25) dst_sel:DWORD dst_unused:UNUSED_PAD src0_sel:BYTE_0
	v_fmac_f32_e32 v51, v34, v15
	v_cvt_f32_i32_sdwa v34, sext(v26) dst_sel:DWORD dst_unused:UNUSED_PAD src0_sel:BYTE_0
	v_cvt_f32_i32_sdwa v35, sext(v35) dst_sel:DWORD dst_unused:UNUSED_PAD src0_sel:BYTE_3
	v_fma_f32 v52, v32, v0, 0
	v_cvt_f32_i32_sdwa v32, sext(v27) dst_sel:DWORD dst_unused:UNUSED_PAD src0_sel:BYTE_0
	v_fmac_f32_e32 v52, v33, v8
	v_cvt_f32_i32_sdwa v33, sext(v24) dst_sel:DWORD dst_unused:UNUSED_PAD src0_sel:BYTE_1
	v_fmac_f32_e32 v52, v34, v12
	v_cvt_f32_i32_sdwa v34, sext(v25) dst_sel:DWORD dst_unused:UNUSED_PAD src0_sel:BYTE_1
	v_fmac_f32_e32 v51, v35, v7
	v_cvt_f32_i32_sdwa v35, sext(v26) dst_sel:DWORD dst_unused:UNUSED_PAD src0_sel:BYTE_1
	v_fmac_f32_e32 v52, v32, v4
	v_fmac_f32_e32 v52, v33, v1
	v_lshlrev_b64 v[36:37], 7, v[56:57]
	v_fmac_f32_e32 v52, v34, v9
	v_lshl_add_u64 v[56:57], v[42:43], 0, v[36:37]
	v_fmac_f32_e32 v52, v35, v13
	global_load_dwordx4 v[32:35], v[58:59], off
	global_load_dwordx4 v[36:39], v[56:57], off
	v_dot4c_i32_i8_e32 v61, v25, v53
	v_cvt_f32_i32_sdwa v53, sext(v27) dst_sel:DWORD dst_unused:UNUSED_PAD src0_sel:BYTE_1
	v_dot4c_i32_i8_e32 v61, v26, v54
	v_cvt_f32_i32_sdwa v54, sext(v24) dst_sel:DWORD dst_unused:UNUSED_PAD src0_sel:BYTE_2
	v_cvt_f32_i32_sdwa v60, sext(v25) dst_sel:DWORD dst_unused:UNUSED_PAD src0_sel:BYTE_2
	v_cvt_f32_i32_sdwa v62, sext(v26) dst_sel:DWORD dst_unused:UNUSED_PAD src0_sel:BYTE_2
	v_cvt_f32_i32_sdwa v63, sext(v27) dst_sel:DWORD dst_unused:UNUSED_PAD src0_sel:BYTE_2
	v_dot4c_i32_i8_e32 v61, v27, v55
	v_cvt_f32_i32_sdwa v55, sext(v24) dst_sel:DWORD dst_unused:UNUSED_PAD src0_sel:BYTE_3
	v_fmac_f32_e32 v52, v53, v5
	ds_bpermute_b32 v24, v44, v50 offset:128
	v_cvt_f32_i32_sdwa v65, sext(v26) dst_sel:DWORD dst_unused:UNUSED_PAD src0_sel:BYTE_3
	v_fmac_f32_e32 v52, v54, v2
	ds_bpermute_b32 v26, v44, v49 offset:128
	v_cvt_f32_i32_sdwa v64, sext(v25) dst_sel:DWORD dst_unused:UNUSED_PAD src0_sel:BYTE_3
	v_fmac_f32_e32 v52, v60, v10
	v_fmac_f32_e32 v52, v62, v14
	v_cvt_f32_i32_sdwa v66, sext(v27) dst_sel:DWORD dst_unused:UNUSED_PAD src0_sel:BYTE_3
	v_fmac_f32_e32 v52, v63, v6
	s_waitcnt lgkmcnt(1)
	v_ashrrev_i32_e32 v25, 31, v24
	v_fmac_f32_e32 v52, v55, v3
	v_lshlrev_b64 v[24:25], 7, v[24:25]
	s_waitcnt lgkmcnt(0)
	v_ashrrev_i32_e32 v27, 31, v26
	v_fmac_f32_e32 v52, v64, v11
	v_lshl_add_u64 v[56:57], v[42:43], 0, v[24:25]
	v_lshlrev_b64 v[24:25], 7, v[26:27]
	v_fmac_f32_e32 v52, v65, v15
	v_lshl_add_u64 v[58:59], v[42:43], 0, v[24:25]
	v_add_f32_dpp v25, v51, v51 quad_perm:[1,0,3,2] row_mask:0xf bank_mask:0xf bound_ctrl:1
	v_fmac_f32_e32 v52, v66, v7
	v_add_u32_dpp v24, v40, v40 quad_perm:[1,0,3,2] row_mask:0xf bank_mask:0xf bound_ctrl:1
	v_add_f32_dpp v25, v25, v25 quad_perm:[2,3,0,1] row_mask:0xf bank_mask:0xf bound_ctrl:1
	v_add_f32_dpp v27, v52, v52 quad_perm:[1,0,3,2] row_mask:0xf bank_mask:0xf bound_ctrl:1
	v_add_u32_dpp v24, v24, v24 quad_perm:[2,3,0,1] row_mask:0xf bank_mask:0xf bound_ctrl:1
	v_add_f32_dpp v25, v25, v25 row_half_mirror row_mask:0xf bank_mask:0xf bound_ctrl:1
	v_add_f32_dpp v27, v27, v27 quad_perm:[2,3,0,1] row_mask:0xf bank_mask:0xf bound_ctrl:1
	v_cndmask_b32_e32 v25, 0, v25, vcc
	v_add_u32_dpp v26, v61, v61 quad_perm:[1,0,3,2] row_mask:0xf bank_mask:0xf bound_ctrl:1
	v_add_f32_dpp v27, v27, v27 row_half_mirror row_mask:0xf bank_mask:0xf bound_ctrl:1
	v_add_u32_dpp v24, v24, v24 row_half_mirror row_mask:0xf bank_mask:0xf bound_ctrl:1
	v_add_u32_dpp v26, v26, v26 quad_perm:[2,3,0,1] row_mask:0xf bank_mask:0xf bound_ctrl:1
	v_cndmask_b32_e64 v40, v25, v27, s[0:1]
	s_waitcnt vmcnt(3)
	v_cvt_f32_i32_sdwa v25, sext(v16) dst_sel:DWORD dst_unused:UNUSED_PAD src0_sel:BYTE_0
	v_cndmask_b32_e32 v24, 0, v24, vcc
	v_add_u32_dpp v26, v26, v26 row_half_mirror row_mask:0xf bank_mask:0xf bound_ctrl:1
	v_cndmask_b32_e64 v51, v24, v26, s[0:1]
	v_cvt_f32_i32_sdwa v24, sext(v17) dst_sel:DWORD dst_unused:UNUSED_PAD src0_sel:BYTE_0
	v_cvt_f32_i32_sdwa v26, sext(v18) dst_sel:DWORD dst_unused:UNUSED_PAD src0_sel:BYTE_0
	v_fma_f32 v64, v25, v0, 0
	v_cvt_f32_i32_sdwa v25, sext(v19) dst_sel:DWORD dst_unused:UNUSED_PAD src0_sel:BYTE_0
	v_fmac_f32_e32 v64, v24, v8
	v_cvt_f32_i32_sdwa v24, sext(v16) dst_sel:DWORD dst_unused:UNUSED_PAD src0_sel:BYTE_1
	v_fmac_f32_e32 v64, v26, v12
	v_fmac_f32_e32 v64, v25, v4
	v_cvt_f32_i32_sdwa v25, sext(v17) dst_sel:DWORD dst_unused:UNUSED_PAD src0_sel:BYTE_1
	v_cvt_f32_i32_sdwa v26, sext(v18) dst_sel:DWORD dst_unused:UNUSED_PAD src0_sel:BYTE_1
	v_fmac_f32_e32 v64, v24, v1
	v_cvt_f32_i32_sdwa v24, sext(v19) dst_sel:DWORD dst_unused:UNUSED_PAD src0_sel:BYTE_1
	v_fmac_f32_e32 v64, v25, v9
	v_fmac_f32_e32 v64, v26, v13
	v_cvt_f32_i32_sdwa v25, sext(v16) dst_sel:DWORD dst_unused:UNUSED_PAD src0_sel:BYTE_2
	v_fmac_f32_e32 v64, v24, v5
	v_cvt_f32_i32_sdwa v24, sext(v17) dst_sel:DWORD dst_unused:UNUSED_PAD src0_sel:BYTE_2
	ds_bpermute_b32 v62, v44, v49 offset:160
	v_fmac_f32_e32 v64, v25, v2
	v_mov_b32_e32 v65, v41
	v_fmac_f32_e32 v64, v24, v10
	v_cvt_f32_i32_sdwa v24, sext(v18) dst_sel:DWORD dst_unused:UNUSED_PAD src0_sel:BYTE_2
	s_waitcnt vmcnt(2)
	v_dot4c_i32_i8_e32 v65, v16, v20
	v_cvt_f32_i32_sdwa v20, sext(v19) dst_sel:DWORD dst_unused:UNUSED_PAD src0_sel:BYTE_2
	ds_bpermute_b32 v60, v44, v50 offset:160
	v_fmac_f32_e32 v64, v24, v14
	global_load_dwordx4 v[24:27], v[56:57], off
	global_load_dwordx4 v[52:55], v[58:59], off
	v_dot4c_i32_i8_e32 v65, v17, v21
	v_cvt_f32_i32_sdwa v21, sext(v16) dst_sel:DWORD dst_unused:UNUSED_PAD src0_sel:BYTE_3
	v_dot4c_i32_i8_e32 v65, v18, v22
	v_cvt_f32_i32_sdwa v22, sext(v17) dst_sel:DWORD dst_unused:UNUSED_PAD src0_sel:BYTE_3
	v_dot4c_i32_i8_e32 v65, v19, v23
	v_cvt_f32_i32_sdwa v23, sext(v18) dst_sel:DWORD dst_unused:UNUSED_PAD src0_sel:BYTE_3
	v_cvt_f32_i32_sdwa v66, sext(v19) dst_sel:DWORD dst_unused:UNUSED_PAD src0_sel:BYTE_3
	s_waitcnt lgkmcnt(1)
	v_ashrrev_i32_e32 v63, 31, v62
	v_fmac_f32_e32 v64, v20, v6
	v_lshlrev_b64 v[18:19], 7, v[62:63]
	v_mov_b32_e32 v62, v41
	v_fmac_f32_e32 v64, v21, v3
	s_waitcnt lgkmcnt(0)
	v_ashrrev_i32_e32 v61, 31, v60
	s_waitcnt vmcnt(2)
	v_dot4c_i32_i8_e32 v62, v32, v36
	v_fmac_f32_e32 v64, v22, v11
	v_lshlrev_b64 v[16:17], 7, v[60:61]
	v_dot4c_i32_i8_e32 v62, v33, v37
	v_fmac_f32_e32 v64, v23, v15
	v_lshl_add_u64 v[16:17], v[42:43], 0, v[16:17]
	v_lshl_add_u64 v[18:19], v[42:43], 0, v[18:19]
	v_dot4c_i32_i8_e32 v62, v34, v38
	v_fmac_f32_e32 v64, v66, v7
	v_dot4c_i32_i8_e32 v62, v35, v39
	global_load_dwordx4 v[36:39], v[16:17], off
	global_load_dwordx4 v[56:59], v[18:19], off
	v_add_f32_dpp v18, v64, v64 quad_perm:[1,0,3,2] row_mask:0xf bank_mask:0xf bound_ctrl:1
	v_add_u32_dpp v17, v65, v65 quad_perm:[1,0,3,2] row_mask:0xf bank_mask:0xf bound_ctrl:1
	v_cvt_f32_i32_sdwa v19, sext(v34) dst_sel:DWORD dst_unused:UNUSED_PAD src0_sel:BYTE_0
	v_add_f32_dpp v18, v18, v18 quad_perm:[2,3,0,1] row_mask:0xf bank_mask:0xf bound_ctrl:1
	v_add_u32_dpp v17, v17, v17 quad_perm:[2,3,0,1] row_mask:0xf bank_mask:0xf bound_ctrl:1
	ds_bpermute_b32 v16, v44, v50 offset:192
	v_add_f32_dpp v18, v18, v18 row_half_mirror row_mask:0xf bank_mask:0xf bound_ctrl:1
	v_cndmask_b32_e64 v40, v40, v18, s[2:3]
	v_cvt_f32_i32_sdwa v18, sext(v32) dst_sel:DWORD dst_unused:UNUSED_PAD src0_sel:BYTE_0
	v_add_u32_dpp v17, v17, v17 row_half_mirror row_mask:0xf bank_mask:0xf bound_ctrl:1
	v_cndmask_b32_e64 v63, v51, v17, s[2:3]
	v_cvt_f32_i32_sdwa v17, sext(v33) dst_sel:DWORD dst_unused:UNUSED_PAD src0_sel:BYTE_0
	v_fma_f32 v51, v18, v0, 0
	v_cvt_f32_i32_sdwa v18, sext(v35) dst_sel:DWORD dst_unused:UNUSED_PAD src0_sel:BYTE_0
	v_cvt_f32_i32_sdwa v20, sext(v33) dst_sel:DWORD dst_unused:UNUSED_PAD src0_sel:BYTE_3
	v_fmac_f32_e32 v51, v17, v8
	v_cvt_f32_i32_sdwa v17, sext(v32) dst_sel:DWORD dst_unused:UNUSED_PAD src0_sel:BYTE_1
	v_fmac_f32_e32 v51, v19, v12
	v_fmac_f32_e32 v51, v18, v4
	v_cvt_f32_i32_sdwa v18, sext(v33) dst_sel:DWORD dst_unused:UNUSED_PAD src0_sel:BYTE_1
	v_cvt_f32_i32_sdwa v19, sext(v34) dst_sel:DWORD dst_unused:UNUSED_PAD src0_sel:BYTE_1
	v_fmac_f32_e32 v51, v17, v1
	v_cvt_f32_i32_sdwa v17, sext(v35) dst_sel:DWORD dst_unused:UNUSED_PAD src0_sel:BYTE_1
	v_fmac_f32_e32 v51, v18, v9
	v_fmac_f32_e32 v51, v19, v13
	v_cvt_f32_i32_sdwa v18, sext(v32) dst_sel:DWORD dst_unused:UNUSED_PAD src0_sel:BYTE_2
	v_fmac_f32_e32 v51, v17, v5
	v_cvt_f32_i32_sdwa v17, sext(v33) dst_sel:DWORD dst_unused:UNUSED_PAD src0_sel:BYTE_2
	v_cvt_f32_i32_sdwa v19, sext(v34) dst_sel:DWORD dst_unused:UNUSED_PAD src0_sel:BYTE_2
	v_fmac_f32_e32 v51, v18, v2
	v_cvt_f32_i32_sdwa v18, sext(v35) dst_sel:DWORD dst_unused:UNUSED_PAD src0_sel:BYTE_2
	v_fmac_f32_e32 v51, v17, v10
	v_fmac_f32_e32 v51, v19, v14
	v_cvt_f32_i32_sdwa v19, sext(v32) dst_sel:DWORD dst_unused:UNUSED_PAD src0_sel:BYTE_3
	v_fmac_f32_e32 v51, v18, v6
	ds_bpermute_b32 v18, v44, v49 offset:192
	s_waitcnt lgkmcnt(1)
	v_ashrrev_i32_e32 v17, 31, v16
	v_fmac_f32_e32 v51, v19, v3
	v_fmac_f32_e32 v51, v20, v11
	v_cvt_f32_i32_sdwa v20, sext(v34) dst_sel:DWORD dst_unused:UNUSED_PAD src0_sel:BYTE_3
	v_cvt_f32_i32_sdwa v34, sext(v35) dst_sel:DWORD dst_unused:UNUSED_PAD src0_sel:BYTE_3
	v_lshlrev_b64 v[16:17], 7, v[16:17]
	s_waitcnt lgkmcnt(0)
	v_ashrrev_i32_e32 v19, 31, v18
	v_lshl_add_u64 v[32:33], v[42:43], 0, v[16:17]
	v_lshlrev_b64 v[16:17], 7, v[18:19]
	v_lshl_add_u64 v[60:61], v[42:43], 0, v[16:17]
	v_fmac_f32_e32 v51, v20, v15
	global_load_dwordx4 v[16:19], v[32:33], off
	global_load_dwordx4 v[20:23], v[60:61], off
	ds_bpermute_b32 v32, v44, v50 offset:224
	v_fmac_f32_e32 v51, v34, v7
	ds_bpermute_b32 v34, v44, v49 offset:224
	v_mov_b32_e32 v60, v41
	v_add_f32_dpp v33, v51, v51 quad_perm:[1,0,3,2] row_mask:0xf bank_mask:0xf bound_ctrl:1
	s_waitcnt vmcnt(5)
	v_cvt_f32_i32_sdwa v35, sext(v26) dst_sel:DWORD dst_unused:UNUSED_PAD src0_sel:BYTE_0
	v_add_f32_dpp v33, v33, v33 quad_perm:[2,3,0,1] row_mask:0xf bank_mask:0xf bound_ctrl:1
	s_waitcnt vmcnt(4)
	v_dot4c_i32_i8_e32 v60, v24, v52
	v_dot4c_i32_i8_e32 v60, v25, v53
	v_add_f32_dpp v33, v33, v33 row_half_mirror row_mask:0xf bank_mask:0xf bound_ctrl:1
	v_cndmask_b32_e64 v40, v40, v33, s[4:5]
	s_waitcnt lgkmcnt(1)
	v_ashrrev_i32_e32 v33, 31, v32
	v_lshlrev_b64 v[32:33], 7, v[32:33]
	v_lshl_add_u64 v[50:51], v[42:43], 0, v[32:33]
	v_cvt_f32_i32_sdwa v33, sext(v25) dst_sel:DWORD dst_unused:UNUSED_PAD src0_sel:BYTE_0
	v_add_u32_dpp v32, v62, v62 quad_perm:[1,0,3,2] row_mask:0xf bank_mask:0xf bound_ctrl:1
	v_cvt_f32_i32_sdwa v52, sext(v27) dst_sel:DWORD dst_unused:UNUSED_PAD src0_sel:BYTE_0
	v_dot4c_i32_i8_e32 v60, v26, v54
	v_add_u32_dpp v32, v32, v32 quad_perm:[2,3,0,1] row_mask:0xf bank_mask:0xf bound_ctrl:1
	v_cvt_f32_i32_sdwa v53, sext(v24) dst_sel:DWORD dst_unused:UNUSED_PAD src0_sel:BYTE_2
	v_dot4c_i32_i8_e32 v60, v27, v55
	v_add_u32_dpp v32, v32, v32 row_half_mirror row_mask:0xf bank_mask:0xf bound_ctrl:1
	v_cndmask_b32_e64 v49, v63, v32, s[4:5]
	v_cvt_f32_i32_sdwa v32, sext(v24) dst_sel:DWORD dst_unused:UNUSED_PAD src0_sel:BYTE_0
	v_cvt_f32_i32_sdwa v55, sext(v25) dst_sel:DWORD dst_unused:UNUSED_PAD src0_sel:BYTE_2
	v_cvt_f32_i32_sdwa v61, sext(v26) dst_sel:DWORD dst_unused:UNUSED_PAD src0_sel:BYTE_3
	v_cvt_f32_i32_sdwa v62, sext(v27) dst_sel:DWORD dst_unused:UNUSED_PAD src0_sel:BYTE_3
	v_fma_f32 v54, v32, v0, 0
	v_fmac_f32_e32 v54, v33, v8
	v_cvt_f32_i32_sdwa v32, sext(v24) dst_sel:DWORD dst_unused:UNUSED_PAD src0_sel:BYTE_1
	v_fmac_f32_e32 v54, v35, v12
	v_cvt_f32_i32_sdwa v33, sext(v25) dst_sel:DWORD dst_unused:UNUSED_PAD src0_sel:BYTE_1
	v_fmac_f32_e32 v54, v52, v4
	v_cvt_f32_i32_sdwa v52, sext(v26) dst_sel:DWORD dst_unused:UNUSED_PAD src0_sel:BYTE_1
	v_fmac_f32_e32 v54, v32, v1
	v_fmac_f32_e32 v54, v33, v9
	s_waitcnt lgkmcnt(0)
	v_ashrrev_i32_e32 v35, 31, v34
	v_fmac_f32_e32 v54, v52, v13
	v_cvt_f32_i32_sdwa v52, sext(v27) dst_sel:DWORD dst_unused:UNUSED_PAD src0_sel:BYTE_1
	v_lshlrev_b64 v[32:33], 7, v[34:35]
	v_cvt_f32_i32_sdwa v34, sext(v26) dst_sel:DWORD dst_unused:UNUSED_PAD src0_sel:BYTE_2
	v_cvt_f32_i32_sdwa v35, sext(v27) dst_sel:DWORD dst_unused:UNUSED_PAD src0_sel:BYTE_2
	v_fmac_f32_e32 v54, v52, v5
	v_fmac_f32_e32 v54, v53, v2
	v_cvt_f32_i32_sdwa v24, sext(v24) dst_sel:DWORD dst_unused:UNUSED_PAD src0_sel:BYTE_3
	v_fmac_f32_e32 v54, v55, v10
	v_fmac_f32_e32 v54, v34, v14
	v_fmac_f32_e32 v54, v35, v6
	v_lshl_add_u64 v[52:53], v[42:43], 0, v[32:33]
	v_fmac_f32_e32 v54, v24, v3
	v_cvt_f32_i32_sdwa v55, sext(v25) dst_sel:DWORD dst_unused:UNUSED_PAD src0_sel:BYTE_3
	global_load_dwordx4 v[24:27], v[50:51], off
	global_load_dwordx4 v[32:35], v[52:53], off
	v_add_u32_dpp v50, v60, v60 quad_perm:[1,0,3,2] row_mask:0xf bank_mask:0xf bound_ctrl:1
	s_waitcnt vmcnt(5)
	v_cvt_f32_i32_sdwa v52, sext(v38) dst_sel:DWORD dst_unused:UNUSED_PAD src0_sel:BYTE_0
	v_fmac_f32_e32 v54, v55, v11
	v_fmac_f32_e32 v54, v61, v15
	v_fmac_f32_e32 v54, v62, v7
	v_add_u32_dpp v50, v50, v50 quad_perm:[2,3,0,1] row_mask:0xf bank_mask:0xf bound_ctrl:1
	v_cvt_f32_i32_sdwa v53, sext(v39) dst_sel:DWORD dst_unused:UNUSED_PAD src0_sel:BYTE_0
	v_add_f32_dpp v51, v54, v54 quad_perm:[1,0,3,2] row_mask:0xf bank_mask:0xf bound_ctrl:1
	v_add_u32_dpp v50, v50, v50 row_half_mirror row_mask:0xf bank_mask:0xf bound_ctrl:1
	v_cndmask_b32_e64 v49, v49, v50, s[6:7]
	v_add_f32_dpp v51, v51, v51 quad_perm:[2,3,0,1] row_mask:0xf bank_mask:0xf bound_ctrl:1
	v_cvt_f32_i32_sdwa v50, sext(v36) dst_sel:DWORD dst_unused:UNUSED_PAD src0_sel:BYTE_0
	v_mov_b32_e32 v54, v41
	v_add_f32_dpp v51, v51, v51 row_half_mirror row_mask:0xf bank_mask:0xf bound_ctrl:1
	v_cndmask_b32_e64 v40, v40, v51, s[6:7]
	v_cvt_f32_i32_sdwa v51, sext(v37) dst_sel:DWORD dst_unused:UNUSED_PAD src0_sel:BYTE_0
	v_fma_f32 v50, v50, v0, 0
	s_waitcnt vmcnt(4)
	v_dot4c_i32_i8_e32 v54, v36, v56
	v_dot4c_i32_i8_e32 v54, v37, v57
	v_fmac_f32_e32 v50, v51, v8
	v_cvt_f32_i32_sdwa v51, sext(v36) dst_sel:DWORD dst_unused:UNUSED_PAD src0_sel:BYTE_1
	v_fmac_f32_e32 v50, v52, v12
	v_cvt_f32_i32_sdwa v52, sext(v37) dst_sel:DWORD dst_unused:UNUSED_PAD src0_sel:BYTE_1
	v_fmac_f32_e32 v50, v53, v4
	v_cvt_f32_i32_sdwa v53, sext(v38) dst_sel:DWORD dst_unused:UNUSED_PAD src0_sel:BYTE_1
	v_fmac_f32_e32 v50, v51, v1
	v_cvt_f32_i32_sdwa v51, sext(v39) dst_sel:DWORD dst_unused:UNUSED_PAD src0_sel:BYTE_1
	v_fmac_f32_e32 v50, v52, v9
	v_cvt_f32_i32_sdwa v52, sext(v36) dst_sel:DWORD dst_unused:UNUSED_PAD src0_sel:BYTE_2
	v_fmac_f32_e32 v50, v53, v13
	v_cvt_f32_i32_sdwa v53, sext(v37) dst_sel:DWORD dst_unused:UNUSED_PAD src0_sel:BYTE_2
	v_fmac_f32_e32 v50, v51, v5
	v_cvt_f32_i32_sdwa v51, sext(v38) dst_sel:DWORD dst_unused:UNUSED_PAD src0_sel:BYTE_2
	v_fmac_f32_e32 v50, v52, v2
	v_cvt_f32_i32_sdwa v52, sext(v39) dst_sel:DWORD dst_unused:UNUSED_PAD src0_sel:BYTE_2
	v_cvt_f32_i32_sdwa v36, sext(v36) dst_sel:DWORD dst_unused:UNUSED_PAD src0_sel:BYTE_3
	v_fmac_f32_e32 v50, v53, v10
	v_fmac_f32_e32 v50, v51, v14
	v_fmac_f32_e32 v50, v52, v6
	v_fmac_f32_e32 v50, v36, v3
	v_cvt_f32_i32_sdwa v36, sext(v37) dst_sel:DWORD dst_unused:UNUSED_PAD src0_sel:BYTE_3
	v_cvt_f32_i32_sdwa v37, sext(v38) dst_sel:DWORD dst_unused:UNUSED_PAD src0_sel:BYTE_3
	v_dot4c_i32_i8_e32 v54, v38, v58
	v_mov_b32_e32 v38, v41
	v_cvt_f32_i32_sdwa v51, sext(v39) dst_sel:DWORD dst_unused:UNUSED_PAD src0_sel:BYTE_3
	s_waitcnt vmcnt(2)
	v_dot4c_i32_i8_e32 v38, v16, v20
	v_cvt_f32_i32_sdwa v20, sext(v16) dst_sel:DWORD dst_unused:UNUSED_PAD src0_sel:BYTE_0
	v_dot4c_i32_i8_e32 v38, v17, v21
	v_cvt_f32_i32_sdwa v21, sext(v17) dst_sel:DWORD dst_unused:UNUSED_PAD src0_sel:BYTE_0
	v_fmac_f32_e32 v50, v36, v11
	v_dot4c_i32_i8_e32 v38, v18, v22
	v_cvt_f32_i32_sdwa v22, sext(v18) dst_sel:DWORD dst_unused:UNUSED_PAD src0_sel:BYTE_0
	v_fmac_f32_e32 v50, v37, v15
	v_dot4c_i32_i8_e32 v54, v39, v59
	v_cvt_f32_i32_sdwa v39, sext(v19) dst_sel:DWORD dst_unused:UNUSED_PAD src0_sel:BYTE_0
	v_fmac_f32_e32 v50, v51, v7
	v_fma_f32 v20, v20, v0, 0
	v_fmac_f32_e32 v20, v21, v8
	v_add_f32_dpp v37, v50, v50 quad_perm:[1,0,3,2] row_mask:0xf bank_mask:0xf bound_ctrl:1
	v_cvt_f32_i32_sdwa v21, sext(v16) dst_sel:DWORD dst_unused:UNUSED_PAD src0_sel:BYTE_1
	v_fmac_f32_e32 v20, v22, v12
	v_add_f32_dpp v37, v37, v37 quad_perm:[2,3,0,1] row_mask:0xf bank_mask:0xf bound_ctrl:1
	v_cvt_f32_i32_sdwa v22, sext(v17) dst_sel:DWORD dst_unused:UNUSED_PAD src0_sel:BYTE_1
	v_fmac_f32_e32 v20, v39, v4
	v_add_f32_dpp v37, v37, v37 row_half_mirror row_mask:0xf bank_mask:0xf bound_ctrl:1
	v_cvt_f32_i32_sdwa v39, sext(v18) dst_sel:DWORD dst_unused:UNUSED_PAD src0_sel:BYTE_1
	v_cndmask_b32_e64 v37, v40, v37, s[8:9]
	v_cvt_f32_i32_sdwa v40, sext(v19) dst_sel:DWORD dst_unused:UNUSED_PAD src0_sel:BYTE_1
	v_fmac_f32_e32 v20, v21, v1
	v_cvt_f32_i32_sdwa v21, sext(v16) dst_sel:DWORD dst_unused:UNUSED_PAD src0_sel:BYTE_2
	v_fmac_f32_e32 v20, v22, v9
	v_cvt_f32_i32_sdwa v22, sext(v17) dst_sel:DWORD dst_unused:UNUSED_PAD src0_sel:BYTE_2
	v_fmac_f32_e32 v20, v39, v13
	v_cvt_f32_i32_sdwa v39, sext(v18) dst_sel:DWORD dst_unused:UNUSED_PAD src0_sel:BYTE_2
	v_fmac_f32_e32 v20, v40, v5
	v_cvt_f32_i32_sdwa v40, sext(v19) dst_sel:DWORD dst_unused:UNUSED_PAD src0_sel:BYTE_2
	v_fmac_f32_e32 v20, v21, v2
	v_cvt_f32_i32_sdwa v16, sext(v16) dst_sel:DWORD dst_unused:UNUSED_PAD src0_sel:BYTE_3
	v_fmac_f32_e32 v20, v22, v10
	v_cvt_f32_i32_sdwa v17, sext(v17) dst_sel:DWORD dst_unused:UNUSED_PAD src0_sel:BYTE_3
	v_fmac_f32_e32 v20, v39, v14
	v_cvt_f32_i32_sdwa v18, sext(v18) dst_sel:DWORD dst_unused:UNUSED_PAD src0_sel:BYTE_3
	v_fmac_f32_e32 v20, v40, v6
	v_cvt_f32_i32_sdwa v21, sext(v19) dst_sel:DWORD dst_unused:UNUSED_PAD src0_sel:BYTE_3
	v_fmac_f32_e32 v20, v16, v3
	v_fmac_f32_e32 v20, v17, v11
	v_fmac_f32_e32 v20, v18, v15
	v_fmac_f32_e32 v20, v21, v7
	v_dot4c_i32_i8_e32 v38, v19, v23
	s_waitcnt vmcnt(1)
	v_cvt_f32_i32_sdwa v19, sext(v24) dst_sel:DWORD dst_unused:UNUSED_PAD src0_sel:BYTE_0
	v_add_f32_dpp v17, v20, v20 quad_perm:[1,0,3,2] row_mask:0xf bank_mask:0xf bound_ctrl:1
	v_cvt_f32_i32_sdwa v20, sext(v25) dst_sel:DWORD dst_unused:UNUSED_PAD src0_sel:BYTE_0
	v_cvt_f32_i32_sdwa v21, sext(v26) dst_sel:DWORD dst_unused:UNUSED_PAD src0_sel:BYTE_0
	v_cvt_f32_i32_sdwa v22, sext(v27) dst_sel:DWORD dst_unused:UNUSED_PAD src0_sel:BYTE_0
	v_fma_f32 v19, v19, v0, 0
	v_fmac_f32_e32 v19, v20, v8
	v_cvt_f32_i32_sdwa v20, sext(v24) dst_sel:DWORD dst_unused:UNUSED_PAD src0_sel:BYTE_1
	v_fmac_f32_e32 v19, v21, v12
	v_cvt_f32_i32_sdwa v21, sext(v25) dst_sel:DWORD dst_unused:UNUSED_PAD src0_sel:BYTE_1
	v_fmac_f32_e32 v19, v22, v4
	v_cvt_f32_i32_sdwa v22, sext(v26) dst_sel:DWORD dst_unused:UNUSED_PAD src0_sel:BYTE_1
	v_cvt_f32_i32_sdwa v23, sext(v27) dst_sel:DWORD dst_unused:UNUSED_PAD src0_sel:BYTE_1
	v_add_u32_dpp v36, v54, v54 quad_perm:[1,0,3,2] row_mask:0xf bank_mask:0xf bound_ctrl:1
	v_fmac_f32_e32 v19, v20, v1
	v_cvt_f32_i32_sdwa v20, sext(v24) dst_sel:DWORD dst_unused:UNUSED_PAD src0_sel:BYTE_2
	v_add_u32_dpp v36, v36, v36 quad_perm:[2,3,0,1] row_mask:0xf bank_mask:0xf bound_ctrl:1
	v_add_u32_dpp v16, v38, v38 quad_perm:[1,0,3,2] row_mask:0xf bank_mask:0xf bound_ctrl:1
	v_fmac_f32_e32 v19, v21, v9
	v_cvt_f32_i32_sdwa v21, sext(v25) dst_sel:DWORD dst_unused:UNUSED_PAD src0_sel:BYTE_2
	v_add_u32_dpp v36, v36, v36 row_half_mirror row_mask:0xf bank_mask:0xf bound_ctrl:1
	v_add_u32_dpp v16, v16, v16 quad_perm:[2,3,0,1] row_mask:0xf bank_mask:0xf bound_ctrl:1
	v_fmac_f32_e32 v19, v22, v13
	v_cvt_f32_i32_sdwa v22, sext(v26) dst_sel:DWORD dst_unused:UNUSED_PAD src0_sel:BYTE_2
	v_cndmask_b32_e64 v36, v49, v36, s[8:9]
	v_add_u32_dpp v16, v16, v16 row_half_mirror row_mask:0xf bank_mask:0xf bound_ctrl:1
	v_fmac_f32_e32 v19, v23, v5
	v_cvt_f32_i32_sdwa v23, sext(v27) dst_sel:DWORD dst_unused:UNUSED_PAD src0_sel:BYTE_2
	v_cndmask_b32_e64 v18, v36, v16, s[10:11]
	v_mov_b32_e32 v16, v41
	v_fmac_f32_e32 v19, v20, v2
	v_cvt_f32_i32_sdwa v20, sext(v24) dst_sel:DWORD dst_unused:UNUSED_PAD src0_sel:BYTE_3
	s_waitcnt vmcnt(0)
	v_dot4c_i32_i8_e32 v16, v24, v32
	v_fmac_f32_e32 v19, v21, v10
	v_cvt_f32_i32_sdwa v21, sext(v25) dst_sel:DWORD dst_unused:UNUSED_PAD src0_sel:BYTE_3
	v_dot4c_i32_i8_e32 v16, v25, v33
	v_fmac_f32_e32 v19, v22, v14
	v_cvt_f32_i32_sdwa v22, sext(v26) dst_sel:DWORD dst_unused:UNUSED_PAD src0_sel:BYTE_3
	v_dot4c_i32_i8_e32 v16, v26, v34
	v_fmac_f32_e32 v19, v23, v6
	v_cvt_f32_i32_sdwa v23, sext(v27) dst_sel:DWORD dst_unused:UNUSED_PAD src0_sel:BYTE_3
	v_fmac_f32_e32 v19, v20, v3
	v_dot4c_i32_i8_e32 v16, v27, v35
	v_fmac_f32_e32 v19, v21, v11
	v_fmac_f32_e32 v19, v22, v15
	v_fmac_f32_e32 v19, v23, v7
	v_add_u32_dpp v16, v16, v16 quad_perm:[1,0,3,2] row_mask:0xf bank_mask:0xf bound_ctrl:1
	v_add_f32_dpp v17, v17, v17 quad_perm:[2,3,0,1] row_mask:0xf bank_mask:0xf bound_ctrl:1
	v_add_f32_dpp v19, v19, v19 quad_perm:[1,0,3,2] row_mask:0xf bank_mask:0xf bound_ctrl:1
	v_add_u32_dpp v16, v16, v16 quad_perm:[2,3,0,1] row_mask:0xf bank_mask:0xf bound_ctrl:1
	v_add_f32_dpp v17, v17, v17 row_half_mirror row_mask:0xf bank_mask:0xf bound_ctrl:1
	v_add_f32_dpp v19, v19, v19 quad_perm:[2,3,0,1] row_mask:0xf bank_mask:0xf bound_ctrl:1
	v_add_u32_dpp v20, v16, v16 row_half_mirror row_mask:0xf bank_mask:0xf bound_ctrl:1
	ds_bpermute_b32 v16, v44, v48
	v_cndmask_b32_e64 v17, v37, v17, s[10:11]
	v_add_f32_dpp v19, v19, v19 row_half_mirror row_mask:0xf bank_mask:0xf bound_ctrl:1
	v_cndmask_b32_e64 v17, v17, v19, s[12:13]
	v_cndmask_b32_e64 v18, v18, v20, s[12:13]
	global_atomic_add v[28:29], v18, off offset:256
	global_atomic_add_f32 v[30:31], v17, off offset:256
	s_waitcnt lgkmcnt(0)
	v_ashrrev_i32_e32 v17, 31, v16
	v_lshlrev_b64 v[16:17], 7, v[16:17]
	v_lshl_add_u64 v[16:17], v[42:43], 0, v[16:17]
	global_load_dwordx4 v[24:27], v[16:17], off
	ds_bpermute_b32 v16, v44, v47
	ds_bpermute_b32 v18, v44, v48 offset:32
	ds_bpermute_b32 v20, v44, v47 offset:32
	s_waitcnt lgkmcnt(2)
	v_ashrrev_i32_e32 v17, 31, v16
	v_lshlrev_b64 v[16:17], 7, v[16:17]
	v_lshl_add_u64 v[16:17], v[42:43], 0, v[16:17]
	s_waitcnt lgkmcnt(1)
	v_ashrrev_i32_e32 v19, 31, v18
	global_load_dwordx4 v[32:35], v[16:17], off
	v_lshlrev_b64 v[16:17], 7, v[18:19]
	s_waitcnt lgkmcnt(0)
	v_ashrrev_i32_e32 v21, 31, v20
	v_lshl_add_u64 v[16:17], v[42:43], 0, v[16:17]
	v_lshlrev_b64 v[18:19], 7, v[20:21]
	v_lshl_add_u64 v[18:19], v[42:43], 0, v[18:19]
	global_load_dwordx4 v[36:39], v[16:17], off
	global_load_dwordx4 v[50:53], v[18:19], off
	ds_bpermute_b32 v16, v44, v48 offset:64
	ds_bpermute_b32 v18, v44, v47 offset:64
	s_waitcnt lgkmcnt(1)
	v_ashrrev_i32_e32 v17, 31, v16
	v_lshlrev_b64 v[16:17], 7, v[16:17]
	s_waitcnt lgkmcnt(0)
	v_ashrrev_i32_e32 v19, 31, v18
	v_lshl_add_u64 v[54:55], v[42:43], 0, v[16:17]
	v_lshlrev_b64 v[16:17], 7, v[18:19]
	v_lshl_add_u64 v[56:57], v[42:43], 0, v[16:17]
	global_load_dwordx4 v[16:19], v[54:55], off
	global_load_dwordx4 v[20:23], v[56:57], off
	ds_bpermute_b32 v54, v44, v48 offset:96
	ds_bpermute_b32 v56, v44, v47 offset:96
	s_waitcnt vmcnt(5)
	v_cvt_f32_i32_sdwa v40, sext(v24) dst_sel:DWORD dst_unused:UNUSED_PAD src0_sel:BYTE_0
	v_cvt_f32_i32_sdwa v49, sext(v25) dst_sel:DWORD dst_unused:UNUSED_PAD src0_sel:BYTE_0
	v_cvt_f32_i32_sdwa v55, sext(v26) dst_sel:DWORD dst_unused:UNUSED_PAD src0_sel:BYTE_0
	v_cvt_f32_i32_sdwa v57, sext(v24) dst_sel:DWORD dst_unused:UNUSED_PAD src0_sel:BYTE_1
	v_fma_f32 v40, v40, v0, 0
	v_fmac_f32_e32 v40, v49, v8
	v_cvt_f32_i32_sdwa v49, sext(v27) dst_sel:DWORD dst_unused:UNUSED_PAD src0_sel:BYTE_0
	v_fmac_f32_e32 v40, v55, v12
	v_cvt_f32_i32_sdwa v58, sext(v26) dst_sel:DWORD dst_unused:UNUSED_PAD src0_sel:BYTE_2
	s_waitcnt lgkmcnt(1)
	v_ashrrev_i32_e32 v55, 31, v54
	v_fmac_f32_e32 v40, v49, v4
	v_cvt_f32_i32_sdwa v49, sext(v25) dst_sel:DWORD dst_unused:UNUSED_PAD src0_sel:BYTE_1
	v_fmac_f32_e32 v40, v57, v1
	v_cvt_f32_i32_sdwa v57, sext(v26) dst_sel:DWORD dst_unused:UNUSED_PAD src0_sel:BYTE_1
	v_lshlrev_b64 v[54:55], 7, v[54:55]
	v_fmac_f32_e32 v40, v49, v9
	v_cvt_f32_i32_sdwa v49, sext(v27) dst_sel:DWORD dst_unused:UNUSED_PAD src0_sel:BYTE_1
	v_fmac_f32_e32 v40, v57, v13
	v_cvt_f32_i32_sdwa v57, sext(v24) dst_sel:DWORD dst_unused:UNUSED_PAD src0_sel:BYTE_2
	v_lshl_add_u64 v[54:55], v[42:43], 0, v[54:55]
	v_fmac_f32_e32 v40, v49, v5
	v_cvt_f32_i32_sdwa v49, sext(v25) dst_sel:DWORD dst_unused:UNUSED_PAD src0_sel:BYTE_2
	v_fmac_f32_e32 v40, v57, v2
	s_waitcnt lgkmcnt(0)
	v_ashrrev_i32_e32 v57, 31, v56
	v_lshlrev_b64 v[56:57], 7, v[56:57]
	v_fmac_f32_e32 v40, v49, v10
	v_cvt_f32_i32_sdwa v49, sext(v27) dst_sel:DWORD dst_unused:UNUSED_PAD src0_sel:BYTE_2
	v_fmac_f32_e32 v40, v58, v14
	v_cvt_f32_i32_sdwa v58, sext(v24) dst_sel:DWORD dst_unused:UNUSED_PAD src0_sel:BYTE_3
	v_lshl_add_u64 v[56:57], v[42:43], 0, v[56:57]
	v_fmac_f32_e32 v40, v49, v6
	v_cvt_f32_i32_sdwa v49, sext(v25) dst_sel:DWORD dst_unused:UNUSED_PAD src0_sel:BYTE_3
	v_fmac_f32_e32 v40, v58, v3
	v_cvt_f32_i32_sdwa v58, sext(v26) dst_sel:DWORD dst_unused:UNUSED_PAD src0_sel:BYTE_3
	s_waitcnt vmcnt(3)
	v_cvt_f32_i32_sdwa v59, sext(v39) dst_sel:DWORD dst_unused:UNUSED_PAD src0_sel:BYTE_1
	v_fmac_f32_e32 v40, v49, v11
	v_mov_b32_e32 v49, v41
	v_fmac_f32_e32 v40, v58, v15
	v_cvt_f32_i32_sdwa v58, sext(v27) dst_sel:DWORD dst_unused:UNUSED_PAD src0_sel:BYTE_3
	v_dot4c_i32_i8_e32 v49, v24, v32
	v_cvt_f32_i32_sdwa v24, sext(v36) dst_sel:DWORD dst_unused:UNUSED_PAD src0_sel:BYTE_0
	v_dot4c_i32_i8_e32 v49, v25, v33
	v_fmac_f32_e32 v40, v58, v7
	v_mov_b32_e32 v58, v41
	s_waitcnt vmcnt(2)
	v_dot4c_i32_i8_e32 v58, v36, v50
	v_dot4c_i32_i8_e32 v58, v37, v51
	v_fma_f32 v51, v24, v0, 0
	v_cvt_f32_i32_sdwa v24, sext(v37) dst_sel:DWORD dst_unused:UNUSED_PAD src0_sel:BYTE_0
	v_cvt_f32_i32_sdwa v25, sext(v38) dst_sel:DWORD dst_unused:UNUSED_PAD src0_sel:BYTE_0
	v_dot4c_i32_i8_e32 v49, v26, v34
	v_cvt_f32_i32_sdwa v26, sext(v39) dst_sel:DWORD dst_unused:UNUSED_PAD src0_sel:BYTE_0
	v_dot4c_i32_i8_e32 v49, v27, v35
	v_cvt_f32_i32_sdwa v27, sext(v36) dst_sel:DWORD dst_unused:UNUSED_PAD src0_sel:BYTE_1
	v_fmac_f32_e32 v51, v24, v8
	v_fmac_f32_e32 v51, v25, v12
	v_fmac_f32_e32 v51, v26, v4
	v_fmac_f32_e32 v51, v27, v1
	global_load_dwordx4 v[24:27], v[54:55], off
	global_load_dwordx4 v[32:35], v[56:57], off
	v_cvt_f32_i32_sdwa v50, sext(v37) dst_sel:DWORD dst_unused:UNUSED_PAD src0_sel:BYTE_1
	v_dot4c_i32_i8_e32 v58, v38, v52
	v_cvt_f32_i32_sdwa v52, sext(v38) dst_sel:DWORD dst_unused:UNUSED_PAD src0_sel:BYTE_1
	v_cvt_f32_i32_sdwa v60, sext(v36) dst_sel:DWORD dst_unused:UNUSED_PAD src0_sel:BYTE_2
	v_cvt_f32_i32_sdwa v61, sext(v37) dst_sel:DWORD dst_unused:UNUSED_PAD src0_sel:BYTE_2
	v_fmac_f32_e32 v51, v50, v9
	v_cvt_f32_i32_sdwa v62, sext(v38) dst_sel:DWORD dst_unused:UNUSED_PAD src0_sel:BYTE_2
	v_fmac_f32_e32 v51, v52, v13
	v_cvt_f32_i32_sdwa v63, sext(v39) dst_sel:DWORD dst_unused:UNUSED_PAD src0_sel:BYTE_2
	v_fmac_f32_e32 v51, v59, v5
	v_dot4c_i32_i8_e32 v58, v39, v53
	v_cvt_f32_i32_sdwa v53, sext(v36) dst_sel:DWORD dst_unused:UNUSED_PAD src0_sel:BYTE_3
	v_fmac_f32_e32 v51, v60, v2
	v_cvt_f32_i32_sdwa v64, sext(v37) dst_sel:DWORD dst_unused:UNUSED_PAD src0_sel:BYTE_3
	v_fmac_f32_e32 v51, v61, v10
	v_cvt_f32_i32_sdwa v65, sext(v38) dst_sel:DWORD dst_unused:UNUSED_PAD src0_sel:BYTE_3
	v_fmac_f32_e32 v51, v62, v14
	v_cvt_f32_i32_sdwa v66, sext(v39) dst_sel:DWORD dst_unused:UNUSED_PAD src0_sel:BYTE_3
	v_fmac_f32_e32 v51, v63, v6
	v_fmac_f32_e32 v51, v53, v3
	v_fmac_f32_e32 v51, v64, v11
	v_fmac_f32_e32 v51, v65, v15
	v_add_f32_dpp v40, v40, v40 quad_perm:[1,0,3,2] row_mask:0xf bank_mask:0xf bound_ctrl:1
	v_fmac_f32_e32 v51, v66, v7
	v_add_u32_dpp v49, v49, v49 quad_perm:[1,0,3,2] row_mask:0xf bank_mask:0xf bound_ctrl:1
	v_add_f32_dpp v40, v40, v40 quad_perm:[2,3,0,1] row_mask:0xf bank_mask:0xf bound_ctrl:1
	v_add_f32_dpp v51, v51, v51 quad_perm:[1,0,3,2] row_mask:0xf bank_mask:0xf bound_ctrl:1
	v_add_u32_dpp v49, v49, v49 quad_perm:[2,3,0,1] row_mask:0xf bank_mask:0xf bound_ctrl:1
	v_add_f32_dpp v40, v40, v40 row_half_mirror row_mask:0xf bank_mask:0xf bound_ctrl:1
	v_add_u32_dpp v53, v58, v58 quad_perm:[1,0,3,2] row_mask:0xf bank_mask:0xf bound_ctrl:1
	v_add_f32_dpp v51, v51, v51 quad_perm:[2,3,0,1] row_mask:0xf bank_mask:0xf bound_ctrl:1
	v_add_u32_dpp v49, v49, v49 row_half_mirror row_mask:0xf bank_mask:0xf bound_ctrl:1
	v_cndmask_b32_e32 v40, 0, v40, vcc
	v_add_u32_dpp v53, v53, v53 quad_perm:[2,3,0,1] row_mask:0xf bank_mask:0xf bound_ctrl:1
	v_add_f32_dpp v51, v51, v51 row_half_mirror row_mask:0xf bank_mask:0xf bound_ctrl:1
	v_cndmask_b32_e32 v49, 0, v49, vcc
	v_add_u32_dpp v53, v53, v53 row_half_mirror row_mask:0xf bank_mask:0xf bound_ctrl:1
	v_cndmask_b32_e64 v40, v40, v51, s[0:1]
	s_waitcnt vmcnt(3)
	v_cvt_f32_i32_sdwa v51, sext(v16) dst_sel:DWORD dst_unused:UNUSED_PAD src0_sel:BYTE_0
	v_cndmask_b32_e64 v49, v49, v53, s[0:1]
	v_cvt_f32_i32_sdwa v53, sext(v17) dst_sel:DWORD dst_unused:UNUSED_PAD src0_sel:BYTE_0
	v_mov_b32_e32 v58, v41
	v_cvt_f32_i32_sdwa v54, sext(v18) dst_sel:DWORD dst_unused:UNUSED_PAD src0_sel:BYTE_0
	s_waitcnt vmcnt(2)
	v_dot4c_i32_i8_e32 v58, v16, v20
	v_cvt_f32_i32_sdwa v20, sext(v19) dst_sel:DWORD dst_unused:UNUSED_PAD src0_sel:BYTE_0
	ds_bpermute_b32 v36, v44, v48 offset:128
	v_fma_f32 v59, v51, v0, 0
	ds_bpermute_b32 v38, v44, v47 offset:128
	v_fmac_f32_e32 v59, v53, v8
	v_cvt_f32_i32_sdwa v51, sext(v16) dst_sel:DWORD dst_unused:UNUSED_PAD src0_sel:BYTE_1
	v_fmac_f32_e32 v59, v54, v12
	v_cvt_f32_i32_sdwa v53, sext(v17) dst_sel:DWORD dst_unused:UNUSED_PAD src0_sel:BYTE_1
	v_fmac_f32_e32 v59, v20, v4
	v_cvt_f32_i32_sdwa v20, sext(v18) dst_sel:DWORD dst_unused:UNUSED_PAD src0_sel:BYTE_1
	v_dot4c_i32_i8_e32 v58, v17, v21
	v_cvt_f32_i32_sdwa v21, sext(v19) dst_sel:DWORD dst_unused:UNUSED_PAD src0_sel:BYTE_1
	s_waitcnt lgkmcnt(1)
	v_ashrrev_i32_e32 v37, 31, v36
	v_fmac_f32_e32 v59, v51, v1
	v_lshlrev_b64 v[36:37], 7, v[36:37]
	s_waitcnt lgkmcnt(0)
	v_ashrrev_i32_e32 v39, 31, v38
	v_fmac_f32_e32 v59, v53, v9
	v_lshl_add_u64 v[36:37], v[42:43], 0, v[36:37]
	v_lshlrev_b64 v[38:39], 7, v[38:39]
	v_dot4c_i32_i8_e32 v58, v18, v22
	v_fmac_f32_e32 v59, v20, v13
	v_lshl_add_u64 v[38:39], v[42:43], 0, v[38:39]
	v_cvt_f32_i32_sdwa v51, sext(v16) dst_sel:DWORD dst_unused:UNUSED_PAD src0_sel:BYTE_2
	v_fmac_f32_e32 v59, v21, v5
	v_cvt_f32_i32_sdwa v54, sext(v17) dst_sel:DWORD dst_unused:UNUSED_PAD src0_sel:BYTE_2
	v_cvt_f32_i32_sdwa v55, sext(v18) dst_sel:DWORD dst_unused:UNUSED_PAD src0_sel:BYTE_2
	v_cvt_f32_i32_sdwa v56, sext(v19) dst_sel:DWORD dst_unused:UNUSED_PAD src0_sel:BYTE_2
	v_dot4c_i32_i8_e32 v58, v19, v23
	v_cvt_f32_i32_sdwa v57, sext(v16) dst_sel:DWORD dst_unused:UNUSED_PAD src0_sel:BYTE_3
	v_cvt_f32_i32_sdwa v60, sext(v17) dst_sel:DWORD dst_unused:UNUSED_PAD src0_sel:BYTE_3
	v_cvt_f32_i32_sdwa v61, sext(v18) dst_sel:DWORD dst_unused:UNUSED_PAD src0_sel:BYTE_3
	v_cvt_f32_i32_sdwa v62, sext(v19) dst_sel:DWORD dst_unused:UNUSED_PAD src0_sel:BYTE_3
	global_load_dwordx4 v[16:19], v[36:37], off
	global_load_dwordx4 v[20:23], v[38:39], off
	v_fmac_f32_e32 v59, v51, v2
	ds_bpermute_b32 v50, v44, v48 offset:160
	v_fmac_f32_e32 v59, v54, v10
	ds_bpermute_b32 v52, v44, v47 offset:160
	v_fmac_f32_e32 v59, v55, v14
	ds_bpermute_b32 v54, v44, v48 offset:192
	v_fmac_f32_e32 v59, v56, v6
	v_fmac_f32_e32 v59, v57, v3
	ds_bpermute_b32 v56, v44, v47 offset:192
	v_fmac_f32_e32 v59, v60, v11
	v_mov_b32_e32 v60, v41
	s_waitcnt lgkmcnt(3)
	v_ashrrev_i32_e32 v51, 31, v50
	s_waitcnt vmcnt(2)
	v_dot4c_i32_i8_e32 v60, v24, v32
	v_lshlrev_b64 v[36:37], 7, v[50:51]
	s_waitcnt lgkmcnt(2)
	v_ashrrev_i32_e32 v53, 31, v52
	v_dot4c_i32_i8_e32 v60, v25, v33
	v_lshl_add_u64 v[50:51], v[42:43], 0, v[36:37]
	v_lshlrev_b64 v[36:37], 7, v[52:53]
	v_dot4c_i32_i8_e32 v60, v26, v34
	s_waitcnt lgkmcnt(1)
	v_ashrrev_i32_e32 v55, 31, v54
	v_lshl_add_u64 v[52:53], v[42:43], 0, v[36:37]
	v_dot4c_i32_i8_e32 v60, v27, v35
	global_load_dwordx4 v[32:35], v[50:51], off
	global_load_dwordx4 v[36:39], v[52:53], off
	v_lshlrev_b64 v[50:51], 7, v[54:55]
	s_waitcnt lgkmcnt(0)
	v_ashrrev_i32_e32 v57, 31, v56
	v_fmac_f32_e32 v59, v61, v15
	v_lshl_add_u64 v[52:53], v[42:43], 0, v[50:51]
	v_lshlrev_b64 v[50:51], 7, v[56:57]
	v_fmac_f32_e32 v59, v62, v7
	v_lshl_add_u64 v[54:55], v[42:43], 0, v[50:51]
	v_add_u32_dpp v50, v58, v58 quad_perm:[1,0,3,2] row_mask:0xf bank_mask:0xf bound_ctrl:1
	v_add_f32_dpp v51, v59, v59 quad_perm:[1,0,3,2] row_mask:0xf bank_mask:0xf bound_ctrl:1
	v_cvt_f32_i32_sdwa v56, sext(v25) dst_sel:DWORD dst_unused:UNUSED_PAD src0_sel:BYTE_0
	v_add_u32_dpp v50, v50, v50 quad_perm:[2,3,0,1] row_mask:0xf bank_mask:0xf bound_ctrl:1
	v_add_f32_dpp v51, v51, v51 quad_perm:[2,3,0,1] row_mask:0xf bank_mask:0xf bound_ctrl:1
	v_cvt_f32_i32_sdwa v57, sext(v26) dst_sel:DWORD dst_unused:UNUSED_PAD src0_sel:BYTE_3
	v_add_u32_dpp v50, v50, v50 row_half_mirror row_mask:0xf bank_mask:0xf bound_ctrl:1
	v_add_f32_dpp v51, v51, v51 row_half_mirror row_mask:0xf bank_mask:0xf bound_ctrl:1
	v_cndmask_b32_e64 v40, v40, v51, s[2:3]
	v_cvt_f32_i32_sdwa v51, sext(v24) dst_sel:DWORD dst_unused:UNUSED_PAD src0_sel:BYTE_0
	v_cndmask_b32_e64 v58, v49, v50, s[2:3]
	v_cvt_f32_i32_sdwa v49, sext(v26) dst_sel:DWORD dst_unused:UNUSED_PAD src0_sel:BYTE_0
	v_cvt_f32_i32_sdwa v50, sext(v27) dst_sel:DWORD dst_unused:UNUSED_PAD src0_sel:BYTE_0
	v_fma_f32 v59, v51, v0, 0
	v_fmac_f32_e32 v59, v56, v8
	v_fmac_f32_e32 v59, v49, v12
	v_cvt_f32_i32_sdwa v49, sext(v24) dst_sel:DWORD dst_unused:UNUSED_PAD src0_sel:BYTE_1
	v_cvt_f32_i32_sdwa v51, sext(v25) dst_sel:DWORD dst_unused:UNUSED_PAD src0_sel:BYTE_1
	v_fmac_f32_e32 v59, v50, v4
	v_cvt_f32_i32_sdwa v50, sext(v26) dst_sel:DWORD dst_unused:UNUSED_PAD src0_sel:BYTE_1
	v_fmac_f32_e32 v59, v49, v1
	v_fmac_f32_e32 v59, v51, v9
	v_cvt_f32_i32_sdwa v49, sext(v27) dst_sel:DWORD dst_unused:UNUSED_PAD src0_sel:BYTE_1
	v_fmac_f32_e32 v59, v50, v13
	v_cvt_f32_i32_sdwa v50, sext(v24) dst_sel:DWORD dst_unused:UNUSED_PAD src0_sel:BYTE_2
	v_cvt_f32_i32_sdwa v51, sext(v25) dst_sel:DWORD dst_unused:UNUSED_PAD src0_sel:BYTE_2
	v_fmac_f32_e32 v59, v49, v5
	v_cvt_f32_i32_sdwa v49, sext(v26) dst_sel:DWORD dst_unused:UNUSED_PAD src0_sel:BYTE_2
	v_fmac_f32_e32 v59, v50, v2
	v_cvt_f32_i32_sdwa v50, sext(v27) dst_sel:DWORD dst_unused:UNUSED_PAD src0_sel:BYTE_2
	v_cvt_f32_i32_sdwa v24, sext(v24) dst_sel:DWORD dst_unused:UNUSED_PAD src0_sel:BYTE_3
	v_fmac_f32_e32 v59, v51, v10
	v_cvt_f32_i32_sdwa v25, sext(v25) dst_sel:DWORD dst_unused:UNUSED_PAD src0_sel:BYTE_3
	v_fmac_f32_e32 v59, v49, v14
	v_fmac_f32_e32 v59, v50, v6
	v_cvt_f32_i32_sdwa v61, sext(v27) dst_sel:DWORD dst_unused:UNUSED_PAD src0_sel:BYTE_3
	ds_bpermute_b32 v56, v44, v48 offset:224
	v_fmac_f32_e32 v59, v24, v3
	v_fmac_f32_e32 v59, v25, v11
	v_fmac_f32_e32 v59, v57, v15
	v_fmac_f32_e32 v59, v61, v7
	global_load_dwordx4 v[24:27], v[52:53], off
	global_load_dwordx4 v[48:51], v[54:55], off
	v_add_f32_dpp v53, v59, v59 quad_perm:[1,0,3,2] row_mask:0xf bank_mask:0xf bound_ctrl:1
	s_waitcnt lgkmcnt(0)
	v_ashrrev_i32_e32 v57, 31, v56
	v_lshlrev_b64 v[54:55], 7, v[56:57]
	v_add_f32_dpp v53, v53, v53 quad_perm:[2,3,0,1] row_mask:0xf bank_mask:0xf bound_ctrl:1
	ds_bpermute_b32 v52, v44, v47 offset:224
	v_add_u32_dpp v47, v60, v60 quad_perm:[1,0,3,2] row_mask:0xf bank_mask:0xf bound_ctrl:1
	v_add_f32_dpp v53, v53, v53 row_half_mirror row_mask:0xf bank_mask:0xf bound_ctrl:1
	s_waitcnt vmcnt(5)
	v_cvt_f32_i32_sdwa v56, sext(v16) dst_sel:DWORD dst_unused:UNUSED_PAD src0_sel:BYTE_0
	v_cndmask_b32_e64 v40, v40, v53, s[4:5]
	v_cvt_f32_i32_sdwa v53, sext(v17) dst_sel:DWORD dst_unused:UNUSED_PAD src0_sel:BYTE_0
	v_cvt_f32_i32_sdwa v57, sext(v18) dst_sel:DWORD dst_unused:UNUSED_PAD src0_sel:BYTE_0
	v_fma_f32 v56, v56, v0, 0
	v_add_u32_dpp v47, v47, v47 quad_perm:[2,3,0,1] row_mask:0xf bank_mask:0xf bound_ctrl:1
	v_fmac_f32_e32 v56, v53, v8
	v_cvt_f32_i32_sdwa v53, sext(v19) dst_sel:DWORD dst_unused:UNUSED_PAD src0_sel:BYTE_0
	v_add_u32_dpp v47, v47, v47 row_half_mirror row_mask:0xf bank_mask:0xf bound_ctrl:1
	v_fmac_f32_e32 v56, v57, v12
	v_cvt_f32_i32_sdwa v57, sext(v16) dst_sel:DWORD dst_unused:UNUSED_PAD src0_sel:BYTE_1
	v_cndmask_b32_e64 v47, v58, v47, s[4:5]
	v_cvt_f32_i32_sdwa v58, sext(v17) dst_sel:DWORD dst_unused:UNUSED_PAD src0_sel:BYTE_1
	v_fmac_f32_e32 v56, v53, v4
	v_fmac_f32_e32 v56, v57, v1
	v_cvt_f32_i32_sdwa v57, sext(v18) dst_sel:DWORD dst_unused:UNUSED_PAD src0_sel:BYTE_1
	v_fmac_f32_e32 v56, v58, v9
	v_cvt_f32_i32_sdwa v58, sext(v19) dst_sel:DWORD dst_unused:UNUSED_PAD src0_sel:BYTE_1
	s_waitcnt lgkmcnt(0)
	v_ashrrev_i32_e32 v53, 31, v52
	v_fmac_f32_e32 v56, v57, v13
	v_cvt_f32_i32_sdwa v57, sext(v16) dst_sel:DWORD dst_unused:UNUSED_PAD src0_sel:BYTE_2
	v_fmac_f32_e32 v56, v58, v5
	v_cvt_f32_i32_sdwa v58, sext(v17) dst_sel:DWORD dst_unused:UNUSED_PAD src0_sel:BYTE_2
	v_lshl_add_u64 v[54:55], v[42:43], 0, v[54:55]
	v_fmac_f32_e32 v56, v57, v2
	v_mov_b32_e32 v57, v41
	v_fmac_f32_e32 v56, v58, v10
	v_cvt_f32_i32_sdwa v58, sext(v18) dst_sel:DWORD dst_unused:UNUSED_PAD src0_sel:BYTE_2
	s_waitcnt vmcnt(4)
	v_dot4c_i32_i8_e32 v57, v16, v20
	v_dot4c_i32_i8_e32 v57, v17, v21
	v_lshlrev_b64 v[52:53], 7, v[52:53]
	v_dot4c_i32_i8_e32 v57, v18, v22
	v_lshl_add_u64 v[52:53], v[42:43], 0, v[52:53]
	v_fmac_f32_e32 v56, v58, v14
	v_cvt_f32_i32_sdwa v58, sext(v19) dst_sel:DWORD dst_unused:UNUSED_PAD src0_sel:BYTE_2
	v_dot4c_i32_i8_e32 v57, v19, v23
	v_cvt_f32_i32_sdwa v59, sext(v16) dst_sel:DWORD dst_unused:UNUSED_PAD src0_sel:BYTE_3
	v_cvt_f32_i32_sdwa v60, sext(v17) dst_sel:DWORD dst_unused:UNUSED_PAD src0_sel:BYTE_3
	v_cvt_f32_i32_sdwa v61, sext(v18) dst_sel:DWORD dst_unused:UNUSED_PAD src0_sel:BYTE_3
	v_cvt_f32_i32_sdwa v62, sext(v19) dst_sel:DWORD dst_unused:UNUSED_PAD src0_sel:BYTE_3
	global_load_dwordx4 v[16:19], v[54:55], off
	global_load_dwordx4 v[20:23], v[52:53], off
	v_fmac_f32_e32 v56, v58, v6
	v_fmac_f32_e32 v56, v59, v3
	v_add_u32_dpp v52, v57, v57 quad_perm:[1,0,3,2] row_mask:0xf bank_mask:0xf bound_ctrl:1
	v_fmac_f32_e32 v56, v60, v11
	v_fmac_f32_e32 v56, v61, v15
	v_add_u32_dpp v52, v52, v52 quad_perm:[2,3,0,1] row_mask:0xf bank_mask:0xf bound_ctrl:1
	v_fmac_f32_e32 v56, v62, v7
	s_waitcnt vmcnt(5)
	v_cvt_f32_i32_sdwa v54, sext(v35) dst_sel:DWORD dst_unused:UNUSED_PAD src0_sel:BYTE_1
	v_add_u32_dpp v52, v52, v52 row_half_mirror row_mask:0xf bank_mask:0xf bound_ctrl:1
	v_cndmask_b32_e64 v47, v47, v52, s[6:7]
	v_mov_b32_e32 v52, v41
	v_add_f32_dpp v53, v56, v56 quad_perm:[1,0,3,2] row_mask:0xf bank_mask:0xf bound_ctrl:1
	s_waitcnt vmcnt(4)
	v_dot4c_i32_i8_e32 v52, v32, v36
	v_cvt_f32_i32_sdwa v36, sext(v32) dst_sel:DWORD dst_unused:UNUSED_PAD src0_sel:BYTE_0
	v_add_f32_dpp v53, v53, v53 quad_perm:[2,3,0,1] row_mask:0xf bank_mask:0xf bound_ctrl:1
	v_dot4c_i32_i8_e32 v52, v33, v37
	v_cvt_f32_i32_sdwa v37, sext(v33) dst_sel:DWORD dst_unused:UNUSED_PAD src0_sel:BYTE_0
	v_add_f32_dpp v53, v53, v53 row_half_mirror row_mask:0xf bank_mask:0xf bound_ctrl:1
	v_dot4c_i32_i8_e32 v52, v34, v38
	v_cvt_f32_i32_sdwa v38, sext(v34) dst_sel:DWORD dst_unused:UNUSED_PAD src0_sel:BYTE_0
	v_cndmask_b32_e64 v40, v40, v53, s[6:7]
	v_cvt_f32_i32_sdwa v53, sext(v35) dst_sel:DWORD dst_unused:UNUSED_PAD src0_sel:BYTE_0
	v_fma_f32 v36, v36, v0, 0
	v_fmac_f32_e32 v36, v37, v8
	v_cvt_f32_i32_sdwa v37, sext(v32) dst_sel:DWORD dst_unused:UNUSED_PAD src0_sel:BYTE_1
	v_fmac_f32_e32 v36, v38, v12
	v_cvt_f32_i32_sdwa v38, sext(v33) dst_sel:DWORD dst_unused:UNUSED_PAD src0_sel:BYTE_1
	v_fmac_f32_e32 v36, v53, v4
	v_cvt_f32_i32_sdwa v53, sext(v34) dst_sel:DWORD dst_unused:UNUSED_PAD src0_sel:BYTE_1
	v_fmac_f32_e32 v36, v37, v1
	v_cvt_f32_i32_sdwa v37, sext(v32) dst_sel:DWORD dst_unused:UNUSED_PAD src0_sel:BYTE_2
	v_fmac_f32_e32 v36, v38, v9
	v_cvt_f32_i32_sdwa v38, sext(v33) dst_sel:DWORD dst_unused:UNUSED_PAD src0_sel:BYTE_2
	v_fmac_f32_e32 v36, v53, v13
	v_cvt_f32_i32_sdwa v53, sext(v34) dst_sel:DWORD dst_unused:UNUSED_PAD src0_sel:BYTE_2
	v_fmac_f32_e32 v36, v54, v5
	v_cvt_f32_i32_sdwa v54, sext(v35) dst_sel:DWORD dst_unused:UNUSED_PAD src0_sel:BYTE_2
	v_fmac_f32_e32 v36, v37, v2
	v_cvt_f32_i32_sdwa v32, sext(v32) dst_sel:DWORD dst_unused:UNUSED_PAD src0_sel:BYTE_3
	v_fmac_f32_e32 v36, v38, v10
	v_cvt_f32_i32_sdwa v33, sext(v33) dst_sel:DWORD dst_unused:UNUSED_PAD src0_sel:BYTE_3
	v_fmac_f32_e32 v36, v53, v14
	v_cvt_f32_i32_sdwa v34, sext(v34) dst_sel:DWORD dst_unused:UNUSED_PAD src0_sel:BYTE_3
	v_fmac_f32_e32 v36, v54, v6
	v_cvt_f32_i32_sdwa v37, sext(v35) dst_sel:DWORD dst_unused:UNUSED_PAD src0_sel:BYTE_3
	v_fmac_f32_e32 v36, v32, v3
	v_fmac_f32_e32 v36, v33, v11
	v_fmac_f32_e32 v36, v34, v15
	v_fmac_f32_e32 v36, v37, v7
	v_dot4c_i32_i8_e32 v52, v35, v39
	s_waitcnt vmcnt(3)
	v_cvt_f32_i32_sdwa v35, sext(v24) dst_sel:DWORD dst_unused:UNUSED_PAD src0_sel:BYTE_0
	v_add_f32_dpp v33, v36, v36 quad_perm:[1,0,3,2] row_mask:0xf bank_mask:0xf bound_ctrl:1
	v_cvt_f32_i32_sdwa v36, sext(v25) dst_sel:DWORD dst_unused:UNUSED_PAD src0_sel:BYTE_0
	v_cvt_f32_i32_sdwa v37, sext(v26) dst_sel:DWORD dst_unused:UNUSED_PAD src0_sel:BYTE_0
	v_cvt_f32_i32_sdwa v38, sext(v27) dst_sel:DWORD dst_unused:UNUSED_PAD src0_sel:BYTE_0
	v_fma_f32 v35, v35, v0, 0
	v_fmac_f32_e32 v35, v36, v8
	v_cvt_f32_i32_sdwa v36, sext(v24) dst_sel:DWORD dst_unused:UNUSED_PAD src0_sel:BYTE_1
	v_fmac_f32_e32 v35, v37, v12
	v_cvt_f32_i32_sdwa v37, sext(v25) dst_sel:DWORD dst_unused:UNUSED_PAD src0_sel:BYTE_1
	v_fmac_f32_e32 v35, v38, v4
	v_cvt_f32_i32_sdwa v38, sext(v26) dst_sel:DWORD dst_unused:UNUSED_PAD src0_sel:BYTE_1
	v_cvt_f32_i32_sdwa v39, sext(v27) dst_sel:DWORD dst_unused:UNUSED_PAD src0_sel:BYTE_1
	v_fmac_f32_e32 v35, v36, v1
	v_cvt_f32_i32_sdwa v36, sext(v24) dst_sel:DWORD dst_unused:UNUSED_PAD src0_sel:BYTE_2
	v_fmac_f32_e32 v35, v37, v9
	v_cvt_f32_i32_sdwa v37, sext(v25) dst_sel:DWORD dst_unused:UNUSED_PAD src0_sel:BYTE_2
	v_fmac_f32_e32 v35, v38, v13
	v_cvt_f32_i32_sdwa v38, sext(v26) dst_sel:DWORD dst_unused:UNUSED_PAD src0_sel:BYTE_2
	v_mov_b32_e32 v34, v41
	v_fmac_f32_e32 v35, v39, v5
	v_cvt_f32_i32_sdwa v39, sext(v27) dst_sel:DWORD dst_unused:UNUSED_PAD src0_sel:BYTE_2
	s_waitcnt vmcnt(2)
	v_dot4c_i32_i8_e32 v34, v24, v48
	v_fmac_f32_e32 v35, v36, v2
	v_cvt_f32_i32_sdwa v24, sext(v24) dst_sel:DWORD dst_unused:UNUSED_PAD src0_sel:BYTE_3
	v_dot4c_i32_i8_e32 v34, v25, v49
	v_fmac_f32_e32 v35, v37, v10
	v_cvt_f32_i32_sdwa v25, sext(v25) dst_sel:DWORD dst_unused:UNUSED_PAD src0_sel:BYTE_3
	v_dot4c_i32_i8_e32 v34, v26, v50
	v_fmac_f32_e32 v35, v38, v14
	v_cvt_f32_i32_sdwa v26, sext(v26) dst_sel:DWORD dst_unused:UNUSED_PAD src0_sel:BYTE_3
	v_fmac_f32_e32 v35, v39, v6
	v_fmac_f32_e32 v35, v24, v3
	v_fmac_f32_e32 v35, v25, v11
	v_fmac_f32_e32 v35, v26, v15
	v_mov_b32_e32 v26, v41
	s_waitcnt vmcnt(0)
	v_dot4c_i32_i8_e32 v26, v16, v20
	v_cvt_f32_i32_sdwa v20, sext(v16) dst_sel:DWORD dst_unused:UNUSED_PAD src0_sel:BYTE_0
	v_dot4c_i32_i8_e32 v26, v17, v21
	v_cvt_f32_i32_sdwa v21, sext(v17) dst_sel:DWORD dst_unused:UNUSED_PAD src0_sel:BYTE_0
	v_dot4c_i32_i8_e32 v26, v18, v22
	v_cvt_f32_i32_sdwa v22, sext(v18) dst_sel:DWORD dst_unused:UNUSED_PAD src0_sel:BYTE_0
	v_cvt_f32_i32_sdwa v36, sext(v27) dst_sel:DWORD dst_unused:UNUSED_PAD src0_sel:BYTE_3
	v_dot4c_i32_i8_e32 v34, v27, v51
	v_cvt_f32_i32_sdwa v27, sext(v19) dst_sel:DWORD dst_unused:UNUSED_PAD src0_sel:BYTE_0
	v_add_u32_dpp v32, v52, v52 quad_perm:[1,0,3,2] row_mask:0xf bank_mask:0xf bound_ctrl:1
	v_fma_f32 v20, v20, v0, 0
	v_add_u32_dpp v24, v34, v34 quad_perm:[1,0,3,2] row_mask:0xf bank_mask:0xf bound_ctrl:1
	v_add_u32_dpp v32, v32, v32 quad_perm:[2,3,0,1] row_mask:0xf bank_mask:0xf bound_ctrl:1
	v_fmac_f32_e32 v20, v21, v8
	v_cvt_f32_i32_sdwa v21, sext(v16) dst_sel:DWORD dst_unused:UNUSED_PAD src0_sel:BYTE_1
	v_add_u32_dpp v32, v32, v32 row_half_mirror row_mask:0xf bank_mask:0xf bound_ctrl:1
	v_add_u32_dpp v24, v24, v24 quad_perm:[2,3,0,1] row_mask:0xf bank_mask:0xf bound_ctrl:1
	v_fmac_f32_e32 v20, v22, v12
	v_cvt_f32_i32_sdwa v22, sext(v17) dst_sel:DWORD dst_unused:UNUSED_PAD src0_sel:BYTE_1
	v_cndmask_b32_e64 v32, v47, v32, s[8:9]
	v_add_u32_dpp v24, v24, v24 row_half_mirror row_mask:0xf bank_mask:0xf bound_ctrl:1
	v_fmac_f32_e32 v20, v27, v4
	v_cvt_f32_i32_sdwa v27, sext(v18) dst_sel:DWORD dst_unused:UNUSED_PAD src0_sel:BYTE_1
	v_cndmask_b32_e64 v24, v32, v24, s[10:11]
	v_cvt_f32_i32_sdwa v32, sext(v19) dst_sel:DWORD dst_unused:UNUSED_PAD src0_sel:BYTE_1
	v_fmac_f32_e32 v20, v21, v1
	v_cvt_f32_i32_sdwa v21, sext(v16) dst_sel:DWORD dst_unused:UNUSED_PAD src0_sel:BYTE_2
	v_fmac_f32_e32 v20, v22, v9
	v_cvt_f32_i32_sdwa v22, sext(v17) dst_sel:DWORD dst_unused:UNUSED_PAD src0_sel:BYTE_2
	v_fmac_f32_e32 v20, v27, v13
	v_cvt_f32_i32_sdwa v27, sext(v18) dst_sel:DWORD dst_unused:UNUSED_PAD src0_sel:BYTE_2
	v_fmac_f32_e32 v20, v32, v5
	v_cvt_f32_i32_sdwa v32, sext(v19) dst_sel:DWORD dst_unused:UNUSED_PAD src0_sel:BYTE_2
	v_fmac_f32_e32 v20, v21, v2
	v_cvt_f32_i32_sdwa v16, sext(v16) dst_sel:DWORD dst_unused:UNUSED_PAD src0_sel:BYTE_3
	v_fmac_f32_e32 v20, v22, v10
	v_cvt_f32_i32_sdwa v17, sext(v17) dst_sel:DWORD dst_unused:UNUSED_PAD src0_sel:BYTE_3
	v_fmac_f32_e32 v20, v27, v14
	v_cvt_f32_i32_sdwa v18, sext(v18) dst_sel:DWORD dst_unused:UNUSED_PAD src0_sel:BYTE_3
	v_fmac_f32_e32 v20, v32, v6
	v_cvt_f32_i32_sdwa v21, sext(v19) dst_sel:DWORD dst_unused:UNUSED_PAD src0_sel:BYTE_3
	v_dot4c_i32_i8_e32 v26, v19, v23
	v_fmac_f32_e32 v20, v16, v3
	v_fmac_f32_e32 v20, v17, v11
	v_fmac_f32_e32 v35, v36, v7
	v_add_u32_dpp v16, v26, v26 quad_perm:[1,0,3,2] row_mask:0xf bank_mask:0xf bound_ctrl:1
	v_fmac_f32_e32 v20, v18, v15
	v_add_f32_dpp v33, v33, v33 quad_perm:[2,3,0,1] row_mask:0xf bank_mask:0xf bound_ctrl:1
	v_add_u32_dpp v16, v16, v16 quad_perm:[2,3,0,1] row_mask:0xf bank_mask:0xf bound_ctrl:1
	v_add_f32_dpp v25, v35, v35 quad_perm:[1,0,3,2] row_mask:0xf bank_mask:0xf bound_ctrl:1
	v_fmac_f32_e32 v20, v21, v7
	v_add_u32_dpp v18, v16, v16 row_half_mirror row_mask:0xf bank_mask:0xf bound_ctrl:1
	ds_bpermute_b32 v16, v44, v45
	v_cndmask_b32_e64 v18, v24, v18, s[12:13]
	v_add_f32_dpp v33, v33, v33 row_half_mirror row_mask:0xf bank_mask:0xf bound_ctrl:1
	v_add_f32_dpp v25, v25, v25 quad_perm:[2,3,0,1] row_mask:0xf bank_mask:0xf bound_ctrl:1
	v_add_f32_dpp v17, v20, v20 quad_perm:[1,0,3,2] row_mask:0xf bank_mask:0xf bound_ctrl:1
	global_atomic_add v[28:29], v18, off offset:512
	ds_bpermute_b32 v18, v44, v46
	v_cndmask_b32_e64 v33, v40, v33, s[8:9]
	v_add_f32_dpp v25, v25, v25 row_half_mirror row_mask:0xf bank_mask:0xf bound_ctrl:1
	v_add_f32_dpp v17, v17, v17 quad_perm:[2,3,0,1] row_mask:0xf bank_mask:0xf bound_ctrl:1
	v_cndmask_b32_e64 v25, v33, v25, s[10:11]
	s_waitcnt lgkmcnt(0)
	v_ashrrev_i32_e32 v19, 31, v18
	v_add_f32_dpp v17, v17, v17 row_half_mirror row_mask:0xf bank_mask:0xf bound_ctrl:1
	v_cndmask_b32_e64 v17, v25, v17, s[12:13]
	global_atomic_add_f32 v[30:31], v17, off offset:512
	v_ashrrev_i32_e32 v17, 31, v16
	v_lshlrev_b64 v[16:17], 7, v[16:17]
	v_lshl_add_u64 v[16:17], v[42:43], 0, v[16:17]
	v_lshlrev_b64 v[18:19], 7, v[18:19]
	v_lshl_add_u64 v[18:19], v[42:43], 0, v[18:19]
	global_load_dwordx4 v[32:35], v[16:17], off
	global_load_dwordx4 v[36:39], v[18:19], off
	ds_bpermute_b32 v16, v44, v45 offset:32
	ds_bpermute_b32 v18, v44, v46 offset:32
	v_mov_b32_e32 v66, v41
	v_mov_b32_e32 v40, v41
	s_waitcnt lgkmcnt(1)
	v_ashrrev_i32_e32 v17, 31, v16
	v_lshlrev_b64 v[16:17], 7, v[16:17]
	s_waitcnt lgkmcnt(0)
	v_ashrrev_i32_e32 v19, 31, v18
	v_lshl_add_u64 v[16:17], v[42:43], 0, v[16:17]
	v_lshlrev_b64 v[18:19], 7, v[18:19]
	v_lshl_add_u64 v[18:19], v[42:43], 0, v[18:19]
	global_load_dwordx4 v[20:23], v[16:17], off
	global_load_dwordx4 v[48:51], v[18:19], off
	ds_bpermute_b32 v16, v44, v45 offset:64
	ds_bpermute_b32 v18, v44, v46 offset:64
	s_waitcnt lgkmcnt(1)
	v_ashrrev_i32_e32 v17, 31, v16
	v_lshlrev_b64 v[16:17], 7, v[16:17]
	s_waitcnt lgkmcnt(0)
	v_ashrrev_i32_e32 v19, 31, v18
	v_lshl_add_u64 v[52:53], v[42:43], 0, v[16:17]
	v_lshlrev_b64 v[16:17], 7, v[18:19]
	v_lshl_add_u64 v[54:55], v[42:43], 0, v[16:17]
	global_load_dwordx4 v[16:19], v[52:53], off
	global_load_dwordx4 v[24:27], v[54:55], off
	s_waitcnt vmcnt(5)
	v_cvt_f32_i32_sdwa v47, sext(v33) dst_sel:DWORD dst_unused:UNUSED_PAD src0_sel:BYTE_0
	s_waitcnt vmcnt(4)
	v_dot4c_i32_i8_e32 v40, v32, v36
	v_dot4c_i32_i8_e32 v40, v33, v37
	v_dot4c_i32_i8_e32 v40, v34, v38
	v_cvt_f32_i32_sdwa v38, sext(v32) dst_sel:DWORD dst_unused:UNUSED_PAD src0_sel:BYTE_0
	v_cvt_f32_i32_sdwa v60, sext(v32) dst_sel:DWORD dst_unused:UNUSED_PAD src0_sel:BYTE_1
	v_cvt_f32_i32_sdwa v61, sext(v33) dst_sel:DWORD dst_unused:UNUSED_PAD src0_sel:BYTE_1
	v_dot4c_i32_i8_e32 v40, v35, v39
	v_cvt_f32_i32_sdwa v39, sext(v32) dst_sel:DWORD dst_unused:UNUSED_PAD src0_sel:BYTE_2
	v_cvt_f32_i32_sdwa v64, sext(v33) dst_sel:DWORD dst_unused:UNUSED_PAD src0_sel:BYTE_2
	v_cvt_f32_i32_sdwa v67, sext(v33) dst_sel:DWORD dst_unused:UNUSED_PAD src0_sel:BYTE_3
	v_cvt_f32_i32_sdwa v58, sext(v34) dst_sel:DWORD dst_unused:UNUSED_PAD src0_sel:BYTE_0
	s_waitcnt vmcnt(3)
	v_cvt_f32_i32_sdwa v68, sext(v20) dst_sel:DWORD dst_unused:UNUSED_PAD src0_sel:BYTE_0
	s_waitcnt vmcnt(2)
	v_dot4c_i32_i8_e32 v66, v20, v48
	v_dot4c_i32_i8_e32 v66, v21, v49
	v_cvt_f32_i32_sdwa v69, sext(v21) dst_sel:DWORD dst_unused:UNUSED_PAD src0_sel:BYTE_0
	v_cvt_f32_i32_sdwa v73, sext(v20) dst_sel:DWORD dst_unused:UNUSED_PAD src0_sel:BYTE_1
	v_cvt_f32_i32_sdwa v74, sext(v21) dst_sel:DWORD dst_unused:UNUSED_PAD src0_sel:BYTE_1
	v_cvt_f32_i32_sdwa v77, sext(v20) dst_sel:DWORD dst_unused:UNUSED_PAD src0_sel:BYTE_2
	v_cvt_f32_i32_sdwa v78, sext(v21) dst_sel:DWORD dst_unused:UNUSED_PAD src0_sel:BYTE_2
	v_cvt_f32_i32_sdwa v81, sext(v20) dst_sel:DWORD dst_unused:UNUSED_PAD src0_sel:BYTE_3
	v_cvt_f32_i32_sdwa v82, sext(v21) dst_sel:DWORD dst_unused:UNUSED_PAD src0_sel:BYTE_3
	v_cvt_f32_i32_sdwa v49, sext(v32) dst_sel:DWORD dst_unused:UNUSED_PAD src0_sel:BYTE_3
	v_dot4c_i32_i8_e32 v66, v22, v50
	s_waitcnt vmcnt(1)
	v_cvt_f32_i32_sdwa v85, sext(v16) dst_sel:DWORD dst_unused:UNUSED_PAD src0_sel:BYTE_0
	s_waitcnt vmcnt(0)
	v_dot4c_i32_i8_e32 v70, v16, v24
	v_dot4c_i32_i8_e32 v70, v17, v25
	v_cvt_f32_i32_sdwa v89, sext(v16) dst_sel:DWORD dst_unused:UNUSED_PAD src0_sel:BYTE_1
	v_cvt_f32_i32_sdwa v93, sext(v16) dst_sel:DWORD dst_unused:UNUSED_PAD src0_sel:BYTE_2
	v_cvt_f32_i32_sdwa v97, sext(v16) dst_sel:DWORD dst_unused:UNUSED_PAD src0_sel:BYTE_3
	ds_bpermute_b32 v16, v44, v45 offset:96
	v_dot4c_i32_i8_e32 v70, v18, v26
	v_cvt_f32_i32_sdwa v87, sext(v18) dst_sel:DWORD dst_unused:UNUSED_PAD src0_sel:BYTE_0
	v_cvt_f32_i32_sdwa v91, sext(v18) dst_sel:DWORD dst_unused:UNUSED_PAD src0_sel:BYTE_1
	v_cvt_f32_i32_sdwa v95, sext(v18) dst_sel:DWORD dst_unused:UNUSED_PAD src0_sel:BYTE_2
	v_cvt_f32_i32_sdwa v99, sext(v18) dst_sel:DWORD dst_unused:UNUSED_PAD src0_sel:BYTE_3
	ds_bpermute_b32 v18, v44, v46 offset:96
	v_cvt_f32_i32_sdwa v86, sext(v17) dst_sel:DWORD dst_unused:UNUSED_PAD src0_sel:BYTE_0
	v_cvt_f32_i32_sdwa v90, sext(v17) dst_sel:DWORD dst_unused:UNUSED_PAD src0_sel:BYTE_1
	v_cvt_f32_i32_sdwa v94, sext(v17) dst_sel:DWORD dst_unused:UNUSED_PAD src0_sel:BYTE_2
	v_cvt_f32_i32_sdwa v98, sext(v17) dst_sel:DWORD dst_unused:UNUSED_PAD src0_sel:BYTE_3
	s_waitcnt lgkmcnt(1)
	v_ashrrev_i32_e32 v17, 31, v16
	v_dot4c_i32_i8_e32 v70, v19, v27
	v_cvt_f32_i32_sdwa v88, sext(v19) dst_sel:DWORD dst_unused:UNUSED_PAD src0_sel:BYTE_0
	v_cvt_f32_i32_sdwa v92, sext(v19) dst_sel:DWORD dst_unused:UNUSED_PAD src0_sel:BYTE_1
	v_cvt_f32_i32_sdwa v96, sext(v19) dst_sel:DWORD dst_unused:UNUSED_PAD src0_sel:BYTE_2
	v_cvt_f32_i32_sdwa v100, sext(v19) dst_sel:DWORD dst_unused:UNUSED_PAD src0_sel:BYTE_3
	v_lshlrev_b64 v[16:17], 7, v[16:17]
	s_waitcnt lgkmcnt(0)
	v_ashrrev_i32_e32 v19, 31, v18
	v_lshl_add_u64 v[20:21], v[42:43], 0, v[16:17]
	ds_bpermute_b32 v16, v44, v45 offset:128
	v_lshlrev_b64 v[18:19], 7, v[18:19]
	v_lshl_add_u64 v[24:25], v[42:43], 0, v[18:19]
	ds_bpermute_b32 v18, v44, v46 offset:128
	v_cvt_f32_i32_sdwa v71, sext(v22) dst_sel:DWORD dst_unused:UNUSED_PAD src0_sel:BYTE_0
	s_waitcnt lgkmcnt(1)
	v_ashrrev_i32_e32 v17, 31, v16
	v_lshlrev_b64 v[16:17], 7, v[16:17]
	v_lshl_add_u64 v[32:33], v[42:43], 0, v[16:17]
	s_waitcnt lgkmcnt(0)
	v_ashrrev_i32_e32 v19, 31, v18
	ds_bpermute_b32 v16, v44, v45 offset:160
	v_lshlrev_b64 v[18:19], 7, v[18:19]
	v_lshl_add_u64 v[36:37], v[42:43], 0, v[18:19]
	ds_bpermute_b32 v18, v44, v46 offset:160
	v_cvt_f32_i32_sdwa v75, sext(v22) dst_sel:DWORD dst_unused:UNUSED_PAD src0_sel:BYTE_1
	v_cvt_f32_i32_sdwa v79, sext(v22) dst_sel:DWORD dst_unused:UNUSED_PAD src0_sel:BYTE_2
	v_cvt_f32_i32_sdwa v83, sext(v22) dst_sel:DWORD dst_unused:UNUSED_PAD src0_sel:BYTE_3
	ds_bpermute_b32 v22, v44, v45 offset:192
	s_waitcnt lgkmcnt(2)
	v_ashrrev_i32_e32 v17, 31, v16
	v_lshlrev_b64 v[16:17], 7, v[16:17]
	s_waitcnt lgkmcnt(1)
	v_ashrrev_i32_e32 v19, 31, v18
	v_dot4c_i32_i8_e32 v66, v23, v51
	v_cvt_f32_i32_sdwa v72, sext(v23) dst_sel:DWORD dst_unused:UNUSED_PAD src0_sel:BYTE_0
	v_cvt_f32_i32_sdwa v76, sext(v23) dst_sel:DWORD dst_unused:UNUSED_PAD src0_sel:BYTE_1
	v_cvt_f32_i32_sdwa v80, sext(v23) dst_sel:DWORD dst_unused:UNUSED_PAD src0_sel:BYTE_2
	v_cvt_f32_i32_sdwa v84, sext(v23) dst_sel:DWORD dst_unused:UNUSED_PAD src0_sel:BYTE_3
	v_lshl_add_u64 v[50:51], v[42:43], 0, v[16:17]
	v_lshlrev_b64 v[16:17], 7, v[18:19]
	s_waitcnt lgkmcnt(0)
	v_ashrrev_i32_e32 v23, 31, v22
	v_lshl_add_u64 v[52:53], v[42:43], 0, v[16:17]
	v_lshlrev_b64 v[16:17], 7, v[22:23]
	v_lshl_add_u64 v[54:55], v[42:43], 0, v[16:17]
	ds_bpermute_b32 v16, v44, v46 offset:192
	ds_bpermute_b32 v18, v44, v45 offset:224
	ds_bpermute_b32 v22, v44, v46 offset:224
	v_cvt_f32_i32_sdwa v59, sext(v35) dst_sel:DWORD dst_unused:UNUSED_PAD src0_sel:BYTE_0
	v_fma_f32 v38, v38, v0, 0
	s_waitcnt lgkmcnt(2)
	v_ashrrev_i32_e32 v17, 31, v16
	v_lshlrev_b64 v[16:17], 7, v[16:17]
	s_waitcnt lgkmcnt(1)
	v_ashrrev_i32_e32 v19, 31, v18
	s_waitcnt lgkmcnt(0)
	v_ashrrev_i32_e32 v23, 31, v22
	v_lshl_add_u64 v[56:57], v[42:43], 0, v[16:17]
	v_lshlrev_b64 v[16:17], 7, v[18:19]
	v_lshlrev_b64 v[18:19], 7, v[22:23]
	global_load_dwordx4 v[20:23], v[20:21], off
	v_fmac_f32_e32 v38, v47, v8
	v_cvt_f32_i32_sdwa v62, sext(v34) dst_sel:DWORD dst_unused:UNUSED_PAD src0_sel:BYTE_1
	v_fmac_f32_e32 v38, v58, v12
	v_cvt_f32_i32_sdwa v63, sext(v35) dst_sel:DWORD dst_unused:UNUSED_PAD src0_sel:BYTE_1
	v_fmac_f32_e32 v38, v59, v4
	v_fmac_f32_e32 v38, v60, v1
	v_fmac_f32_e32 v38, v61, v9
	v_cvt_f32_i32_sdwa v65, sext(v34) dst_sel:DWORD dst_unused:UNUSED_PAD src0_sel:BYTE_2
	v_fmac_f32_e32 v38, v62, v13
	v_cvt_f32_i32_sdwa v48, sext(v35) dst_sel:DWORD dst_unused:UNUSED_PAD src0_sel:BYTE_2
	v_fmac_f32_e32 v38, v63, v5
	v_fmac_f32_e32 v38, v39, v2
	v_fmac_f32_e32 v38, v64, v10
	v_cvt_f32_i32_sdwa v34, sext(v34) dst_sel:DWORD dst_unused:UNUSED_PAD src0_sel:BYTE_3
	v_fmac_f32_e32 v38, v65, v14
	v_fmac_f32_e32 v38, v48, v6
	v_fmac_f32_e32 v38, v49, v3
	v_fmac_f32_e32 v38, v67, v11
	v_fmac_f32_e32 v38, v34, v15
	v_fma_f32 v34, v68, v0, 0
	v_fmac_f32_e32 v34, v69, v8
	v_fmac_f32_e32 v34, v71, v12
	v_fmac_f32_e32 v34, v72, v4
	global_load_dwordx4 v[24:27], v[24:25], off
	v_fmac_f32_e32 v34, v73, v1
	v_fmac_f32_e32 v34, v74, v9
	v_fmac_f32_e32 v34, v75, v13
	v_fmac_f32_e32 v34, v76, v5
	v_fmac_f32_e32 v34, v77, v2
	v_fmac_f32_e32 v34, v78, v10
	v_cvt_f32_i32_sdwa v35, sext(v35) dst_sel:DWORD dst_unused:UNUSED_PAD src0_sel:BYTE_3
	v_fmac_f32_e32 v34, v79, v14
	v_fmac_f32_e32 v34, v80, v6
	v_fmac_f32_e32 v34, v81, v3
	v_fmac_f32_e32 v34, v82, v11
	v_fmac_f32_e32 v38, v35, v7
	v_fmac_f32_e32 v34, v83, v15
	v_fmac_f32_e32 v34, v84, v7
	v_add_f32_dpp v35, v38, v38 quad_perm:[1,0,3,2] row_mask:0xf bank_mask:0xf bound_ctrl:1
	v_lshl_add_u64 v[16:17], v[42:43], 0, v[16:17]
	v_add_f32_dpp v34, v34, v34 quad_perm:[1,0,3,2] row_mask:0xf bank_mask:0xf bound_ctrl:1
	v_add_f32_dpp v35, v35, v35 quad_perm:[2,3,0,1] row_mask:0xf bank_mask:0xf bound_ctrl:1
	v_lshl_add_u64 v[18:19], v[42:43], 0, v[18:19]
	v_add_f32_dpp v34, v34, v34 quad_perm:[2,3,0,1] row_mask:0xf bank_mask:0xf bound_ctrl:1
	v_add_f32_dpp v35, v35, v35 row_half_mirror row_mask:0xf bank_mask:0xf bound_ctrl:1
	v_cndmask_b32_e32 v35, 0, v35, vcc
	v_add_f32_dpp v34, v34, v34 row_half_mirror row_mask:0xf bank_mask:0xf bound_ctrl:1
	v_cndmask_b32_e64 v42, v35, v34, s[0:1]
	global_load_dwordx4 v[32:35], v[32:33], off
	v_fma_f32 v43, v85, v0, 0
	v_fmac_f32_e32 v43, v86, v8
	v_fmac_f32_e32 v43, v87, v12
	v_fmac_f32_e32 v43, v88, v4
	v_fmac_f32_e32 v43, v89, v1
	v_fmac_f32_e32 v43, v90, v9
	v_fmac_f32_e32 v43, v91, v13
	v_fmac_f32_e32 v43, v92, v5
	v_fmac_f32_e32 v43, v93, v2
	v_fmac_f32_e32 v43, v94, v10
	v_fmac_f32_e32 v43, v95, v14
	v_fmac_f32_e32 v43, v96, v6
	v_fmac_f32_e32 v43, v97, v3
	v_fmac_f32_e32 v43, v98, v11
	v_fmac_f32_e32 v43, v99, v15
	v_fmac_f32_e32 v43, v100, v7
	v_add_u32_dpp v38, v40, v40 quad_perm:[1,0,3,2] row_mask:0xf bank_mask:0xf bound_ctrl:1
	v_add_u32_dpp v39, v66, v66 quad_perm:[1,0,3,2] row_mask:0xf bank_mask:0xf bound_ctrl:1
	v_add_f32_dpp v43, v43, v43 quad_perm:[1,0,3,2] row_mask:0xf bank_mask:0xf bound_ctrl:1
	v_add_u32_dpp v38, v38, v38 quad_perm:[2,3,0,1] row_mask:0xf bank_mask:0xf bound_ctrl:1
	v_add_u32_dpp v39, v39, v39 quad_perm:[2,3,0,1] row_mask:0xf bank_mask:0xf bound_ctrl:1
	v_add_f32_dpp v43, v43, v43 quad_perm:[2,3,0,1] row_mask:0xf bank_mask:0xf bound_ctrl:1
	v_add_u32_dpp v38, v38, v38 row_half_mirror row_mask:0xf bank_mask:0xf bound_ctrl:1
	v_add_u32_dpp v44, v70, v70 quad_perm:[1,0,3,2] row_mask:0xf bank_mask:0xf bound_ctrl:1
	v_add_f32_dpp v43, v43, v43 row_half_mirror row_mask:0xf bank_mask:0xf bound_ctrl:1
	v_cndmask_b32_e64 v58, v42, v43, s[2:3]
	v_cndmask_b32_e32 v38, 0, v38, vcc
	v_add_u32_dpp v39, v39, v39 row_half_mirror row_mask:0xf bank_mask:0xf bound_ctrl:1
	v_add_u32_dpp v44, v44, v44 quad_perm:[2,3,0,1] row_mask:0xf bank_mask:0xf bound_ctrl:1
	v_cndmask_b32_e64 v40, v38, v39, s[0:1]
	s_waitcnt vmcnt(2)
	v_cvt_f32_i32_sdwa v42, sext(v20) dst_sel:DWORD dst_unused:UNUSED_PAD src0_sel:BYTE_0
	v_cvt_f32_i32_sdwa v43, sext(v21) dst_sel:DWORD dst_unused:UNUSED_PAD src0_sel:BYTE_0
	v_cvt_f32_i32_sdwa v45, sext(v22) dst_sel:DWORD dst_unused:UNUSED_PAD src0_sel:BYTE_0
	v_add_u32_dpp v44, v44, v44 row_half_mirror row_mask:0xf bank_mask:0xf bound_ctrl:1
	v_fma_f32 v59, v42, v0, 0
	v_fmac_f32_e32 v59, v43, v8
	global_load_dwordx4 v[36:39], v[36:37], off
	v_cndmask_b32_e64 v40, v40, v44, s[2:3]
	v_fmac_f32_e32 v59, v45, v12
	global_load_dwordx4 v[42:45], v[50:51], off
	global_load_dwordx4 v[46:49], v[52:53], off
	v_cvt_f32_i32_sdwa v60, sext(v23) dst_sel:DWORD dst_unused:UNUSED_PAD src0_sel:BYTE_0
	v_cvt_f32_i32_sdwa v61, sext(v20) dst_sel:DWORD dst_unused:UNUSED_PAD src0_sel:BYTE_1
	v_cvt_f32_i32_sdwa v62, sext(v21) dst_sel:DWORD dst_unused:UNUSED_PAD src0_sel:BYTE_1
	v_cvt_f32_i32_sdwa v50, sext(v22) dst_sel:DWORD dst_unused:UNUSED_PAD src0_sel:BYTE_1
	v_fmac_f32_e32 v59, v60, v4
	v_fmac_f32_e32 v59, v61, v1
	v_cvt_f32_i32_sdwa v51, sext(v23) dst_sel:DWORD dst_unused:UNUSED_PAD src0_sel:BYTE_1
	v_mov_b32_e32 v52, v41
	v_fmac_f32_e32 v59, v62, v9
	v_fmac_f32_e32 v59, v50, v13
	v_cvt_f32_i32_sdwa v50, sext(v21) dst_sel:DWORD dst_unused:UNUSED_PAD src0_sel:BYTE_2
	v_fmac_f32_e32 v59, v51, v5
	v_cvt_f32_i32_sdwa v51, sext(v23) dst_sel:DWORD dst_unused:UNUSED_PAD src0_sel:BYTE_2
	v_cvt_f32_i32_sdwa v53, sext(v20) dst_sel:DWORD dst_unused:UNUSED_PAD src0_sel:BYTE_3
	s_waitcnt vmcnt(4)
	v_dot4c_i32_i8_e32 v52, v20, v24
	v_cvt_f32_i32_sdwa v24, sext(v20) dst_sel:DWORD dst_unused:UNUSED_PAD src0_sel:BYTE_2
	v_dot4c_i32_i8_e32 v52, v21, v25
	v_dot4c_i32_i8_e32 v52, v22, v26
	v_dot4c_i32_i8_e32 v52, v23, v27
	v_fmac_f32_e32 v59, v24, v2
	v_fmac_f32_e32 v59, v50, v10
	v_cvt_f32_i32_sdwa v50, sext(v22) dst_sel:DWORD dst_unused:UNUSED_PAD src0_sel:BYTE_2
	v_cvt_f32_i32_sdwa v60, sext(v21) dst_sel:DWORD dst_unused:UNUSED_PAD src0_sel:BYTE_3
	v_cvt_f32_i32_sdwa v61, sext(v22) dst_sel:DWORD dst_unused:UNUSED_PAD src0_sel:BYTE_3
	v_cvt_f32_i32_sdwa v62, sext(v23) dst_sel:DWORD dst_unused:UNUSED_PAD src0_sel:BYTE_3
	global_load_dwordx4 v[20:23], v[54:55], off
	global_load_dwordx4 v[24:27], v[56:57], off
	v_fmac_f32_e32 v59, v50, v14
	v_fmac_f32_e32 v59, v51, v6
	v_fmac_f32_e32 v59, v53, v3
	v_fmac_f32_e32 v59, v60, v11
	v_fmac_f32_e32 v59, v61, v15
	v_fmac_f32_e32 v59, v62, v7
	v_add_u32_dpp v50, v52, v52 quad_perm:[1,0,3,2] row_mask:0xf bank_mask:0xf bound_ctrl:1
	s_waitcnt vmcnt(5)
	v_cvt_f32_i32_sdwa v52, sext(v32) dst_sel:DWORD dst_unused:UNUSED_PAD src0_sel:BYTE_0
	v_add_u32_dpp v50, v50, v50 quad_perm:[2,3,0,1] row_mask:0xf bank_mask:0xf bound_ctrl:1
	v_add_f32_dpp v51, v59, v59 quad_perm:[1,0,3,2] row_mask:0xf bank_mask:0xf bound_ctrl:1
	v_cvt_f32_i32_sdwa v53, sext(v32) dst_sel:DWORD dst_unused:UNUSED_PAD src0_sel:BYTE_1
	v_add_u32_dpp v50, v50, v50 row_half_mirror row_mask:0xf bank_mask:0xf bound_ctrl:1
	v_add_f32_dpp v51, v51, v51 quad_perm:[2,3,0,1] row_mask:0xf bank_mask:0xf bound_ctrl:1
	v_cndmask_b32_e64 v40, v40, v50, s[4:5]
	v_cvt_f32_i32_sdwa v50, sext(v33) dst_sel:DWORD dst_unused:UNUSED_PAD src0_sel:BYTE_0
	v_add_f32_dpp v51, v51, v51 row_half_mirror row_mask:0xf bank_mask:0xf bound_ctrl:1
	v_cndmask_b32_e64 v58, v58, v51, s[4:5]
	v_cvt_f32_i32_sdwa v51, sext(v34) dst_sel:DWORD dst_unused:UNUSED_PAD src0_sel:BYTE_0
	v_fma_f32 v59, v52, v0, 0
	v_cvt_f32_i32_sdwa v52, sext(v35) dst_sel:DWORD dst_unused:UNUSED_PAD src0_sel:BYTE_0
	v_fmac_f32_e32 v59, v50, v8
	v_cvt_f32_i32_sdwa v50, sext(v33) dst_sel:DWORD dst_unused:UNUSED_PAD src0_sel:BYTE_1
	v_fmac_f32_e32 v59, v51, v12
	v_cvt_f32_i32_sdwa v51, sext(v34) dst_sel:DWORD dst_unused:UNUSED_PAD src0_sel:BYTE_1
	v_fmac_f32_e32 v59, v52, v4
	v_cvt_f32_i32_sdwa v52, sext(v35) dst_sel:DWORD dst_unused:UNUSED_PAD src0_sel:BYTE_1
	v_fmac_f32_e32 v59, v53, v1
	v_cvt_f32_i32_sdwa v53, sext(v32) dst_sel:DWORD dst_unused:UNUSED_PAD src0_sel:BYTE_2
	v_fmac_f32_e32 v59, v50, v9
	v_fmac_f32_e32 v59, v51, v13
	v_fmac_f32_e32 v59, v52, v5
	v_fmac_f32_e32 v59, v53, v2
	global_load_dwordx4 v[50:53], v[16:17], off
	global_load_dwordx4 v[54:57], v[18:19], off
	v_cvt_f32_i32_sdwa v60, sext(v33) dst_sel:DWORD dst_unused:UNUSED_PAD src0_sel:BYTE_2
	v_cvt_f32_i32_sdwa v61, sext(v34) dst_sel:DWORD dst_unused:UNUSED_PAD src0_sel:BYTE_2
	v_cvt_f32_i32_sdwa v62, sext(v35) dst_sel:DWORD dst_unused:UNUSED_PAD src0_sel:BYTE_2
	v_cvt_f32_i32_sdwa v16, sext(v32) dst_sel:DWORD dst_unused:UNUSED_PAD src0_sel:BYTE_3
	v_fmac_f32_e32 v59, v60, v10
	v_mov_b32_e32 v18, v41
	v_fmac_f32_e32 v59, v61, v14
	v_fmac_f32_e32 v59, v62, v6
	v_cvt_f32_i32_sdwa v17, sext(v33) dst_sel:DWORD dst_unused:UNUSED_PAD src0_sel:BYTE_3
	v_fmac_f32_e32 v59, v16, v3
	v_cvt_f32_i32_sdwa v16, sext(v34) dst_sel:DWORD dst_unused:UNUSED_PAD src0_sel:BYTE_3
	s_waitcnt vmcnt(6)
	v_dot4c_i32_i8_e32 v18, v32, v36
	v_dot4c_i32_i8_e32 v18, v33, v37
	s_waitcnt vmcnt(5)
	v_cvt_f32_i32_sdwa v19, sext(v42) dst_sel:DWORD dst_unused:UNUSED_PAD src0_sel:BYTE_0
	v_cvt_f32_i32_sdwa v32, sext(v43) dst_sel:DWORD dst_unused:UNUSED_PAD src0_sel:BYTE_0
	v_cvt_f32_i32_sdwa v33, sext(v44) dst_sel:DWORD dst_unused:UNUSED_PAD src0_sel:BYTE_0
	v_dot4c_i32_i8_e32 v18, v34, v38
	v_cvt_f32_i32_sdwa v34, sext(v45) dst_sel:DWORD dst_unused:UNUSED_PAD src0_sel:BYTE_0
	v_fma_f32 v19, v19, v0, 0
	v_fmac_f32_e32 v19, v32, v8
	v_cvt_f32_i32_sdwa v32, sext(v42) dst_sel:DWORD dst_unused:UNUSED_PAD src0_sel:BYTE_1
	v_fmac_f32_e32 v19, v33, v12
	v_cvt_f32_i32_sdwa v33, sext(v43) dst_sel:DWORD dst_unused:UNUSED_PAD src0_sel:BYTE_1
	v_fmac_f32_e32 v19, v34, v4
	v_cvt_f32_i32_sdwa v34, sext(v44) dst_sel:DWORD dst_unused:UNUSED_PAD src0_sel:BYTE_1
	v_fmac_f32_e32 v59, v17, v11
	v_cvt_f32_i32_sdwa v17, sext(v35) dst_sel:DWORD dst_unused:UNUSED_PAD src0_sel:BYTE_3
	v_dot4c_i32_i8_e32 v18, v35, v39
	v_cvt_f32_i32_sdwa v35, sext(v45) dst_sel:DWORD dst_unused:UNUSED_PAD src0_sel:BYTE_1
	v_fmac_f32_e32 v19, v32, v1
	v_cvt_f32_i32_sdwa v32, sext(v42) dst_sel:DWORD dst_unused:UNUSED_PAD src0_sel:BYTE_2
	v_fmac_f32_e32 v19, v33, v9
	v_cvt_f32_i32_sdwa v33, sext(v43) dst_sel:DWORD dst_unused:UNUSED_PAD src0_sel:BYTE_2
	v_fmac_f32_e32 v19, v34, v13
	v_cvt_f32_i32_sdwa v34, sext(v44) dst_sel:DWORD dst_unused:UNUSED_PAD src0_sel:BYTE_2
	v_fmac_f32_e32 v19, v35, v5
	v_cvt_f32_i32_sdwa v35, sext(v45) dst_sel:DWORD dst_unused:UNUSED_PAD src0_sel:BYTE_2
	v_fmac_f32_e32 v19, v32, v2
	v_cvt_f32_i32_sdwa v32, sext(v42) dst_sel:DWORD dst_unused:UNUSED_PAD src0_sel:BYTE_3
	v_fmac_f32_e32 v19, v33, v10
	v_cvt_f32_i32_sdwa v33, sext(v43) dst_sel:DWORD dst_unused:UNUSED_PAD src0_sel:BYTE_3
	v_fmac_f32_e32 v19, v34, v14
	v_cvt_f32_i32_sdwa v34, sext(v44) dst_sel:DWORD dst_unused:UNUSED_PAD src0_sel:BYTE_3
	v_fmac_f32_e32 v59, v16, v15
	v_add_u32_dpp v16, v18, v18 quad_perm:[1,0,3,2] row_mask:0xf bank_mask:0xf bound_ctrl:1
	v_mov_b32_e32 v18, v41
	v_fmac_f32_e32 v19, v35, v6
	v_cvt_f32_i32_sdwa v35, sext(v45) dst_sel:DWORD dst_unused:UNUSED_PAD src0_sel:BYTE_3
	s_waitcnt vmcnt(4)
	v_dot4c_i32_i8_e32 v18, v42, v46
	v_fmac_f32_e32 v19, v32, v3
	v_dot4c_i32_i8_e32 v18, v43, v47
	v_fmac_f32_e32 v19, v33, v11
	v_fmac_f32_e32 v59, v17, v7
	v_dot4c_i32_i8_e32 v18, v44, v48
	v_fmac_f32_e32 v19, v34, v15
	v_add_f32_dpp v17, v59, v59 quad_perm:[1,0,3,2] row_mask:0xf bank_mask:0xf bound_ctrl:1
	v_fmac_f32_e32 v19, v35, v7
	v_dot4c_i32_i8_e32 v18, v45, v49
	v_add_u32_dpp v16, v16, v16 quad_perm:[2,3,0,1] row_mask:0xf bank_mask:0xf bound_ctrl:1
	v_add_f32_dpp v17, v17, v17 quad_perm:[2,3,0,1] row_mask:0xf bank_mask:0xf bound_ctrl:1
	v_add_f32_dpp v19, v19, v19 quad_perm:[1,0,3,2] row_mask:0xf bank_mask:0xf bound_ctrl:1
	v_add_u32_dpp v18, v18, v18 quad_perm:[1,0,3,2] row_mask:0xf bank_mask:0xf bound_ctrl:1
	v_add_f32_dpp v17, v17, v17 row_half_mirror row_mask:0xf bank_mask:0xf bound_ctrl:1
	v_add_u32_dpp v16, v16, v16 row_half_mirror row_mask:0xf bank_mask:0xf bound_ctrl:1
	v_add_u32_dpp v18, v18, v18 quad_perm:[2,3,0,1] row_mask:0xf bank_mask:0xf bound_ctrl:1
	v_add_f32_dpp v19, v19, v19 quad_perm:[2,3,0,1] row_mask:0xf bank_mask:0xf bound_ctrl:1
	v_cndmask_b32_e64 v17, v58, v17, s[6:7]
	v_cndmask_b32_e64 v16, v40, v16, s[6:7]
	v_add_f32_dpp v19, v19, v19 row_half_mirror row_mask:0xf bank_mask:0xf bound_ctrl:1
	v_add_u32_dpp v18, v18, v18 row_half_mirror row_mask:0xf bank_mask:0xf bound_ctrl:1
	v_cndmask_b32_e64 v17, v17, v19, s[8:9]
	v_cndmask_b32_e64 v16, v16, v18, s[8:9]
	v_mov_b32_e32 v18, v41
	s_waitcnt vmcnt(3)
	v_cvt_f32_i32_sdwa v19, sext(v20) dst_sel:DWORD dst_unused:UNUSED_PAD src0_sel:BYTE_0
	s_waitcnt vmcnt(2)
	v_dot4c_i32_i8_e32 v18, v20, v24
	v_cvt_f32_i32_sdwa v24, sext(v21) dst_sel:DWORD dst_unused:UNUSED_PAD src0_sel:BYTE_0
	v_dot4c_i32_i8_e32 v18, v21, v25
	v_cvt_f32_i32_sdwa v25, sext(v22) dst_sel:DWORD dst_unused:UNUSED_PAD src0_sel:BYTE_0
	v_dot4c_i32_i8_e32 v18, v22, v26
	v_cvt_f32_i32_sdwa v26, sext(v23) dst_sel:DWORD dst_unused:UNUSED_PAD src0_sel:BYTE_0
	v_fma_f32 v19, v19, v0, 0
	v_fmac_f32_e32 v19, v24, v8
	v_cvt_f32_i32_sdwa v24, sext(v20) dst_sel:DWORD dst_unused:UNUSED_PAD src0_sel:BYTE_1
	v_fmac_f32_e32 v19, v25, v12
	v_cvt_f32_i32_sdwa v25, sext(v21) dst_sel:DWORD dst_unused:UNUSED_PAD src0_sel:BYTE_1
	v_fmac_f32_e32 v19, v26, v4
	v_cvt_f32_i32_sdwa v26, sext(v22) dst_sel:DWORD dst_unused:UNUSED_PAD src0_sel:BYTE_1
	v_cvt_f32_i32_sdwa v32, sext(v23) dst_sel:DWORD dst_unused:UNUSED_PAD src0_sel:BYTE_1
	v_fmac_f32_e32 v19, v24, v1
	v_cvt_f32_i32_sdwa v24, sext(v20) dst_sel:DWORD dst_unused:UNUSED_PAD src0_sel:BYTE_2
	v_fmac_f32_e32 v19, v25, v9
	v_cvt_f32_i32_sdwa v25, sext(v21) dst_sel:DWORD dst_unused:UNUSED_PAD src0_sel:BYTE_2
	v_fmac_f32_e32 v19, v26, v13
	v_cvt_f32_i32_sdwa v26, sext(v22) dst_sel:DWORD dst_unused:UNUSED_PAD src0_sel:BYTE_2
	v_fmac_f32_e32 v19, v32, v5
	v_cvt_f32_i32_sdwa v32, sext(v23) dst_sel:DWORD dst_unused:UNUSED_PAD src0_sel:BYTE_2
	v_fmac_f32_e32 v19, v24, v2
	v_cvt_f32_i32_sdwa v20, sext(v20) dst_sel:DWORD dst_unused:UNUSED_PAD src0_sel:BYTE_3
	v_fmac_f32_e32 v19, v25, v10
	v_cvt_f32_i32_sdwa v21, sext(v21) dst_sel:DWORD dst_unused:UNUSED_PAD src0_sel:BYTE_3
	v_fmac_f32_e32 v19, v26, v14
	v_cvt_f32_i32_sdwa v22, sext(v22) dst_sel:DWORD dst_unused:UNUSED_PAD src0_sel:BYTE_3
	v_fmac_f32_e32 v19, v32, v6
	v_cvt_f32_i32_sdwa v24, sext(v23) dst_sel:DWORD dst_unused:UNUSED_PAD src0_sel:BYTE_3
	v_fmac_f32_e32 v19, v20, v3
	v_fmac_f32_e32 v19, v21, v11
	v_fmac_f32_e32 v19, v22, v15
	v_dot4c_i32_i8_e32 v18, v23, v27
	v_fmac_f32_e32 v19, v24, v7
	s_waitcnt vmcnt(1)
	v_cvt_f32_i32_sdwa v20, sext(v52) dst_sel:DWORD dst_unused:UNUSED_PAD src0_sel:BYTE_0
	v_cvt_f32_i32_sdwa v21, sext(v53) dst_sel:DWORD dst_unused:UNUSED_PAD src0_sel:BYTE_0
	v_add_u32_dpp v18, v18, v18 quad_perm:[1,0,3,2] row_mask:0xf bank_mask:0xf bound_ctrl:1
	v_add_f32_dpp v19, v19, v19 quad_perm:[1,0,3,2] row_mask:0xf bank_mask:0xf bound_ctrl:1
	s_waitcnt vmcnt(0)
	v_dot4c_i32_i8_e32 v41, v50, v54
	v_add_u32_dpp v18, v18, v18 quad_perm:[2,3,0,1] row_mask:0xf bank_mask:0xf bound_ctrl:1
	v_add_f32_dpp v19, v19, v19 quad_perm:[2,3,0,1] row_mask:0xf bank_mask:0xf bound_ctrl:1
	v_dot4c_i32_i8_e32 v41, v51, v55
	v_add_u32_dpp v18, v18, v18 row_half_mirror row_mask:0xf bank_mask:0xf bound_ctrl:1
	v_add_f32_dpp v19, v19, v19 row_half_mirror row_mask:0xf bank_mask:0xf bound_ctrl:1
	v_cndmask_b32_e64 v16, v16, v18, s[10:11]
	v_cvt_f32_i32_sdwa v18, sext(v50) dst_sel:DWORD dst_unused:UNUSED_PAD src0_sel:BYTE_0
	v_cndmask_b32_e64 v17, v17, v19, s[10:11]
	v_cvt_f32_i32_sdwa v19, sext(v51) dst_sel:DWORD dst_unused:UNUSED_PAD src0_sel:BYTE_0
	v_dot4c_i32_i8_e32 v41, v52, v56
	v_fma_f32 v0, v18, v0, 0
	v_cvt_f32_i32_sdwa v18, sext(v53) dst_sel:DWORD dst_unused:UNUSED_PAD src0_sel:BYTE_1
	v_fmac_f32_e32 v0, v19, v8
	v_fmac_f32_e32 v0, v20, v12
	v_fmac_f32_e32 v0, v21, v4
	v_cvt_f32_i32_sdwa v4, sext(v50) dst_sel:DWORD dst_unused:UNUSED_PAD src0_sel:BYTE_1
	v_cvt_f32_i32_sdwa v8, sext(v51) dst_sel:DWORD dst_unused:UNUSED_PAD src0_sel:BYTE_1
	v_cvt_f32_i32_sdwa v12, sext(v52) dst_sel:DWORD dst_unused:UNUSED_PAD src0_sel:BYTE_1
	v_dot4c_i32_i8_e32 v41, v53, v57
	v_fmac_f32_e32 v0, v4, v1
	v_fmac_f32_e32 v0, v8, v9
	v_cvt_f32_i32_sdwa v1, sext(v50) dst_sel:DWORD dst_unused:UNUSED_PAD src0_sel:BYTE_2
	v_fmac_f32_e32 v0, v12, v13
	v_cvt_f32_i32_sdwa v4, sext(v51) dst_sel:DWORD dst_unused:UNUSED_PAD src0_sel:BYTE_2
	v_fmac_f32_e32 v0, v18, v5
	v_cvt_f32_i32_sdwa v5, sext(v52) dst_sel:DWORD dst_unused:UNUSED_PAD src0_sel:BYTE_2
	v_cvt_f32_i32_sdwa v8, sext(v53) dst_sel:DWORD dst_unused:UNUSED_PAD src0_sel:BYTE_2
	v_fmac_f32_e32 v0, v1, v2
	v_cvt_f32_i32_sdwa v1, sext(v50) dst_sel:DWORD dst_unused:UNUSED_PAD src0_sel:BYTE_3
	v_fmac_f32_e32 v0, v4, v10
	v_cvt_f32_i32_sdwa v2, sext(v51) dst_sel:DWORD dst_unused:UNUSED_PAD src0_sel:BYTE_3
	v_fmac_f32_e32 v0, v5, v14
	v_cvt_f32_i32_sdwa v4, sext(v52) dst_sel:DWORD dst_unused:UNUSED_PAD src0_sel:BYTE_3
	v_fmac_f32_e32 v0, v8, v6
	v_cvt_f32_i32_sdwa v5, sext(v53) dst_sel:DWORD dst_unused:UNUSED_PAD src0_sel:BYTE_3
	v_fmac_f32_e32 v0, v1, v3
	v_fmac_f32_e32 v0, v2, v11
	v_fmac_f32_e32 v0, v4, v15
	v_fmac_f32_e32 v0, v5, v7
	v_add_u32_dpp v1, v41, v41 quad_perm:[1,0,3,2] row_mask:0xf bank_mask:0xf bound_ctrl:1
	s_nop 0
	v_add_f32_dpp v0, v0, v0 quad_perm:[1,0,3,2] row_mask:0xf bank_mask:0xf bound_ctrl:1
	v_add_u32_dpp v1, v1, v1 quad_perm:[2,3,0,1] row_mask:0xf bank_mask:0xf bound_ctrl:1
	s_nop 0
	v_add_f32_dpp v0, v0, v0 quad_perm:[2,3,0,1] row_mask:0xf bank_mask:0xf bound_ctrl:1
	v_add_u32_dpp v1, v1, v1 row_half_mirror row_mask:0xf bank_mask:0xf bound_ctrl:1
	v_cndmask_b32_e64 v1, v16, v1, s[12:13]
	v_add_f32_dpp v0, v0, v0 row_half_mirror row_mask:0xf bank_mask:0xf bound_ctrl:1
	v_cndmask_b32_e64 v0, v17, v0, s[12:13]
	global_atomic_add v[28:29], v1, off offset:768
	global_atomic_add_f32 v[30:31], v0, off offset:768
	s_endpgm
